# adds: MoE gate/up epilogue rows rewritten branch-free with preloaded routing weights, MoE gather index loads issued together, QKV rotary quads prefetched 2 rows ahead, MoE down epilogue index loads in
# speedup vs baseline: 1.0285x; 1.0014x over previous
.LBB0_252:
	ds_read_b128 v[40:43], v161
	ds_read_b128 v[44:47], v161 offset:1024
	ds_read_b128 v[56:59], v161 offset:2048
	ds_read_b128 v[60:63], v161 offset:3072
	ds_read_b128 v[148:151], v162
	ds_read_b128 v[152:155], v162 offset:1024
	ds_read_b128 v[164:167], v162 offset:2048
	ds_read_b128 v[168:171], v162 offset:3072
	s_add_u32 s25, s30, 0xfffa0080
	s_addc_u32 s34, s31, -1
	s_cmp_eq_u32 s23, 12
	s_cselect_b32 s35, s27, s34
	s_cselect_b32 s34, s26, s25
	s_cselect_b32 s40, s28, s5
	s_cselect_b32 s41, s29, s18
	s_add_u32 s38, s34, 0x80
	s_addc_u32 s39, s35, 0
	s_add_u32 s78, s30, 0xfffe0000
	v_mov_b32_e32 v146, v159
	s_addc_u32 s79, s31, -1
	ds_read_b128 v[172:175], v163
	ds_read_b128 v[176:179], v163 offset:1024
	ds_read_b128 v[180:183], v163 offset:2048
	ds_read_b128 v[184:187], v163 offset:3072
	ds_read_b128 v[188:191], v163 offset:4096
	ds_read_b128 v[192:195], v163 offset:5120
	ds_read_b128 v[196:199], v163 offset:6144
	ds_read_b128 v[200:203], v163 offset:7168
	s_add_i32 m0, s52, 0xc000
	s_nop 0
	global_load_lds_dwordx4 v146, s[78:79]
	v_mov_b32_e32 v146, v159
	s_mov_b64 s[78:79], s[30:31]
	s_add_i32 m0, s52, 0xe000
	s_nop 0
	global_load_lds_dwordx4 v146, s[78:79]
	s_waitcnt vmcnt(8)
	s_waitcnt lgkmcnt(0)
	s_barrier
	s_setprio 3
	v_mfma_f32_16x16x32_bf16 v[140:143], v[40:43], v[172:175], v[140:143]
	v_mfma_f32_16x16x32_bf16 v[132:135], v[56:59], v[172:175], v[132:135]
	v_mfma_f32_16x16x32_bf16 v[124:127], v[40:43], v[180:183], v[124:127]
	v_mfma_f32_16x16x32_bf16 v[116:119], v[56:59], v[180:183], v[116:119]
	v_mfma_f32_16x16x32_bf16 v[108:111], v[40:43], v[188:191], v[108:111]
	v_mfma_f32_16x16x32_bf16 v[100:103], v[56:59], v[188:191], v[100:103]
	v_mfma_f32_16x16x32_bf16 v[92:95], v[40:43], v[196:199], v[92:95]
	v_mfma_f32_16x16x32_bf16 v[84:87], v[56:59], v[196:199], v[84:87]
	v_mfma_f32_16x16x32_bf16 v[140:143], v[44:47], v[176:179], v[140:143]
	v_mfma_f32_16x16x32_bf16 v[132:135], v[60:63], v[176:179], v[132:135]
	v_mfma_f32_16x16x32_bf16 v[124:127], v[44:47], v[184:187], v[124:127]
	v_mfma_f32_16x16x32_bf16 v[116:119], v[60:63], v[184:187], v[116:119]
	v_mfma_f32_16x16x32_bf16 v[108:111], v[44:47], v[192:195], v[108:111]
	v_mfma_f32_16x16x32_bf16 v[100:103], v[60:63], v[192:195], v[100:103]
	v_mfma_f32_16x16x32_bf16 v[92:95], v[44:47], v[200:203], v[92:95]
	v_mfma_f32_16x16x32_bf16 v[84:87], v[60:63], v[200:203], v[84:87]
	v_mfma_f32_16x16x32_bf16 v[136:139], v[148:151], v[172:175], v[136:139]
	v_mfma_f32_16x16x32_bf16 v[128:131], v[164:167], v[172:175], v[128:131]
	v_mfma_f32_16x16x32_bf16 v[120:123], v[148:151], v[180:183], v[120:123]
	v_mfma_f32_16x16x32_bf16 v[112:115], v[164:167], v[180:183], v[112:115]
	v_mfma_f32_16x16x32_bf16 v[104:107], v[148:151], v[188:191], v[104:107]
	v_mfma_f32_16x16x32_bf16 v[96:99], v[164:167], v[188:191], v[96:99]
	v_mfma_f32_16x16x32_bf16 v[88:91], v[148:151], v[196:199], v[88:91]
	v_mfma_f32_16x16x32_bf16 v[80:83], v[164:167], v[196:199], v[80:83]
	v_mfma_f32_16x16x32_bf16 v[136:139], v[152:155], v[176:179], v[136:139]
	v_mfma_f32_16x16x32_bf16 v[128:131], v[168:171], v[176:179], v[128:131]
	v_mfma_f32_16x16x32_bf16 v[120:123], v[152:155], v[184:187], v[120:123]
	v_mfma_f32_16x16x32_bf16 v[112:115], v[168:171], v[184:187], v[112:115]
	v_mfma_f32_16x16x32_bf16 v[104:107], v[152:155], v[192:195], v[104:107]
	v_mfma_f32_16x16x32_bf16 v[96:99], v[168:171], v[192:195], v[96:99]
	v_mfma_f32_16x16x32_bf16 v[88:91], v[152:155], v[200:203], v[88:91]
	v_mfma_f32_16x16x32_bf16 v[80:83], v[168:171], v[200:203], v[80:83]
	s_setprio 0
	s_barrier
	v_mov_b32_e32 v146, v158
	s_mov_b64 s[78:79], s[40:41]
	s_add_i32 s25, s72, s51
	ds_read_b128 v[172:175], v163 offset:16384
	ds_read_b128 v[176:179], v163 offset:17408
	ds_read_b128 v[180:183], v163 offset:18432
	ds_read_b128 v[184:187], v163 offset:19456
	ds_read_b128 v[188:191], v163 offset:20480
	ds_read_b128 v[192:195], v163 offset:21504
	ds_read_b128 v[196:199], v163 offset:22528
	ds_read_b128 v[200:203], v163 offset:23552
	s_mov_b32 m0, s25
	s_nop 0
	global_load_lds_dwordx4 v146, s[78:79]
	s_add_u32 s78, s40, 0x20000
	v_mov_b32_e32 v146, v158
	s_addc_u32 s79, s41, 0
	s_add_i32 m0, s25, 0x2000
	s_nop 0
	global_load_lds_dwordx4 v146, s[78:79]
	s_add_u32 s78, s40, 0x40000
	v_mov_b32_e32 v146, v158
	s_addc_u32 s79, s41, 0
	s_add_i32 s25, s73, s51
	s_mov_b32 m0, s25
	s_nop 0
	global_load_lds_dwordx4 v146, s[78:79]
	s_add_u32 s78, s40, 0x60000
	v_mov_b32_e32 v146, v158
	s_addc_u32 s79, s41, 0
	s_add_i32 m0, s25, 0x2000
	s_nop 0
	global_load_lds_dwordx4 v146, s[78:79]
	v_mov_b32_e32 v146, v159
	s_mov_b64 s[78:79], s[34:35]
	s_mov_b32 m0, s52
	s_nop 0
	global_load_lds_dwordx4 v146, s[78:79]
	s_add_u32 s78, s34, 0x20000
	v_mov_b32_e32 v146, v159
	s_addc_u32 s79, s35, 0
	s_mov_b32 m0, s53
	s_nop 0
	global_load_lds_dwordx4 v146, s[78:79]
	s_waitcnt vmcnt(8)
	s_waitcnt lgkmcnt(0)
	s_barrier
	s_setprio 3
	v_mfma_f32_16x16x32_bf16 v[76:79], v[40:43], v[172:175], v[76:79]
	v_mfma_f32_16x16x32_bf16 v[68:71], v[56:59], v[172:175], v[68:71]
	v_mfma_f32_16x16x32_bf16 v[52:55], v[40:43], v[180:183], v[52:55]
	v_mfma_f32_16x16x32_bf16 v[36:39], v[56:59], v[180:183], v[36:39]
	v_mfma_f32_16x16x32_bf16 v[28:31], v[40:43], v[188:191], v[28:31]
	v_mfma_f32_16x16x32_bf16 v[20:23], v[56:59], v[188:191], v[20:23]
	v_mfma_f32_16x16x32_bf16 v[12:15], v[40:43], v[196:199], v[12:15]
	v_mfma_f32_16x16x32_bf16 v[4:7], v[56:59], v[196:199], v[4:7]
	v_mfma_f32_16x16x32_bf16 v[76:79], v[44:47], v[176:179], v[76:79]
	v_mfma_f32_16x16x32_bf16 v[68:71], v[60:63], v[176:179], v[68:71]
	v_mfma_f32_16x16x32_bf16 v[52:55], v[44:47], v[184:187], v[52:55]
	v_mfma_f32_16x16x32_bf16 v[36:39], v[60:63], v[184:187], v[36:39]
	v_mfma_f32_16x16x32_bf16 v[28:31], v[44:47], v[192:195], v[28:31]
	v_mfma_f32_16x16x32_bf16 v[20:23], v[60:63], v[192:195], v[20:23]
	v_mfma_f32_16x16x32_bf16 v[12:15], v[44:47], v[200:203], v[12:15]
	v_mfma_f32_16x16x32_bf16 v[4:7], v[60:63], v[200:203], v[4:7]
	v_mfma_f32_16x16x32_bf16 v[48:51], v[148:151], v[180:183], v[48:51]
	v_mfma_f32_16x16x32_bf16 v[32:35], v[164:167], v[180:183], v[32:35]
	v_mfma_f32_16x16x32_bf16 v[24:27], v[148:151], v[188:191], v[24:27]
	v_mfma_f32_16x16x32_bf16 v[16:19], v[164:167], v[188:191], v[16:19]
	v_mfma_f32_16x16x32_bf16 v[8:11], v[148:151], v[196:199], v[8:11]
	v_mfma_f32_16x16x32_bf16 v[0:3], v[164:167], v[196:199], v[0:3]
	v_mfma_f32_16x16x32_bf16 v[40:43], v[148:151], v[172:175], v[72:75]
	v_mfma_f32_16x16x32_bf16 v[44:47], v[164:167], v[172:175], v[64:67]
	v_mfma_f32_16x16x32_bf16 v[48:51], v[152:155], v[184:187], v[48:51]
	v_mfma_f32_16x16x32_bf16 v[32:35], v[168:171], v[184:187], v[32:35]
	v_mfma_f32_16x16x32_bf16 v[24:27], v[152:155], v[192:195], v[24:27]
	v_mfma_f32_16x16x32_bf16 v[16:19], v[168:171], v[192:195], v[16:19]
	v_mfma_f32_16x16x32_bf16 v[8:11], v[152:155], v[200:203], v[8:11]
	v_mfma_f32_16x16x32_bf16 v[0:3], v[168:171], v[200:203], v[0:3]
	v_mfma_f32_16x16x32_bf16 v[40:43], v[152:155], v[176:179], v[40:43]
	v_mfma_f32_16x16x32_bf16 v[44:47], v[168:171], v[176:179], v[44:47]
	s_setprio 0
	s_barrier
	s_add_i32 s25, 0, 0x18000
	s_add_i32 s37, 0, 0x1c000
	v_add_u32_e32 v72, s25, v160
	v_add_u32_e32 v146, s37, v160
	ds_read_b128 v[56:59], v72
	ds_read_b128 v[60:63], v72 offset:1024
	ds_read_b128 v[64:67], v72 offset:2048
	ds_read_b128 v[72:75], v72 offset:3072
	ds_read_b128 v[148:151], v146
	ds_read_b128 v[152:155], v146 offset:1024
	ds_read_b128 v[164:167], v146 offset:2048
	ds_read_b128 v[168:171], v146 offset:3072
	s_add_u32 s78, s34, 0x40000
	v_mov_b32_e32 v146, v159
	s_addc_u32 s79, s35, 0
	s_mov_b32 m0, s60
	ds_read_b128 v[172:175], v163 offset:32768
	ds_read_b128 v[176:179], v163 offset:33792
	ds_read_b128 v[180:183], v163 offset:34816
	ds_read_b128 v[184:187], v163 offset:35840
	ds_read_b128 v[188:191], v163 offset:36864
	ds_read_b128 v[192:195], v163 offset:37888
	ds_read_b128 v[196:199], v163 offset:38912
	ds_read_b128 v[200:203], v163 offset:39936
	s_nop 0
	global_load_lds_dwordx4 v146, s[78:79]
	s_add_u32 s78, s34, 0x60000
	v_mov_b32_e32 v146, v159
	s_addc_u32 s79, s35, 0
	s_mov_b32 m0, s61
	s_nop 0
	global_load_lds_dwordx4 v146, s[78:79]
	s_waitcnt vmcnt(8)
	s_waitcnt lgkmcnt(0)
	s_barrier
	s_setprio 3
	v_mfma_f32_16x16x32_bf16 v[140:143], v[56:59], v[172:175], v[140:143]
	v_mfma_f32_16x16x32_bf16 v[132:135], v[64:67], v[172:175], v[132:135]
	v_mfma_f32_16x16x32_bf16 v[124:127], v[56:59], v[180:183], v[124:127]
	v_mfma_f32_16x16x32_bf16 v[116:119], v[64:67], v[180:183], v[116:119]
	v_mfma_f32_16x16x32_bf16 v[108:111], v[56:59], v[188:191], v[108:111]
	v_mfma_f32_16x16x32_bf16 v[100:103], v[64:67], v[188:191], v[100:103]
	v_mfma_f32_16x16x32_bf16 v[92:95], v[56:59], v[196:199], v[92:95]
	v_mfma_f32_16x16x32_bf16 v[84:87], v[64:67], v[196:199], v[84:87]
	v_mfma_f32_16x16x32_bf16 v[140:143], v[60:63], v[176:179], v[140:143]
	v_mfma_f32_16x16x32_bf16 v[132:135], v[72:75], v[176:179], v[132:135]
	v_mfma_f32_16x16x32_bf16 v[124:127], v[60:63], v[184:187], v[124:127]
	v_mfma_f32_16x16x32_bf16 v[116:119], v[72:75], v[184:187], v[116:119]
	v_mfma_f32_16x16x32_bf16 v[108:111], v[60:63], v[192:195], v[108:111]
	v_mfma_f32_16x16x32_bf16 v[100:103], v[72:75], v[192:195], v[100:103]
	v_mfma_f32_16x16x32_bf16 v[92:95], v[60:63], v[200:203], v[92:95]
	v_mfma_f32_16x16x32_bf16 v[84:87], v[72:75], v[200:203], v[84:87]
	v_mfma_f32_16x16x32_bf16 v[136:139], v[148:151], v[172:175], v[136:139]
	v_mfma_f32_16x16x32_bf16 v[128:131], v[164:167], v[172:175], v[128:131]
	v_mfma_f32_16x16x32_bf16 v[120:123], v[148:151], v[180:183], v[120:123]
	v_mfma_f32_16x16x32_bf16 v[112:115], v[164:167], v[180:183], v[112:115]
	v_mfma_f32_16x16x32_bf16 v[104:107], v[148:151], v[188:191], v[104:107]
	v_mfma_f32_16x16x32_bf16 v[96:99], v[164:167], v[188:191], v[96:99]
	v_mfma_f32_16x16x32_bf16 v[88:91], v[148:151], v[196:199], v[88:91]
	v_mfma_f32_16x16x32_bf16 v[80:83], v[164:167], v[196:199], v[80:83]
	v_mfma_f32_16x16x32_bf16 v[136:139], v[152:155], v[176:179], v[136:139]
	v_mfma_f32_16x16x32_bf16 v[128:131], v[168:171], v[176:179], v[128:131]
	v_mfma_f32_16x16x32_bf16 v[120:123], v[152:155], v[184:187], v[120:123]
	v_mfma_f32_16x16x32_bf16 v[112:115], v[168:171], v[184:187], v[112:115]
	v_mfma_f32_16x16x32_bf16 v[104:107], v[152:155], v[192:195], v[104:107]
	v_mfma_f32_16x16x32_bf16 v[96:99], v[168:171], v[192:195], v[96:99]
	v_mfma_f32_16x16x32_bf16 v[88:91], v[152:155], v[200:203], v[88:91]
	v_mfma_f32_16x16x32_bf16 v[80:83], v[168:171], v[200:203], v[80:83]
	s_setprio 0
	s_barrier
	s_add_u32 s78, s40, 0x80
	s_addc_u32 s79, s41, 0
	v_mov_b32_e32 v146, v158
	s_add_i32 s25, s25, s51
	ds_read_b128 v[172:175], v163 offset:49152
	ds_read_b128 v[176:179], v163 offset:50176
	ds_read_b128 v[180:183], v163 offset:51200
	ds_read_b128 v[184:187], v163 offset:52224
	ds_read_b128 v[188:191], v163 offset:53248
	ds_read_b128 v[192:195], v163 offset:54272
	ds_read_b128 v[196:199], v163 offset:55296
	ds_read_b128 v[200:203], v163 offset:56320
	s_mov_b32 m0, s25
	s_nop 0
	global_load_lds_dwordx4 v146, s[78:79]
	s_add_u32 s78, s40, 0x20080
	v_mov_b32_e32 v146, v158
	s_addc_u32 s79, s41, 0
	s_add_i32 m0, s25, 0x2000
	s_nop 0
	global_load_lds_dwordx4 v146, s[78:79]
	s_add_u32 s78, s40, 0x40080
	v_mov_b32_e32 v146, v158
	s_addc_u32 s79, s41, 0
	s_add_i32 s25, s37, s51
	s_mov_b32 m0, s25
	s_add_u32 s40, s40, 0x60080
	global_load_lds_dwordx4 v146, s[78:79]
	v_mov_b32_e32 v146, v158
	s_addc_u32 s41, s41, 0
	s_add_i32 m0, s25, 0x2000
	s_add_u32 s34, s34, 0x20080
	global_load_lds_dwordx4 v146, s[40:41]
	v_mov_b32_e32 v146, v159
	s_mov_b32 m0, s69
	s_addc_u32 s35, s35, 0
	global_load_lds_dwordx4 v146, s[38:39]
	v_mov_b32_e32 v146, v159
	s_mov_b32 m0, s70
	s_nop 0
	global_load_lds_dwordx4 v146, s[34:35]
	s_waitcnt vmcnt(8)
	s_waitcnt lgkmcnt(0)
	s_barrier
	s_setprio 3
	v_mfma_f32_16x16x32_bf16 v[76:79], v[56:59], v[172:175], v[76:79]
	v_mfma_f32_16x16x32_bf16 v[68:71], v[64:67], v[172:175], v[68:71]
	v_mfma_f32_16x16x32_bf16 v[52:55], v[56:59], v[180:183], v[52:55]
	v_mfma_f32_16x16x32_bf16 v[36:39], v[64:67], v[180:183], v[36:39]
	v_mfma_f32_16x16x32_bf16 v[28:31], v[56:59], v[188:191], v[28:31]
	v_mfma_f32_16x16x32_bf16 v[20:23], v[64:67], v[188:191], v[20:23]
	v_mfma_f32_16x16x32_bf16 v[12:15], v[56:59], v[196:199], v[12:15]
	v_mfma_f32_16x16x32_bf16 v[4:7], v[64:67], v[196:199], v[4:7]
	v_mfma_f32_16x16x32_bf16 v[76:79], v[60:63], v[176:179], v[76:79]
	v_mfma_f32_16x16x32_bf16 v[68:71], v[72:75], v[176:179], v[68:71]
	v_mfma_f32_16x16x32_bf16 v[52:55], v[60:63], v[184:187], v[52:55]
	v_mfma_f32_16x16x32_bf16 v[36:39], v[72:75], v[184:187], v[36:39]
	v_mfma_f32_16x16x32_bf16 v[28:31], v[60:63], v[192:195], v[28:31]
	v_mfma_f32_16x16x32_bf16 v[20:23], v[72:75], v[192:195], v[20:23]
	v_mfma_f32_16x16x32_bf16 v[12:15], v[60:63], v[200:203], v[12:15]
	v_mfma_f32_16x16x32_bf16 v[4:7], v[72:75], v[200:203], v[4:7]
	v_mfma_f32_16x16x32_bf16 v[40:43], v[148:151], v[172:175], v[40:43]
	v_mfma_f32_16x16x32_bf16 v[72:75], v[152:155], v[176:179], v[40:43]
	v_mfma_f32_16x16x32_bf16 v[40:43], v[164:167], v[172:175], v[44:47]
	v_mfma_f32_16x16x32_bf16 v[64:67], v[168:171], v[176:179], v[40:43]
	v_mfma_f32_16x16x32_bf16 v[40:43], v[148:151], v[180:183], v[48:51]
	v_mfma_f32_16x16x32_bf16 v[32:35], v[164:167], v[180:183], v[32:35]
	v_mfma_f32_16x16x32_bf16 v[24:27], v[148:151], v[188:191], v[24:27]
	v_mfma_f32_16x16x32_bf16 v[16:19], v[164:167], v[188:191], v[16:19]
	v_mfma_f32_16x16x32_bf16 v[8:11], v[148:151], v[196:199], v[8:11]
	v_mfma_f32_16x16x32_bf16 v[0:3], v[164:167], v[196:199], v[0:3]
	v_mfma_f32_16x16x32_bf16 v[48:51], v[152:155], v[184:187], v[40:43]
	v_mfma_f32_16x16x32_bf16 v[32:35], v[168:171], v[184:187], v[32:35]
	v_mfma_f32_16x16x32_bf16 v[24:27], v[152:155], v[192:195], v[24:27]
	v_mfma_f32_16x16x32_bf16 v[16:19], v[168:171], v[192:195], v[16:19]
	v_mfma_f32_16x16x32_bf16 v[8:11], v[152:155], v[200:203], v[8:11]
	v_mfma_f32_16x16x32_bf16 v[0:3], v[168:171], v[200:203], v[0:3]
	s_setprio 0
	s_barrier
	s_add_i32 s23, s23, 2
	s_add_u32 s5, s5, 0x100
	s_addc_u32 s18, s18, 0
	s_add_u32 s30, s30, 0x100
	s_addc_u32 s31, s31, 0
	s_cmp_gt_u32 s23, 13
	s_cbranch_scc0 .LBB0_252
	s_and_b64 vcc, exec, s[20:21]
	s_cbranch_vccz .LBB0_255
	s_barrier

.LBB0_262:
	v_and_or_b32 v164, v154, 15, s68
	s_lshl_b32 s18, s4, 8
	v_add_u32_e32 v136, s18, v164
	v_ashrrev_i32_e32 v137, 31, v136
	v_lshlrev_b64 v[156:157], 7, v[136:137]
	v_add_u32_e32 v236, v156, v146
	global_load_dwordx4 v[204:207], v236, s[8:9]
	global_load_dwordx4 v[208:211], v236, s[10:11]
	global_load_dwordx4 v[212:215], v236, s[8:9] offset:16
	global_load_dwordx4 v[216:219], v236, s[10:11] offset:16
	v_add_u32_e32 v237, 0x800, v236
	global_load_dwordx4 v[220:223], v237, s[8:9]
	global_load_dwordx4 v[224:227], v237, s[10:11]
	global_load_dwordx4 v[228:231], v237, s[8:9] offset:16
	global_load_dwordx4 v[232:235], v237, s[10:11] offset:16
	v_lshl_add_u64 v[154:155], s[8:9], 0, v[156:157]
	v_lshl_add_u64 v[156:157], s[10:11], 0, v[156:157]
	s_mov_b32 s35, s34
	v_lshl_add_u64 v[154:155], v[154:155], 0, v[146:147]
	s_andn2_b64 vcc, exec, s[40:41]
	v_lshl_add_u64 v[156:157], v[156:157], 0, v[146:147]
	s_cbranch_vccnz .LBB0_264
	s_mov_b32 s4, s34
	s_mov_b32 s5, s34
	s_waitcnt vmcnt(4)
	v_mov_b32_e32 v166, v204
	v_mov_b32_e32 v167, v205
	v_mov_b32_e32 v168, v206
	v_mov_b32_e32 v169, v207
	v_mov_b32_e32 v170, v208
	v_mov_b32_e32 v171, v209
	v_mov_b32_e32 v172, v210
	v_mov_b32_e32 v173, v211
	v_pk_mul_f32 v[142:143], v[138:139], v[172:173]
	v_pk_mul_f32 v[148:149], v[140:141], v[170:171]
	v_pk_fma_f32 v[142:143], v[150:151], v[168:169], v[142:143] neg_lo:[0,0,1] neg_hi:[0,0,1]
	v_pk_fma_f32 v[148:149], v[152:153], v[166:167], v[148:149] neg_lo:[0,0,1] neg_hi:[0,0,1]
	v_pk_mul_f32 v[150:151], v[150:151], v[172:173]
	v_pk_mul_f32 v[152:153], v[152:153], v[170:171]
	v_pk_fma_f32 v[138:139], v[138:139], v[168:169], v[150:151]
	v_pk_fma_f32 v[140:141], v[140:141], v[166:167], v[152:153]
	v_pk_mul_f32 v[142:143], s[4:5], v[142:143]
	v_pk_mul_f32 v[148:149], s[34:35], v[148:149]
	v_pk_mul_f32 v[138:139], s[4:5], v[138:139]
	v_pk_mul_f32 v[140:141], s[34:35], v[140:141]

.LBB0_266:
	s_andn2_b64 vcc, exec, s[36:37]
	s_cbranch_vccnz .LBB0_268
	s_mov_b32 s36, s34
	s_mov_b32 s37, s34
	v_mov_b32_e32 v152, v212
	v_mov_b32_e32 v153, v213
	v_mov_b32_e32 v154, v214
	v_mov_b32_e32 v155, v215
	v_mov_b32_e32 v166, v216
	v_mov_b32_e32 v167, v217
	v_mov_b32_e32 v168, v218
	v_mov_b32_e32 v169, v219
	v_add_u32_e32 v237, 0x1000, v236
	global_load_dwordx4 v[204:207], v237, s[8:9]
	global_load_dwordx4 v[208:211], v237, s[10:11]
	global_load_dwordx4 v[212:215], v237, s[8:9] offset:16
	global_load_dwordx4 v[216:219], v237, s[10:11] offset:16
	v_pk_mul_f32 v[128:129], v[130:131], v[168:169]
	v_pk_mul_f32 v[156:157], v[132:133], v[166:167]
	v_pk_fma_f32 v[128:129], v[134:135], v[154:155], v[128:129] neg_lo:[0,0,1] neg_hi:[0,0,1]
	v_pk_fma_f32 v[156:157], v[150:151], v[152:153], v[156:157] neg_lo:[0,0,1] neg_hi:[0,0,1]
	v_pk_mul_f32 v[134:135], v[134:135], v[168:169]
	v_pk_mul_f32 v[150:151], v[150:151], v[166:167]
	v_pk_mul_f32 v[128:129], s[36:37], v[128:129]
	v_pk_mul_f32 v[156:157], s[34:35], v[156:157]
	v_pk_fma_f32 v[130:131], v[130:131], v[154:155], v[134:135]
	v_pk_fma_f32 v[132:133], v[132:133], v[152:153], v[150:151]
	v_pk_mul_f32 v[130:131], s[36:37], v[130:131]
	v_pk_mul_f32 v[132:133], s[34:35], v[132:133]
	v_mov_b32_e32 v150, v156
	v_mov_b32_e32 v151, v157
	v_mov_b32_e32 v134, v128
	v_mov_b32_e32 v135, v129

.LBB0_270:
	v_add3_u32 v130, v164, s18, 16
	v_ashrrev_i32_e32 v131, 31, v130
	v_lshlrev_b64 v[134:135], 7, v[130:131]
	v_lshl_add_u64 v[132:133], s[8:9], 0, v[134:135]
	v_lshl_add_u64 v[134:135], s[10:11], 0, v[134:135]
	v_lshl_add_u64 v[132:133], v[132:133], 0, v[146:147]
	s_andn2_b64 vcc, exec, s[36:37]
	v_lshl_add_u64 v[134:135], v[134:135], 0, v[146:147]
	s_cbranch_vccnz .LBB0_272
	s_mov_b32 s36, s34
	s_mov_b32 s37, s34
	s_waitcnt vmcnt(6)
	v_mov_b32_e32 v138, v220
	v_mov_b32_e32 v139, v221
	v_mov_b32_e32 v140, v222
	v_mov_b32_e32 v141, v223
	v_mov_b32_e32 v148, v224
	v_mov_b32_e32 v149, v225
	v_mov_b32_e32 v150, v226
	v_mov_b32_e32 v151, v227
	v_pk_mul_f32 v[142:143], v[122:123], v[150:151]
	v_pk_mul_f32 v[152:153], v[120:121], v[148:149]
	v_pk_fma_f32 v[142:143], v[126:127], v[140:141], v[142:143] neg_lo:[0,0,1] neg_hi:[0,0,1]
	v_pk_fma_f32 v[152:153], v[124:125], v[138:139], v[152:153] neg_lo:[0,0,1] neg_hi:[0,0,1]
	v_pk_mul_f32 v[126:127], v[126:127], v[150:151]
	v_pk_mul_f32 v[124:125], v[124:125], v[148:149]
	v_pk_mul_f32 v[142:143], s[36:37], v[142:143]
	v_pk_mul_f32 v[152:153], s[34:35], v[152:153]
	v_pk_fma_f32 v[122:123], v[122:123], v[140:141], v[126:127]
	v_pk_fma_f32 v[120:121], v[120:121], v[138:139], v[124:125]
	v_pk_mul_f32 v[122:123], s[36:37], v[122:123]
	v_pk_mul_f32 v[120:121], s[34:35], v[120:121]
	v_mov_b32_e32 v124, v152
	v_mov_b32_e32 v125, v153
	v_mov_b32_e32 v126, v142
	v_mov_b32_e32 v127, v143

.LBB0_274:
	s_andn2_b64 vcc, exec, s[36:37]
	s_cbranch_vccnz .LBB0_276
	s_mov_b32 s36, s34
	s_mov_b32 s37, s34
	v_mov_b32_e32 v138, v228
	v_mov_b32_e32 v139, v229
	v_mov_b32_e32 v140, v230
	v_mov_b32_e32 v141, v231
	v_mov_b32_e32 v132, v232
	v_mov_b32_e32 v133, v233
	v_mov_b32_e32 v134, v234
	v_mov_b32_e32 v135, v235
	v_add_u32_e32 v237, 0x1800, v236
	global_load_dwordx4 v[220:223], v237, s[8:9]
	global_load_dwordx4 v[224:227], v237, s[10:11]
	global_load_dwordx4 v[228:231], v237, s[8:9] offset:16
	global_load_dwordx4 v[232:235], v237, s[10:11] offset:16
	v_pk_mul_f32 v[142:143], v[114:115], v[134:135]
	v_pk_mul_f32 v[148:149], v[112:113], v[132:133]
	v_pk_fma_f32 v[142:143], v[118:119], v[140:141], v[142:143] neg_lo:[0,0,1] neg_hi:[0,0,1]
	v_pk_fma_f32 v[148:149], v[116:117], v[138:139], v[148:149] neg_lo:[0,0,1] neg_hi:[0,0,1]
	v_pk_mul_f32 v[118:119], v[118:119], v[134:135]
	v_pk_mul_f32 v[116:117], v[116:117], v[132:133]
	v_pk_mul_f32 v[142:143], s[36:37], v[142:143]
	v_pk_mul_f32 v[148:149], s[34:35], v[148:149]
	v_pk_fma_f32 v[114:115], v[114:115], v[140:141], v[118:119]
	v_pk_fma_f32 v[112:113], v[112:113], v[138:139], v[116:117]
	v_pk_mul_f32 v[114:115], s[36:37], v[114:115]
	v_pk_mul_f32 v[112:113], s[34:35], v[112:113]
	v_mov_b32_e32 v116, v148
	v_mov_b32_e32 v117, v149
	v_mov_b32_e32 v118, v142
	v_mov_b32_e32 v119, v143

.LBB0_278:
	v_add3_u32 v112, v164, s18, 32
	v_ashrrev_i32_e32 v113, 31, v112
	v_lshlrev_b64 v[116:117], 7, v[112:113]
	v_lshl_add_u64 v[114:115], s[8:9], 0, v[116:117]
	v_lshl_add_u64 v[116:117], s[10:11], 0, v[116:117]
	v_lshl_add_u64 v[114:115], v[114:115], 0, v[146:147]
	s_andn2_b64 vcc, exec, s[36:37]
	v_lshl_add_u64 v[116:117], v[116:117], 0, v[146:147]
	s_cbranch_vccnz .LBB0_280
	s_mov_b32 s36, s34
	s_mov_b32 s37, s34
	s_waitcnt vmcnt(8)
	v_mov_b32_e32 v118, v204
	v_mov_b32_e32 v119, v205
	v_mov_b32_e32 v120, v206
	v_mov_b32_e32 v121, v207
	v_mov_b32_e32 v122, v208
	v_mov_b32_e32 v123, v209
	v_mov_b32_e32 v124, v210
	v_mov_b32_e32 v125, v211
	v_pk_mul_f32 v[126:127], v[106:107], v[124:125]
	v_pk_mul_f32 v[130:131], v[104:105], v[122:123]
	v_pk_fma_f32 v[126:127], v[110:111], v[120:121], v[126:127] neg_lo:[0,0,1] neg_hi:[0,0,1]
	v_pk_fma_f32 v[130:131], v[108:109], v[118:119], v[130:131] neg_lo:[0,0,1] neg_hi:[0,0,1]
	v_pk_mul_f32 v[110:111], v[110:111], v[124:125]
	v_pk_mul_f32 v[108:109], v[108:109], v[122:123]
	v_pk_mul_f32 v[126:127], s[36:37], v[126:127]
	v_pk_mul_f32 v[130:131], s[34:35], v[130:131]
	v_pk_fma_f32 v[106:107], v[106:107], v[120:121], v[110:111]
	v_pk_fma_f32 v[104:105], v[104:105], v[118:119], v[108:109]
	v_pk_mul_f32 v[106:107], s[36:37], v[106:107]
	v_pk_mul_f32 v[104:105], s[34:35], v[104:105]
	v_mov_b32_e32 v108, v130
	v_mov_b32_e32 v109, v131
	v_mov_b32_e32 v110, v126
	v_mov_b32_e32 v111, v127

.LBB0_282:
	s_andn2_b64 vcc, exec, s[36:37]
	s_cbranch_vccnz .LBB0_284
	s_mov_b32 s36, s34
	s_mov_b32 s37, s34
	v_mov_b32_e32 v118, v212
	v_mov_b32_e32 v119, v213
	v_mov_b32_e32 v120, v214
	v_mov_b32_e32 v121, v215
	v_mov_b32_e32 v114, v216
	v_mov_b32_e32 v115, v217
	v_mov_b32_e32 v116, v218
	v_mov_b32_e32 v117, v219
	v_add_u32_e32 v237, 0x4000, v236
	global_load_dwordx4 v[204:207], v237, s[8:9]
	global_load_dwordx4 v[208:211], v237, s[10:11]
	global_load_dwordx4 v[212:215], v237, s[8:9] offset:16
	global_load_dwordx4 v[216:219], v237, s[10:11] offset:16
	v_pk_mul_f32 v[122:123], v[98:99], v[116:117]
	v_pk_mul_f32 v[124:125], v[96:97], v[114:115]
	v_pk_fma_f32 v[122:123], v[102:103], v[120:121], v[122:123] neg_lo:[0,0,1] neg_hi:[0,0,1]
	v_pk_fma_f32 v[124:125], v[100:101], v[118:119], v[124:125] neg_lo:[0,0,1] neg_hi:[0,0,1]
	v_pk_mul_f32 v[102:103], v[102:103], v[116:117]
	v_pk_mul_f32 v[100:101], v[100:101], v[114:115]
	v_pk_mul_f32 v[122:123], s[36:37], v[122:123]
	v_pk_mul_f32 v[124:125], s[34:35], v[124:125]
	v_pk_fma_f32 v[98:99], v[98:99], v[120:121], v[102:103]
	v_pk_fma_f32 v[96:97], v[96:97], v[118:119], v[100:101]
	v_pk_mul_f32 v[98:99], s[36:37], v[98:99]
	v_pk_mul_f32 v[96:97], s[34:35], v[96:97]
	v_mov_b32_e32 v100, v124
	v_mov_b32_e32 v101, v125
	v_mov_b32_e32 v102, v122
	v_mov_b32_e32 v103, v123

.LBB0_286:
	v_add3_u32 v96, v164, s18, 48
	v_ashrrev_i32_e32 v97, 31, v96
	v_lshlrev_b64 v[100:101], 7, v[96:97]
	v_lshl_add_u64 v[98:99], s[8:9], 0, v[100:101]
	v_lshl_add_u64 v[100:101], s[10:11], 0, v[100:101]
	v_lshl_add_u64 v[98:99], v[98:99], 0, v[146:147]
	s_andn2_b64 vcc, exec, s[36:37]
	v_lshl_add_u64 v[100:101], v[100:101], 0, v[146:147]
	s_cbranch_vccnz .LBB0_288
	s_mov_b32 s36, s34
	s_mov_b32 s37, s34
	s_waitcnt vmcnt(8)
	v_mov_b32_e32 v102, v220
	v_mov_b32_e32 v103, v221
	v_mov_b32_e32 v104, v222
	v_mov_b32_e32 v105, v223
	v_mov_b32_e32 v106, v224
	v_mov_b32_e32 v107, v225
	v_mov_b32_e32 v108, v226
	v_mov_b32_e32 v109, v227
	v_pk_mul_f32 v[110:111], v[90:91], v[108:109]
	v_pk_mul_f32 v[112:113], v[88:89], v[106:107]
	v_pk_fma_f32 v[110:111], v[94:95], v[104:105], v[110:111] neg_lo:[0,0,1] neg_hi:[0,0,1]
	v_pk_fma_f32 v[112:113], v[92:93], v[102:103], v[112:113] neg_lo:[0,0,1] neg_hi:[0,0,1]
	v_pk_mul_f32 v[94:95], v[94:95], v[108:109]
	v_pk_mul_f32 v[92:93], v[92:93], v[106:107]
	v_pk_mul_f32 v[110:111], s[36:37], v[110:111]
	v_pk_mul_f32 v[112:113], s[34:35], v[112:113]
	v_pk_fma_f32 v[90:91], v[90:91], v[104:105], v[94:95]
	v_pk_fma_f32 v[88:89], v[88:89], v[102:103], v[92:93]
	v_pk_mul_f32 v[90:91], s[36:37], v[90:91]
	v_pk_mul_f32 v[88:89], s[34:35], v[88:89]
	v_mov_b32_e32 v92, v112
	v_mov_b32_e32 v93, v113
	v_mov_b32_e32 v94, v110
	v_mov_b32_e32 v95, v111

.LBB0_290:
	s_andn2_b64 vcc, exec, s[36:37]
	s_cbranch_vccnz .LBB0_292
	s_mov_b32 s36, s34
	s_mov_b32 s37, s34
	v_mov_b32_e32 v102, v228
	v_mov_b32_e32 v103, v229
	v_mov_b32_e32 v104, v230
	v_mov_b32_e32 v105, v231
	v_mov_b32_e32 v98, v232
	v_mov_b32_e32 v99, v233
	v_mov_b32_e32 v100, v234
	v_mov_b32_e32 v101, v235
	v_add_u32_e32 v237, 0x4800, v236
	global_load_dwordx4 v[220:223], v237, s[8:9]
	global_load_dwordx4 v[224:227], v237, s[10:11]
	global_load_dwordx4 v[228:231], v237, s[8:9] offset:16
	global_load_dwordx4 v[232:235], v237, s[10:11] offset:16
	v_pk_mul_f32 v[106:107], v[82:83], v[100:101]
	v_pk_mul_f32 v[108:109], v[80:81], v[98:99]
	v_pk_fma_f32 v[106:107], v[86:87], v[104:105], v[106:107] neg_lo:[0,0,1] neg_hi:[0,0,1]
	v_pk_fma_f32 v[108:109], v[84:85], v[102:103], v[108:109] neg_lo:[0,0,1] neg_hi:[0,0,1]
	v_pk_mul_f32 v[86:87], v[86:87], v[100:101]
	v_pk_mul_f32 v[84:85], v[84:85], v[98:99]
	v_pk_mul_f32 v[106:107], s[36:37], v[106:107]
	v_pk_mul_f32 v[108:109], s[34:35], v[108:109]
	v_pk_fma_f32 v[82:83], v[82:83], v[104:105], v[86:87]
	v_pk_fma_f32 v[80:81], v[80:81], v[102:103], v[84:85]
	v_pk_mul_f32 v[82:83], s[36:37], v[82:83]
	v_pk_mul_f32 v[80:81], s[34:35], v[80:81]
	v_mov_b32_e32 v84, v108
	v_mov_b32_e32 v85, v109
	v_mov_b32_e32 v86, v106
	v_mov_b32_e32 v87, v107

.LBB0_294:
	v_add_u32_e32 v80, 0x80, v136
	v_ashrrev_i32_e32 v81, 31, v80
	v_lshlrev_b64 v[84:85], 7, v[80:81]
	v_lshl_add_u64 v[82:83], s[8:9], 0, v[84:85]
	v_lshl_add_u64 v[84:85], s[10:11], 0, v[84:85]
	v_lshl_add_u64 v[82:83], v[82:83], 0, v[146:147]
	s_andn2_b64 vcc, exec, s[36:37]
	v_lshl_add_u64 v[84:85], v[84:85], 0, v[146:147]
	s_cbranch_vccnz .LBB0_296
	s_mov_b32 s36, s34
	s_mov_b32 s37, s34
	s_waitcnt vmcnt(8)
	v_mov_b32_e32 v86, v204
	v_mov_b32_e32 v87, v205
	v_mov_b32_e32 v88, v206
	v_mov_b32_e32 v89, v207
	v_mov_b32_e32 v90, v208
	v_mov_b32_e32 v91, v209
	v_mov_b32_e32 v92, v210
	v_mov_b32_e32 v93, v211
	v_pk_mul_f32 v[94:95], v[74:75], v[92:93]
	v_pk_mul_f32 v[96:97], v[72:73], v[90:91]
	v_pk_fma_f32 v[94:95], v[78:79], v[88:89], v[94:95] neg_lo:[0,0,1] neg_hi:[0,0,1]
	v_pk_fma_f32 v[96:97], v[76:77], v[86:87], v[96:97] neg_lo:[0,0,1] neg_hi:[0,0,1]
	v_pk_mul_f32 v[78:79], v[78:79], v[92:93]
	v_pk_mul_f32 v[76:77], v[76:77], v[90:91]
	v_pk_mul_f32 v[94:95], s[36:37], v[94:95]
	v_pk_mul_f32 v[96:97], s[34:35], v[96:97]
	v_pk_fma_f32 v[74:75], v[74:75], v[88:89], v[78:79]
	v_pk_fma_f32 v[72:73], v[72:73], v[86:87], v[76:77]
	v_pk_mul_f32 v[74:75], s[36:37], v[74:75]
	v_pk_mul_f32 v[72:73], s[34:35], v[72:73]
	v_mov_b32_e32 v76, v96
	v_mov_b32_e32 v77, v97
	v_mov_b32_e32 v78, v94
	v_mov_b32_e32 v79, v95

.LBB0_298:
	s_andn2_b64 vcc, exec, s[36:37]
	s_cbranch_vccnz .LBB0_300
	s_mov_b32 s36, s34
	s_mov_b32 s37, s34
	v_mov_b32_e32 v86, v212
	v_mov_b32_e32 v87, v213
	v_mov_b32_e32 v88, v214
	v_mov_b32_e32 v89, v215
	v_mov_b32_e32 v82, v216
	v_mov_b32_e32 v83, v217
	v_mov_b32_e32 v84, v218
	v_mov_b32_e32 v85, v219
	v_add_u32_e32 v237, 0x5000, v236
	global_load_dwordx4 v[204:207], v237, s[8:9]
	global_load_dwordx4 v[208:211], v237, s[10:11]
	global_load_dwordx4 v[212:215], v237, s[8:9] offset:16
	global_load_dwordx4 v[216:219], v237, s[10:11] offset:16
	v_pk_mul_f32 v[90:91], v[66:67], v[84:85]
	v_pk_mul_f32 v[92:93], v[64:65], v[82:83]
	v_pk_fma_f32 v[90:91], v[70:71], v[88:89], v[90:91] neg_lo:[0,0,1] neg_hi:[0,0,1]
	v_pk_fma_f32 v[92:93], v[68:69], v[86:87], v[92:93] neg_lo:[0,0,1] neg_hi:[0,0,1]
	v_pk_mul_f32 v[70:71], v[70:71], v[84:85]
	v_pk_mul_f32 v[68:69], v[68:69], v[82:83]
	v_pk_mul_f32 v[90:91], s[36:37], v[90:91]
	v_pk_mul_f32 v[92:93], s[34:35], v[92:93]
	v_pk_fma_f32 v[66:67], v[66:67], v[88:89], v[70:71]
	v_pk_fma_f32 v[64:65], v[64:65], v[86:87], v[68:69]
	v_pk_mul_f32 v[66:67], s[36:37], v[66:67]
	v_pk_mul_f32 v[64:65], s[34:35], v[64:65]
	v_mov_b32_e32 v68, v92
	v_mov_b32_e32 v69, v93
	v_mov_b32_e32 v70, v90
	v_mov_b32_e32 v71, v91

.LBB0_302:
	v_add_u32_e32 v64, 0x90, v136
	v_ashrrev_i32_e32 v65, 31, v64
	v_lshlrev_b64 v[68:69], 7, v[64:65]
	v_lshl_add_u64 v[66:67], s[8:9], 0, v[68:69]
	v_lshl_add_u64 v[68:69], s[10:11], 0, v[68:69]
	v_lshl_add_u64 v[66:67], v[66:67], 0, v[146:147]
	s_andn2_b64 vcc, exec, s[36:37]
	v_lshl_add_u64 v[68:69], v[68:69], 0, v[146:147]
	s_cbranch_vccnz .LBB0_304
	s_mov_b32 s36, s34
	s_mov_b32 s37, s34
	s_waitcnt vmcnt(8)
	v_mov_b32_e32 v70, v220
	v_mov_b32_e32 v71, v221
	v_mov_b32_e32 v72, v222
	v_mov_b32_e32 v73, v223
	v_mov_b32_e32 v74, v224
	v_mov_b32_e32 v75, v225
	v_mov_b32_e32 v76, v226
	v_mov_b32_e32 v77, v227
	v_pk_mul_f32 v[78:79], v[50:51], v[76:77]
	v_pk_mul_f32 v[80:81], v[48:49], v[74:75]
	v_pk_fma_f32 v[78:79], v[54:55], v[72:73], v[78:79] neg_lo:[0,0,1] neg_hi:[0,0,1]
	v_pk_fma_f32 v[80:81], v[52:53], v[70:71], v[80:81] neg_lo:[0,0,1] neg_hi:[0,0,1]
	v_pk_mul_f32 v[54:55], v[54:55], v[76:77]
	v_pk_mul_f32 v[52:53], v[52:53], v[74:75]
	v_pk_mul_f32 v[78:79], s[36:37], v[78:79]
	v_pk_mul_f32 v[80:81], s[34:35], v[80:81]
	v_pk_fma_f32 v[50:51], v[50:51], v[72:73], v[54:55]
	v_pk_fma_f32 v[48:49], v[48:49], v[70:71], v[52:53]
	v_pk_mul_f32 v[50:51], s[36:37], v[50:51]
	v_pk_mul_f32 v[48:49], s[34:35], v[48:49]
	v_mov_b32_e32 v52, v80
	v_mov_b32_e32 v53, v81
	v_mov_b32_e32 v54, v78
	v_mov_b32_e32 v55, v79

.LBB0_306:
	s_andn2_b64 vcc, exec, s[36:37]
	s_cbranch_vccnz .LBB0_308
	s_mov_b32 s36, s34
	s_mov_b32 s37, s34
	v_mov_b32_e32 v70, v228
	v_mov_b32_e32 v71, v229
	v_mov_b32_e32 v72, v230
	v_mov_b32_e32 v73, v231
	v_mov_b32_e32 v66, v232
	v_mov_b32_e32 v67, v233
	v_mov_b32_e32 v68, v234
	v_mov_b32_e32 v69, v235
	v_add_u32_e32 v237, 0x5800, v236
	global_load_dwordx4 v[220:223], v237, s[8:9]
	global_load_dwordx4 v[224:227], v237, s[10:11]
	global_load_dwordx4 v[228:231], v237, s[8:9] offset:16
	global_load_dwordx4 v[232:235], v237, s[10:11] offset:16
	v_pk_mul_f32 v[74:75], v[34:35], v[68:69]
	v_pk_mul_f32 v[76:77], v[32:33], v[66:67]
	v_pk_fma_f32 v[74:75], v[38:39], v[72:73], v[74:75] neg_lo:[0,0,1] neg_hi:[0,0,1]
	v_pk_fma_f32 v[76:77], v[36:37], v[70:71], v[76:77] neg_lo:[0,0,1] neg_hi:[0,0,1]
	v_pk_mul_f32 v[38:39], v[38:39], v[68:69]
	v_pk_mul_f32 v[36:37], v[36:37], v[66:67]
	v_pk_mul_f32 v[74:75], s[36:37], v[74:75]
	v_pk_mul_f32 v[76:77], s[34:35], v[76:77]
	v_pk_fma_f32 v[34:35], v[34:35], v[72:73], v[38:39]
	v_pk_fma_f32 v[32:33], v[32:33], v[70:71], v[36:37]
	v_pk_mul_f32 v[34:35], s[36:37], v[34:35]
	v_pk_mul_f32 v[32:33], s[34:35], v[32:33]
	v_mov_b32_e32 v36, v76
	v_mov_b32_e32 v37, v77
	v_mov_b32_e32 v38, v74
	v_mov_b32_e32 v39, v75

.LBB0_310:
	v_add_u32_e32 v32, 0xa0, v136
	v_ashrrev_i32_e32 v33, 31, v32
	v_lshlrev_b64 v[36:37], 7, v[32:33]
	v_lshl_add_u64 v[34:35], s[8:9], 0, v[36:37]
	v_lshl_add_u64 v[36:37], s[10:11], 0, v[36:37]
	v_lshl_add_u64 v[34:35], v[34:35], 0, v[146:147]
	s_andn2_b64 vcc, exec, s[36:37]
	v_lshl_add_u64 v[36:37], v[36:37], 0, v[146:147]
	s_cbranch_vccnz .LBB0_312
	s_mov_b32 s36, s34
	s_mov_b32 s37, s34
	s_waitcnt vmcnt(8)
	v_mov_b32_e32 v48, v204
	v_mov_b32_e32 v49, v205
	v_mov_b32_e32 v50, v206
	v_mov_b32_e32 v51, v207
	v_mov_b32_e32 v52, v208
	v_mov_b32_e32 v53, v209
	v_mov_b32_e32 v54, v210
	v_mov_b32_e32 v55, v211
	v_pk_mul_f32 v[38:39], v[26:27], v[54:55]
	v_pk_mul_f32 v[64:65], v[24:25], v[52:53]
	v_pk_fma_f32 v[38:39], v[30:31], v[50:51], v[38:39] neg_lo:[0,0,1] neg_hi:[0,0,1]
	v_pk_fma_f32 v[64:65], v[28:29], v[48:49], v[64:65] neg_lo:[0,0,1] neg_hi:[0,0,1]
	v_pk_mul_f32 v[30:31], v[30:31], v[54:55]
	v_pk_mul_f32 v[28:29], v[28:29], v[52:53]
	v_pk_mul_f32 v[38:39], s[36:37], v[38:39]
	v_pk_mul_f32 v[64:65], s[34:35], v[64:65]
	v_pk_fma_f32 v[26:27], v[26:27], v[50:51], v[30:31]
	v_pk_fma_f32 v[24:25], v[24:25], v[48:49], v[28:29]
	v_pk_mul_f32 v[26:27], s[36:37], v[26:27]
	v_pk_mul_f32 v[24:25], s[34:35], v[24:25]
	v_mov_b32_e32 v28, v64
	v_mov_b32_e32 v29, v65
	v_mov_b32_e32 v30, v38
	v_mov_b32_e32 v31, v39

.LBB0_314:
	s_andn2_b64 vcc, exec, s[36:37]
	s_cbranch_vccnz .LBB0_316
	s_mov_b32 s36, s34
	s_mov_b32 s37, s34
	v_mov_b32_e32 v48, v212
	v_mov_b32_e32 v49, v213
	v_mov_b32_e32 v50, v214
	v_mov_b32_e32 v51, v215
	v_mov_b32_e32 v34, v216
	v_mov_b32_e32 v35, v217
	v_mov_b32_e32 v36, v218
	v_mov_b32_e32 v37, v219
	v_pk_mul_f32 v[38:39], v[18:19], v[36:37]
	v_pk_mul_f32 v[52:53], v[16:17], v[34:35]
	v_pk_fma_f32 v[38:39], v[22:23], v[50:51], v[38:39] neg_lo:[0,0,1] neg_hi:[0,0,1]
	v_pk_fma_f32 v[52:53], v[20:21], v[48:49], v[52:53] neg_lo:[0,0,1] neg_hi:[0,0,1]
	v_pk_mul_f32 v[22:23], v[22:23], v[36:37]
	v_pk_mul_f32 v[20:21], v[20:21], v[34:35]
	v_pk_mul_f32 v[38:39], s[36:37], v[38:39]
	v_pk_mul_f32 v[52:53], s[34:35], v[52:53]
	v_pk_fma_f32 v[18:19], v[18:19], v[50:51], v[22:23]
	v_pk_fma_f32 v[16:17], v[16:17], v[48:49], v[20:21]
	v_pk_mul_f32 v[18:19], s[36:37], v[18:19]
	v_pk_mul_f32 v[16:17], s[34:35], v[16:17]
	v_mov_b32_e32 v20, v52
	v_mov_b32_e32 v21, v53
	v_mov_b32_e32 v22, v38
	v_mov_b32_e32 v23, v39

.LBB0_318:
	v_add_u32_e32 v16, 0xb0, v136
	v_ashrrev_i32_e32 v17, 31, v16
	v_lshlrev_b64 v[20:21], 7, v[16:17]
	v_lshl_add_u64 v[18:19], s[8:9], 0, v[20:21]
	v_lshl_add_u64 v[20:21], s[10:11], 0, v[20:21]
	v_lshl_add_u64 v[18:19], v[18:19], 0, v[146:147]
	s_andn2_b64 vcc, exec, s[36:37]
	v_lshl_add_u64 v[20:21], v[20:21], 0, v[146:147]
	s_cbranch_vccnz .LBB0_320
	s_mov_b32 s36, s34
	s_mov_b32 s37, s34
	s_waitcnt vmcnt(4)
	v_mov_b32_e32 v22, v220
	v_mov_b32_e32 v23, v221
	v_mov_b32_e32 v24, v222
	v_mov_b32_e32 v25, v223
	v_mov_b32_e32 v26, v224
	v_mov_b32_e32 v27, v225
	v_mov_b32_e32 v28, v226
	v_mov_b32_e32 v29, v227
	v_pk_mul_f32 v[30:31], v[10:11], v[28:29]
	v_pk_mul_f32 v[32:33], v[8:9], v[26:27]
	v_pk_fma_f32 v[30:31], v[14:15], v[24:25], v[30:31] neg_lo:[0,0,1] neg_hi:[0,0,1]
	v_pk_fma_f32 v[32:33], v[12:13], v[22:23], v[32:33] neg_lo:[0,0,1] neg_hi:[0,0,1]
	v_pk_mul_f32 v[14:15], v[14:15], v[28:29]
	v_pk_mul_f32 v[12:13], v[12:13], v[26:27]
	v_pk_mul_f32 v[30:31], s[36:37], v[30:31]
	v_pk_mul_f32 v[32:33], s[34:35], v[32:33]
	v_pk_fma_f32 v[10:11], v[10:11], v[24:25], v[14:15]
	v_pk_fma_f32 v[8:9], v[8:9], v[22:23], v[12:13]
	v_pk_mul_f32 v[10:11], s[36:37], v[10:11]
	v_pk_mul_f32 v[8:9], s[34:35], v[8:9]
	v_mov_b32_e32 v12, v32
	v_mov_b32_e32 v13, v33
	v_mov_b32_e32 v14, v30
	v_mov_b32_e32 v15, v31

.LBB0_322:
	s_andn2_b64 vcc, exec, s[4:5]
	s_cbranch_vccnz .LBB0_324
	s_mov_b32 s4, s34
	s_mov_b32 s5, s34
	v_mov_b32_e32 v22, v228
	v_mov_b32_e32 v23, v229
	v_mov_b32_e32 v24, v230
	v_mov_b32_e32 v25, v231
	v_mov_b32_e32 v18, v232
	v_mov_b32_e32 v19, v233
	v_mov_b32_e32 v20, v234
	v_mov_b32_e32 v21, v235
	v_pk_mul_f32 v[26:27], v[2:3], v[20:21]
	v_pk_mul_f32 v[28:29], v[0:1], v[18:19]
	v_pk_fma_f32 v[26:27], v[6:7], v[24:25], v[26:27] neg_lo:[0,0,1] neg_hi:[0,0,1]
	v_pk_fma_f32 v[28:29], v[4:5], v[22:23], v[28:29] neg_lo:[0,0,1] neg_hi:[0,0,1]
	v_pk_mul_f32 v[6:7], v[6:7], v[20:21]
	v_pk_mul_f32 v[4:5], v[4:5], v[18:19]
	v_pk_mul_f32 v[26:27], s[4:5], v[26:27]
	v_pk_mul_f32 v[28:29], s[34:35], v[28:29]
	v_pk_fma_f32 v[2:3], v[2:3], v[24:25], v[6:7]
	v_pk_fma_f32 v[0:1], v[0:1], v[22:23], v[4:5]
	v_pk_mul_f32 v[2:3], s[4:5], v[2:3]
	v_pk_mul_f32 v[0:1], s[34:35], v[0:1]
	v_mov_b32_e32 v4, v28
	v_mov_b32_e32 v5, v29
	v_mov_b32_e32 v6, v26
	v_mov_b32_e32 v7, v27

.LBB0_333:
	ds_read_b128 v[52:55], v38
	ds_read_b128 v[56:59], v38 offset:1024
	ds_read_b128 v[80:83], v38 offset:2048
	ds_read_b128 v[84:87], v38 offset:3072
	ds_read_b128 v[88:91], v39
	ds_read_b128 v[92:95], v39 offset:1024
	ds_read_b128 v[96:99], v39 offset:2048
	ds_read_b128 v[100:103], v39 offset:3072
	s_cmp_eq_u32 s34, 12
	s_cselect_b32 s14, s4, s30
	s_cselect_b32 s15, s5, s31
	s_cselect_b32 s18, s12, s28
	s_cselect_b32 s19, s13, s29
	s_add_u32 s16, s14, 0x80
	s_addc_u32 s17, s15, 0
	ds_read_b128 v[104:107], v40
	ds_read_b128 v[108:111], v40 offset:1024
	ds_read_b128 v[112:115], v40 offset:2048
	ds_read_b128 v[116:119], v40 offset:3072
	ds_read_b128 v[120:123], v40 offset:4096
	ds_read_b128 v[124:127], v40 offset:5120
	ds_read_b128 v[128:131], v40 offset:6144
	ds_read_b128 v[132:135], v40 offset:7168
	s_waitcnt vmcnt(6)
	s_waitcnt lgkmcnt(0)
	s_barrier
	s_setprio 3
	v_mfma_f32_16x16x32_bf16 v[76:79], v[52:55], v[104:107], v[76:79]
	v_mfma_f32_16x16x32_bf16 v[68:71], v[80:83], v[104:107], v[68:71]
	v_mfma_f32_16x16x32_bf16 v[60:63], v[52:55], v[112:115], v[60:63]
	v_mfma_f32_16x16x32_bf16 v[44:47], v[80:83], v[112:115], v[44:47]
	v_mfma_f32_16x16x32_bf16 v[28:31], v[52:55], v[120:123], v[28:31]
	v_mfma_f32_16x16x32_bf16 v[20:23], v[80:83], v[120:123], v[20:23]
	v_mfma_f32_16x16x32_bf16 v[12:15], v[52:55], v[128:131], v[12:15]
	v_mfma_f32_16x16x32_bf16 v[4:7], v[80:83], v[128:131], v[4:7]
	v_mfma_f32_16x16x32_bf16 v[76:79], v[56:59], v[108:111], v[76:79]
	v_mfma_f32_16x16x32_bf16 v[68:71], v[84:87], v[108:111], v[68:71]
	v_mfma_f32_16x16x32_bf16 v[60:63], v[56:59], v[116:119], v[60:63]
	v_mfma_f32_16x16x32_bf16 v[44:47], v[84:87], v[116:119], v[44:47]
	v_mfma_f32_16x16x32_bf16 v[28:31], v[56:59], v[124:127], v[28:31]
	v_mfma_f32_16x16x32_bf16 v[20:23], v[84:87], v[124:127], v[20:23]
	v_mfma_f32_16x16x32_bf16 v[12:15], v[56:59], v[132:135], v[12:15]
	v_mfma_f32_16x16x32_bf16 v[4:7], v[84:87], v[132:135], v[4:7]
	v_mfma_f32_16x16x32_bf16 v[48:51], v[88:91], v[112:115], v[48:51]
	v_mfma_f32_16x16x32_bf16 v[32:35], v[96:99], v[112:115], v[32:35]
	v_mfma_f32_16x16x32_bf16 v[24:27], v[88:91], v[120:123], v[24:27]
	v_mfma_f32_16x16x32_bf16 v[16:19], v[96:99], v[120:123], v[16:19]
	v_mfma_f32_16x16x32_bf16 v[8:11], v[88:91], v[128:131], v[8:11]
	v_mfma_f32_16x16x32_bf16 v[0:3], v[96:99], v[128:131], v[0:3]
	v_mfma_f32_16x16x32_bf16 v[52:55], v[88:91], v[104:107], v[72:75]
	v_mfma_f32_16x16x32_bf16 v[56:59], v[96:99], v[104:107], v[64:67]
	v_mfma_f32_16x16x32_bf16 v[48:51], v[92:95], v[116:119], v[48:51]
	v_mfma_f32_16x16x32_bf16 v[32:35], v[100:103], v[116:119], v[32:35]
	v_mfma_f32_16x16x32_bf16 v[24:27], v[92:95], v[124:127], v[24:27]
	v_mfma_f32_16x16x32_bf16 v[16:19], v[100:103], v[124:127], v[16:19]
	v_mfma_f32_16x16x32_bf16 v[8:11], v[92:95], v[132:135], v[8:11]
	v_mfma_f32_16x16x32_bf16 v[0:3], v[100:103], v[132:135], v[0:3]
	v_mfma_f32_16x16x32_bf16 v[52:55], v[92:95], v[108:111], v[52:55]
	v_mfma_f32_16x16x32_bf16 v[56:59], v[100:103], v[108:111], v[56:59]
	s_setprio 0
	s_barrier
	v_mov_b32_e32 v43, v36
	s_mov_b64 s[50:51], s[18:19]
	s_mov_b32 m0, s35
	s_nop 0
	global_load_lds_dwordx4 v43, s[50:51]
	s_add_u32 s50, s18, 0x20000
	v_mov_b32_e32 v43, v36
	s_addc_u32 s51, s19, 0
	s_mov_b32 m0, s36
	s_nop 0
	global_load_lds_dwordx4 v43, s[50:51]
	s_add_u32 s50, s18, 0x40000
	v_mov_b32_e32 v43, v36
	s_addc_u32 s51, s19, 0
	s_mov_b32 m0, s37
	s_nop 0
	global_load_lds_dwordx4 v43, s[50:51]
	s_add_u32 s50, s18, 0x60000
	v_mov_b32_e32 v43, v36
	s_addc_u32 s51, s19, 0
	s_mov_b32 m0, s38
	s_nop 0
	global_load_lds_dwordx4 v43, s[50:51]
	v_mov_b32_e32 v43, v37
	s_mov_b64 s[50:51], s[14:15]
	s_mov_b32 m0, s23
	s_nop 0
	global_load_lds_dwordx4 v43, s[50:51]
	s_add_u32 s50, s14, 0x20000
	v_mov_b32_e32 v43, v37
	s_addc_u32 s51, s15, 0
	s_mov_b32 m0, s24
	s_nop 0
	global_load_lds_dwordx4 v43, s[50:51]
	s_waitcnt vmcnt(6)
	s_waitcnt lgkmcnt(0)
	s_barrier
	s_barrier
	ds_read_b128 v[64:67], v41
	ds_read_b128 v[72:75], v41 offset:1024
	ds_read_b128 v[80:83], v41 offset:2048
	ds_read_b128 v[84:87], v41 offset:3072
	ds_read_b128 v[88:91], v42
	ds_read_b128 v[92:95], v42 offset:1024
	ds_read_b128 v[96:99], v42 offset:2048
	ds_read_b128 v[100:103], v42 offset:3072
	ds_read_b128 v[104:107], v40 offset:32768
	ds_read_b128 v[108:111], v40 offset:33792
	ds_read_b128 v[112:115], v40 offset:34816
	ds_read_b128 v[116:119], v40 offset:35840
	ds_read_b128 v[120:123], v40 offset:36864
	ds_read_b128 v[124:127], v40 offset:37888
	ds_read_b128 v[128:131], v40 offset:38912
	ds_read_b128 v[132:135], v40 offset:39936
	s_waitcnt vmcnt(6)
	s_waitcnt lgkmcnt(0)
	s_barrier
	s_setprio 3
	v_mfma_f32_16x16x32_bf16 v[76:79], v[64:67], v[104:107], v[76:79]
	v_mfma_f32_16x16x32_bf16 v[68:71], v[80:83], v[104:107], v[68:71]
	v_mfma_f32_16x16x32_bf16 v[60:63], v[64:67], v[112:115], v[60:63]
	v_mfma_f32_16x16x32_bf16 v[44:47], v[80:83], v[112:115], v[44:47]
	v_mfma_f32_16x16x32_bf16 v[28:31], v[64:67], v[120:123], v[28:31]
	v_mfma_f32_16x16x32_bf16 v[20:23], v[80:83], v[120:123], v[20:23]
	v_mfma_f32_16x16x32_bf16 v[12:15], v[64:67], v[128:131], v[12:15]
	v_mfma_f32_16x16x32_bf16 v[4:7], v[80:83], v[128:131], v[4:7]
	v_mfma_f32_16x16x32_bf16 v[76:79], v[72:75], v[108:111], v[76:79]
	v_mfma_f32_16x16x32_bf16 v[68:71], v[84:87], v[108:111], v[68:71]
	v_mfma_f32_16x16x32_bf16 v[60:63], v[72:75], v[116:119], v[60:63]
	v_mfma_f32_16x16x32_bf16 v[44:47], v[84:87], v[116:119], v[44:47]
	v_mfma_f32_16x16x32_bf16 v[28:31], v[72:75], v[124:127], v[28:31]
	v_mfma_f32_16x16x32_bf16 v[20:23], v[84:87], v[124:127], v[20:23]
	v_mfma_f32_16x16x32_bf16 v[12:15], v[72:75], v[132:135], v[12:15]
	v_mfma_f32_16x16x32_bf16 v[4:7], v[84:87], v[132:135], v[4:7]
	v_mfma_f32_16x16x32_bf16 v[52:55], v[88:91], v[104:107], v[52:55]
	s_add_u32 s50, s18, 0x80
	s_addc_u32 s51, s19, 0
	v_mfma_f32_16x16x32_bf16 v[72:75], v[92:95], v[108:111], v[52:55]
	v_mfma_f32_16x16x32_bf16 v[52:55], v[96:99], v[104:107], v[56:59]
	v_mfma_f32_16x16x32_bf16 v[48:51], v[88:91], v[112:115], v[48:51]
	v_mfma_f32_16x16x32_bf16 v[32:35], v[96:99], v[112:115], v[32:35]
	v_mfma_f32_16x16x32_bf16 v[24:27], v[88:91], v[120:123], v[24:27]
	v_mfma_f32_16x16x32_bf16 v[16:19], v[96:99], v[120:123], v[16:19]
	v_mfma_f32_16x16x32_bf16 v[8:11], v[88:91], v[128:131], v[8:11]
	v_mfma_f32_16x16x32_bf16 v[0:3], v[96:99], v[128:131], v[0:3]
	v_mfma_f32_16x16x32_bf16 v[64:67], v[100:103], v[108:111], v[52:55]
	v_mfma_f32_16x16x32_bf16 v[48:51], v[92:95], v[116:119], v[48:51]
	v_mfma_f32_16x16x32_bf16 v[32:35], v[100:103], v[116:119], v[32:35]
	v_mfma_f32_16x16x32_bf16 v[24:27], v[92:95], v[124:127], v[24:27]
	v_mfma_f32_16x16x32_bf16 v[16:19], v[100:103], v[124:127], v[16:19]
	v_mfma_f32_16x16x32_bf16 v[8:11], v[92:95], v[132:135], v[8:11]
	v_mfma_f32_16x16x32_bf16 v[0:3], v[100:103], v[132:135], v[0:3]
	s_setprio 0
	s_barrier
	v_mov_b32_e32 v43, v36
	s_mov_b32 m0, s39
	s_nop 0
	global_load_lds_dwordx4 v43, s[50:51]
	s_add_u32 s50, s18, 0x20080
	v_mov_b32_e32 v43, v36
	s_addc_u32 s51, s19, 0
	s_mov_b32 m0, s40
	s_nop 0
	global_load_lds_dwordx4 v43, s[50:51]
	v_mov_b32_e32 v43, v36
	s_add_u32 s50, s18, 0x40080
	s_addc_u32 s51, s19, 0
	s_mov_b32 m0, s41
	s_add_u32 s18, s18, 0x60080
	global_load_lds_dwordx4 v43, s[50:51]
	v_mov_b32_e32 v43, v36
	s_addc_u32 s19, s19, 0
	s_mov_b32 m0, s49
	s_add_u32 s14, s14, 0x20080
	global_load_lds_dwordx4 v43, s[18:19]
	v_mov_b32_e32 v43, v37
	s_mov_b32 m0, s26
	s_addc_u32 s15, s15, 0
	global_load_lds_dwordx4 v43, s[16:17]
	v_mov_b32_e32 v43, v37
	s_mov_b32 m0, s27
	s_nop 0
	global_load_lds_dwordx4 v43, s[14:15]
	s_waitcnt vmcnt(6)
	s_waitcnt lgkmcnt(0)
	s_barrier
	s_barrier
	s_add_i32 s34, s34, 2
	s_add_u32 s28, s28, 0x100
	s_addc_u32 s29, s29, 0
	s_add_u32 s30, s30, 0x100
	s_addc_u32 s31, s31, 0
	s_cmp_gt_u32 s34, 13
	s_cbranch_scc0 .LBB0_333
	s_cmpk_lt_u32 s1, 0x100
	s_cbranch_scc0 .LBB0_336
	s_barrier

.LBB0_725:
	ds_read_b128 v[130:133], v177
	ds_read_b128 v[134:137], v177 offset:1024
	ds_read_b128 v[138:141], v177 offset:2048
	ds_read_b128 v[142:145], v177 offset:3072
	ds_read_b128 v[146:149], v178
	ds_read_b128 v[150:153], v178 offset:1024
	ds_read_b128 v[154:157], v178 offset:2048
	ds_read_b128 v[158:161], v178 offset:3072
	s_add_u32 s26, s24, 0xfffa0080
	s_addc_u32 s27, s25, -1
	s_cmp_eq_u32 s60, 12
	s_cselect_b32 s26, s18, s26
	s_cselect_b32 s27, s19, s27
	s_cselect_b32 s30, s20, s15
	s_cselect_b32 s31, s21, s17
	s_add_u32 s28, s26, 0x80
	s_addc_u32 s29, s27, 0
	s_add_u32 s64, s24, 0xfffe0000
	v_mov_b32_e32 v200, v175
	s_addc_u32 s65, s25, -1
	ds_read_b128 v[162:165], v179
	ds_read_b128 v[166:169], v179 offset:1024
	ds_read_b128 v[170:173], v179 offset:2048
	ds_read_b128 v[180:183], v179 offset:3072
	ds_read_b128 v[184:187], v179 offset:4096
	ds_read_b128 v[188:191], v179 offset:5120
	ds_read_b128 v[192:195], v179 offset:6144
	ds_read_b128 v[196:199], v179 offset:7168
	s_add_i32 m0, s23, 0xc000
	s_nop 0
	global_load_lds_dwordx4 v200, s[64:65]
	v_mov_b32_e32 v200, v175
	s_mov_b64 s[64:65], s[24:25]
	s_add_i32 m0, s23, 0xe000
	s_nop 0
	global_load_lds_dwordx4 v200, s[64:65]
	s_waitcnt vmcnt(8)
	s_waitcnt lgkmcnt(0)
	s_barrier
	s_setprio 3
	v_mfma_f32_16x16x32_bf16 v[124:127], v[130:133], v[162:165], v[124:127]
	v_mfma_f32_16x16x32_bf16 v[120:123], v[138:141], v[162:165], v[120:123]
	v_mfma_f32_16x16x32_bf16 v[108:111], v[130:133], v[170:173], v[108:111]
	v_mfma_f32_16x16x32_bf16 v[104:107], v[138:141], v[170:173], v[104:107]
	v_mfma_f32_16x16x32_bf16 v[92:95], v[130:133], v[184:187], v[92:95]
	v_mfma_f32_16x16x32_bf16 v[88:91], v[138:141], v[184:187], v[88:91]
	v_mfma_f32_16x16x32_bf16 v[76:79], v[130:133], v[192:195], v[76:79]
	v_mfma_f32_16x16x32_bf16 v[72:75], v[138:141], v[192:195], v[72:75]
	v_mfma_f32_16x16x32_bf16 v[124:127], v[134:137], v[166:169], v[124:127]
	v_mfma_f32_16x16x32_bf16 v[120:123], v[142:145], v[166:169], v[120:123]
	v_mfma_f32_16x16x32_bf16 v[108:111], v[134:137], v[180:183], v[108:111]
	v_mfma_f32_16x16x32_bf16 v[104:107], v[142:145], v[180:183], v[104:107]
	v_mfma_f32_16x16x32_bf16 v[92:95], v[134:137], v[188:191], v[92:95]
	v_mfma_f32_16x16x32_bf16 v[88:91], v[142:145], v[188:191], v[88:91]
	v_mfma_f32_16x16x32_bf16 v[76:79], v[134:137], v[196:199], v[76:79]
	v_mfma_f32_16x16x32_bf16 v[72:75], v[142:145], v[196:199], v[72:75]
	v_mfma_f32_16x16x32_bf16 v[116:119], v[146:149], v[162:165], v[116:119]
	v_mfma_f32_16x16x32_bf16 v[112:115], v[154:157], v[162:165], v[112:115]
	v_mfma_f32_16x16x32_bf16 v[100:103], v[146:149], v[170:173], v[100:103]
	v_mfma_f32_16x16x32_bf16 v[96:99], v[154:157], v[170:173], v[96:99]
	v_mfma_f32_16x16x32_bf16 v[84:87], v[146:149], v[184:187], v[84:87]
	v_mfma_f32_16x16x32_bf16 v[80:83], v[154:157], v[184:187], v[80:83]
	v_mfma_f32_16x16x32_bf16 v[68:71], v[146:149], v[192:195], v[68:71]
	v_mfma_f32_16x16x32_bf16 v[64:67], v[154:157], v[192:195], v[64:67]
	v_mfma_f32_16x16x32_bf16 v[116:119], v[150:153], v[166:169], v[116:119]
	v_mfma_f32_16x16x32_bf16 v[112:115], v[158:161], v[166:169], v[112:115]
	v_mfma_f32_16x16x32_bf16 v[100:103], v[150:153], v[180:183], v[100:103]
	v_mfma_f32_16x16x32_bf16 v[96:99], v[158:161], v[180:183], v[96:99]
	v_mfma_f32_16x16x32_bf16 v[84:87], v[150:153], v[188:191], v[84:87]
	v_mfma_f32_16x16x32_bf16 v[80:83], v[158:161], v[188:191], v[80:83]
	v_mfma_f32_16x16x32_bf16 v[68:71], v[150:153], v[196:199], v[68:71]
	v_mfma_f32_16x16x32_bf16 v[64:67], v[158:161], v[196:199], v[64:67]
	s_setprio 0
	s_barrier
	v_mov_b32_e32 v200, v174
	s_mov_b64 s[64:65], s[30:31]
	s_add_i32 s61, s51, s36
	ds_read_b128 v[162:165], v179 offset:16384
	ds_read_b128 v[166:169], v179 offset:17408
	ds_read_b128 v[170:173], v179 offset:18432
	ds_read_b128 v[180:183], v179 offset:19456
	ds_read_b128 v[184:187], v179 offset:20480
	ds_read_b128 v[188:191], v179 offset:21504
	ds_read_b128 v[192:195], v179 offset:22528
	ds_read_b128 v[196:199], v179 offset:23552
	s_mov_b32 m0, s61
	s_nop 0
	global_load_lds_dwordx4 v200, s[64:65]
	s_add_u32 s64, s30, 0x20000
	v_mov_b32_e32 v200, v174
	s_addc_u32 s65, s31, 0
	s_add_i32 m0, s61, 0x2000
	s_nop 0
	global_load_lds_dwordx4 v200, s[64:65]
	s_add_u32 s64, s30, 0x40000
	v_mov_b32_e32 v200, v174
	s_addc_u32 s65, s31, 0
	s_add_i32 s61, s52, s36
	s_mov_b32 m0, s61
	s_nop 0
	global_load_lds_dwordx4 v200, s[64:65]
	s_add_u32 s64, s30, 0x60000
	v_mov_b32_e32 v200, v174
	s_addc_u32 s65, s31, 0
	s_add_i32 m0, s61, 0x2000
	s_nop 0
	global_load_lds_dwordx4 v200, s[64:65]
	v_mov_b32_e32 v200, v175
	s_mov_b64 s[64:65], s[26:27]
	s_mov_b32 m0, s23
	s_nop 0
	global_load_lds_dwordx4 v200, s[64:65]
	s_add_u32 s64, s26, 0x20000
	v_mov_b32_e32 v200, v175
	s_addc_u32 s65, s27, 0
	s_mov_b32 m0, s38
	s_nop 0
	global_load_lds_dwordx4 v200, s[64:65]
	s_waitcnt vmcnt(8)
	s_waitcnt lgkmcnt(0)
	s_barrier
	s_setprio 3
	v_mfma_f32_16x16x32_bf16 v[60:63], v[130:133], v[162:165], v[60:63]
	v_mfma_f32_16x16x32_bf16 v[56:59], v[138:141], v[162:165], v[56:59]
	v_mfma_f32_16x16x32_bf16 v[44:47], v[130:133], v[170:173], v[44:47]
	v_mfma_f32_16x16x32_bf16 v[40:43], v[138:141], v[170:173], v[40:43]
	v_mfma_f32_16x16x32_bf16 v[28:31], v[130:133], v[184:187], v[28:31]
	v_mfma_f32_16x16x32_bf16 v[24:27], v[138:141], v[184:187], v[24:27]
	v_mfma_f32_16x16x32_bf16 v[12:15], v[130:133], v[192:195], v[12:15]
	v_mfma_f32_16x16x32_bf16 v[8:11], v[138:141], v[192:195], v[8:11]
	v_mfma_f32_16x16x32_bf16 v[60:63], v[134:137], v[166:169], v[60:63]
	v_mfma_f32_16x16x32_bf16 v[56:59], v[142:145], v[166:169], v[56:59]
	v_mfma_f32_16x16x32_bf16 v[44:47], v[134:137], v[180:183], v[44:47]
	v_mfma_f32_16x16x32_bf16 v[40:43], v[142:145], v[180:183], v[40:43]
	v_mfma_f32_16x16x32_bf16 v[28:31], v[134:137], v[188:191], v[28:31]
	v_mfma_f32_16x16x32_bf16 v[24:27], v[142:145], v[188:191], v[24:27]
	v_mfma_f32_16x16x32_bf16 v[12:15], v[134:137], v[196:199], v[12:15]
	v_mfma_f32_16x16x32_bf16 v[8:11], v[142:145], v[196:199], v[8:11]
	v_mfma_f32_16x16x32_bf16 v[52:55], v[146:149], v[162:165], v[52:55]
	v_mfma_f32_16x16x32_bf16 v[48:51], v[154:157], v[162:165], v[48:51]
	v_mfma_f32_16x16x32_bf16 v[36:39], v[146:149], v[170:173], v[36:39]
	v_mfma_f32_16x16x32_bf16 v[32:35], v[154:157], v[170:173], v[32:35]
	v_mfma_f32_16x16x32_bf16 v[20:23], v[146:149], v[184:187], v[20:23]
	v_mfma_f32_16x16x32_bf16 v[16:19], v[154:157], v[184:187], v[16:19]
	v_mfma_f32_16x16x32_bf16 v[4:7], v[146:149], v[192:195], v[4:7]
	v_mfma_f32_16x16x32_bf16 v[0:3], v[154:157], v[192:195], v[0:3]
	v_mfma_f32_16x16x32_bf16 v[52:55], v[150:153], v[166:169], v[52:55]
	v_mfma_f32_16x16x32_bf16 v[48:51], v[158:161], v[166:169], v[48:51]
	v_mfma_f32_16x16x32_bf16 v[36:39], v[150:153], v[180:183], v[36:39]
	v_mfma_f32_16x16x32_bf16 v[32:35], v[158:161], v[180:183], v[32:35]
	v_mfma_f32_16x16x32_bf16 v[20:23], v[150:153], v[188:191], v[20:23]
	v_mfma_f32_16x16x32_bf16 v[16:19], v[158:161], v[188:191], v[16:19]
	v_mfma_f32_16x16x32_bf16 v[4:7], v[150:153], v[196:199], v[4:7]
	v_mfma_f32_16x16x32_bf16 v[0:3], v[158:161], v[196:199], v[0:3]
	s_setprio 0
	s_barrier
	s_add_i32 s61, 0, 0x18000
	s_add_i32 s68, 0, 0x1c000
	v_add_u32_e32 v142, s61, v176
	v_add_u32_e32 v158, s68, v176
	ds_read_b128 v[130:133], v142
	ds_read_b128 v[134:137], v142 offset:1024
	ds_read_b128 v[138:141], v142 offset:2048
	ds_read_b128 v[142:145], v142 offset:3072
	ds_read_b128 v[146:149], v158
	ds_read_b128 v[150:153], v158 offset:1024
	ds_read_b128 v[154:157], v158 offset:2048
	ds_read_b128 v[158:161], v158 offset:3072
	s_add_u32 s64, s26, 0x40000
	v_mov_b32_e32 v200, v175
	s_addc_u32 s65, s27, 0
	s_mov_b32 m0, s39
	ds_read_b128 v[162:165], v179 offset:32768
	ds_read_b128 v[166:169], v179 offset:33792
	ds_read_b128 v[170:173], v179 offset:34816
	ds_read_b128 v[180:183], v179 offset:35840
	ds_read_b128 v[184:187], v179 offset:36864
	ds_read_b128 v[188:191], v179 offset:37888
	ds_read_b128 v[192:195], v179 offset:38912
	ds_read_b128 v[196:199], v179 offset:39936
	s_nop 0
	global_load_lds_dwordx4 v200, s[64:65]
	s_add_u32 s64, s26, 0x60000
	v_mov_b32_e32 v200, v175
	s_addc_u32 s65, s27, 0
	s_mov_b32 m0, s40
	s_nop 0
	global_load_lds_dwordx4 v200, s[64:65]
	s_waitcnt vmcnt(8)
	s_waitcnt lgkmcnt(0)
	s_barrier
	s_setprio 3
	v_mfma_f32_16x16x32_bf16 v[124:127], v[130:133], v[162:165], v[124:127]
	v_mfma_f32_16x16x32_bf16 v[120:123], v[138:141], v[162:165], v[120:123]
	v_mfma_f32_16x16x32_bf16 v[108:111], v[130:133], v[170:173], v[108:111]
	v_mfma_f32_16x16x32_bf16 v[104:107], v[138:141], v[170:173], v[104:107]
	v_mfma_f32_16x16x32_bf16 v[92:95], v[130:133], v[184:187], v[92:95]
	v_mfma_f32_16x16x32_bf16 v[88:91], v[138:141], v[184:187], v[88:91]
	v_mfma_f32_16x16x32_bf16 v[76:79], v[130:133], v[192:195], v[76:79]
	v_mfma_f32_16x16x32_bf16 v[72:75], v[138:141], v[192:195], v[72:75]
	v_mfma_f32_16x16x32_bf16 v[124:127], v[134:137], v[166:169], v[124:127]
	v_mfma_f32_16x16x32_bf16 v[120:123], v[142:145], v[166:169], v[120:123]
	v_mfma_f32_16x16x32_bf16 v[108:111], v[134:137], v[180:183], v[108:111]
	v_mfma_f32_16x16x32_bf16 v[104:107], v[142:145], v[180:183], v[104:107]
	v_mfma_f32_16x16x32_bf16 v[92:95], v[134:137], v[188:191], v[92:95]
	v_mfma_f32_16x16x32_bf16 v[88:91], v[142:145], v[188:191], v[88:91]
	v_mfma_f32_16x16x32_bf16 v[76:79], v[134:137], v[196:199], v[76:79]
	v_mfma_f32_16x16x32_bf16 v[72:75], v[142:145], v[196:199], v[72:75]
	v_mfma_f32_16x16x32_bf16 v[116:119], v[146:149], v[162:165], v[116:119]
	v_mfma_f32_16x16x32_bf16 v[112:115], v[154:157], v[162:165], v[112:115]
	v_mfma_f32_16x16x32_bf16 v[100:103], v[146:149], v[170:173], v[100:103]
	v_mfma_f32_16x16x32_bf16 v[96:99], v[154:157], v[170:173], v[96:99]
	v_mfma_f32_16x16x32_bf16 v[84:87], v[146:149], v[184:187], v[84:87]
	v_mfma_f32_16x16x32_bf16 v[80:83], v[154:157], v[184:187], v[80:83]
	v_mfma_f32_16x16x32_bf16 v[68:71], v[146:149], v[192:195], v[68:71]
	v_mfma_f32_16x16x32_bf16 v[64:67], v[154:157], v[192:195], v[64:67]
	v_mfma_f32_16x16x32_bf16 v[116:119], v[150:153], v[166:169], v[116:119]
	v_mfma_f32_16x16x32_bf16 v[112:115], v[158:161], v[166:169], v[112:115]
	v_mfma_f32_16x16x32_bf16 v[100:103], v[150:153], v[180:183], v[100:103]
	v_mfma_f32_16x16x32_bf16 v[96:99], v[158:161], v[180:183], v[96:99]
	v_mfma_f32_16x16x32_bf16 v[84:87], v[150:153], v[188:191], v[84:87]
	v_mfma_f32_16x16x32_bf16 v[80:83], v[158:161], v[188:191], v[80:83]
	v_mfma_f32_16x16x32_bf16 v[68:71], v[150:153], v[196:199], v[68:71]
	v_mfma_f32_16x16x32_bf16 v[64:67], v[158:161], v[196:199], v[64:67]
	s_setprio 0
	s_barrier
	s_add_u32 s64, s30, 0x80
	s_addc_u32 s65, s31, 0
	v_mov_b32_e32 v200, v174
	s_add_i32 s61, s61, s36
	ds_read_b128 v[162:165], v179 offset:49152
	ds_read_b128 v[166:169], v179 offset:50176
	ds_read_b128 v[170:173], v179 offset:51200
	ds_read_b128 v[180:183], v179 offset:52224
	ds_read_b128 v[184:187], v179 offset:53248
	ds_read_b128 v[188:191], v179 offset:54272
	ds_read_b128 v[192:195], v179 offset:55296
	ds_read_b128 v[196:199], v179 offset:56320
	s_mov_b32 m0, s61
	s_nop 0
	global_load_lds_dwordx4 v200, s[64:65]
	s_add_u32 s64, s30, 0x20080
	v_mov_b32_e32 v200, v174
	s_addc_u32 s65, s31, 0
	s_add_i32 m0, s61, 0x2000
	s_nop 0
	global_load_lds_dwordx4 v200, s[64:65]
	s_add_u32 s64, s30, 0x40080
	v_mov_b32_e32 v200, v174
	s_addc_u32 s65, s31, 0
	s_add_i32 s61, s68, s36
	s_mov_b32 m0, s61
	s_add_u32 s30, s30, 0x60080
	global_load_lds_dwordx4 v200, s[64:65]
	v_mov_b32_e32 v200, v174
	s_addc_u32 s31, s31, 0
	s_add_i32 m0, s61, 0x2000
	s_add_u32 s26, s26, 0x20080
	global_load_lds_dwordx4 v200, s[30:31]
	v_mov_b32_e32 v200, v175
	s_mov_b32 m0, s48
	s_addc_u32 s27, s27, 0
	global_load_lds_dwordx4 v200, s[28:29]
	v_mov_b32_e32 v200, v175
	s_mov_b32 m0, s49
	s_nop 0
	global_load_lds_dwordx4 v200, s[26:27]
	s_waitcnt vmcnt(8)
	s_waitcnt lgkmcnt(0)
	s_barrier
	s_setprio 3
	v_mfma_f32_16x16x32_bf16 v[60:63], v[130:133], v[162:165], v[60:63]
	v_mfma_f32_16x16x32_bf16 v[56:59], v[138:141], v[162:165], v[56:59]
	v_mfma_f32_16x16x32_bf16 v[44:47], v[130:133], v[170:173], v[44:47]
	v_mfma_f32_16x16x32_bf16 v[40:43], v[138:141], v[170:173], v[40:43]
	v_mfma_f32_16x16x32_bf16 v[28:31], v[130:133], v[184:187], v[28:31]
	v_mfma_f32_16x16x32_bf16 v[24:27], v[138:141], v[184:187], v[24:27]
	v_mfma_f32_16x16x32_bf16 v[12:15], v[130:133], v[192:195], v[12:15]
	v_mfma_f32_16x16x32_bf16 v[8:11], v[138:141], v[192:195], v[8:11]
	v_mfma_f32_16x16x32_bf16 v[60:63], v[134:137], v[166:169], v[60:63]
	v_mfma_f32_16x16x32_bf16 v[56:59], v[142:145], v[166:169], v[56:59]
	v_mfma_f32_16x16x32_bf16 v[44:47], v[134:137], v[180:183], v[44:47]
	v_mfma_f32_16x16x32_bf16 v[40:43], v[142:145], v[180:183], v[40:43]
	v_mfma_f32_16x16x32_bf16 v[28:31], v[134:137], v[188:191], v[28:31]
	v_mfma_f32_16x16x32_bf16 v[24:27], v[142:145], v[188:191], v[24:27]
	v_mfma_f32_16x16x32_bf16 v[12:15], v[134:137], v[196:199], v[12:15]
	v_mfma_f32_16x16x32_bf16 v[8:11], v[142:145], v[196:199], v[8:11]
	v_mfma_f32_16x16x32_bf16 v[52:55], v[146:149], v[162:165], v[52:55]
	v_mfma_f32_16x16x32_bf16 v[48:51], v[154:157], v[162:165], v[48:51]
	v_mfma_f32_16x16x32_bf16 v[36:39], v[146:149], v[170:173], v[36:39]
	v_mfma_f32_16x16x32_bf16 v[32:35], v[154:157], v[170:173], v[32:35]
	v_mfma_f32_16x16x32_bf16 v[20:23], v[146:149], v[184:187], v[20:23]
	v_mfma_f32_16x16x32_bf16 v[16:19], v[154:157], v[184:187], v[16:19]
	v_mfma_f32_16x16x32_bf16 v[4:7], v[146:149], v[192:195], v[4:7]
	v_mfma_f32_16x16x32_bf16 v[0:3], v[154:157], v[192:195], v[0:3]
	v_mfma_f32_16x16x32_bf16 v[52:55], v[150:153], v[166:169], v[52:55]
	v_mfma_f32_16x16x32_bf16 v[48:51], v[158:161], v[166:169], v[48:51]
	v_mfma_f32_16x16x32_bf16 v[36:39], v[150:153], v[180:183], v[36:39]
	v_mfma_f32_16x16x32_bf16 v[32:35], v[158:161], v[180:183], v[32:35]
	v_mfma_f32_16x16x32_bf16 v[20:23], v[150:153], v[188:191], v[20:23]
	v_mfma_f32_16x16x32_bf16 v[16:19], v[158:161], v[188:191], v[16:19]
	v_mfma_f32_16x16x32_bf16 v[4:7], v[150:153], v[196:199], v[4:7]
	v_mfma_f32_16x16x32_bf16 v[0:3], v[158:161], v[196:199], v[0:3]
	s_setprio 0
	s_barrier
	s_add_i32 s60, s60, 2
	s_add_u32 s15, s15, 0x100
	s_addc_u32 s17, s17, 0
	s_add_u32 s24, s24, 0x100
	s_addc_u32 s25, s25, 0
	s_cmp_gt_u32 s60, 13
	s_cbranch_scc0 .LBB0_725
	s_and_b64 vcc, exec, s[10:11]
	s_cbranch_vccz .LBB0_728
	s_barrier

.LBB0_1097:
	s_add_u32 s29, s78, 0x9000
	s_addc_u32 s50, s79, 0
	s_lshl_b32 s28, s4, 1
	s_min_i32 s30, s28, s33
	s_add_u32 s4, s78, 0x2500000
	s_addc_u32 s5, s79, 0
	s_add_u32 s12, s78, 0x16500000
	s_addc_u32 s13, s79, 0
	s_cmp_ge_i32 s16, s30
	s_cbranch_scc1 .LBB0_1278
	s_and_b32 s31, s18, 0xffffffc0
	v_mbcnt_lo_u32_b32 v0, -1, 0
	v_mbcnt_hi_u32_b32 v0, -1, v0
	s_ashr_i32 s34, s16, 1
	v_add_u32_e32 v0, s31, v0
	s_lshl_b32 s14, s34, 2
	v_ashrrev_i32_e32 v2, 31, v0
	v_lshrrev_b32_e32 v2, 26, v2
	v_add_u32_e32 v2, v0, v2
	v_lshlrev_b32_e32 v1, 4, v0
	v_ashrrev_i32_e32 v2, 6, v2
	v_bfe_i32 v0, v0, 27, 1
	v_lshrrev_b32_e32 v0, 22, v0
	v_lshlrev_b32_e32 v2, 3, v2
	s_add_i32 s14, s3, s14
	v_add_u32_e32 v0, v1, v0
	v_and_b32_e32 v4, -16, v2
	v_mov_b32_e32 v2, s14
	v_and_b32_e32 v0, 0xfffffc00, v0
	ds_read2_b32 v[2:3], v2 offset0:64 offset1:224
	v_sub_u32_e32 v0, v1, v0
	v_lshrrev_b32_e32 v1, 4, v0
	v_ashrrev_i32_e32 v5, 31, v0
	v_and_b32_e32 v1, 32, v1
	v_lshrrev_b32_e32 v5, 26, v5
	v_xad_u32 v0, v1, v0, v5
	v_ashrrev_i32_e32 v5, 6, v0
	s_waitcnt lgkmcnt(0)
	v_lshlrev_b32_e32 v0, 2, v2
	v_add_u32_e32 v0, s3, v0
	ds_read_b32 v11, v0 offset:4
	v_ashrrev_i32_e32 v1, 31, v2
	v_mov_b32_e32 v0, v2
	v_add3_u32 v4, v5, v4, v3
	v_lshlrev_b64 v[2:3], 16, v[0:1]
	v_lshl_add_u64 v[2:3], s[6:7], 0, v[2:3]
	s_waitcnt lgkmcnt(0)
	v_cmp_lt_i32_e32 vcc, v4, v11
	v_mov_b32_e32 v10, 0
	v_mov_b32_e32 v9, 0
	v_mov_b32_e32 v240, 0
	v_mov_b32_e32 v241, 0
	v_mov_b32_e32 v242, 0
	v_mov_b32_e32 v243, 0
	s_and_saveexec_b64 s[14:15], vcc
	s_cbranch_execz .LBB0_1100
	v_ashrrev_i32_e32 v5, 31, v4
	v_lshl_add_u64 v[6:7], v[4:5], 2, v[2:3]
	global_load_dword v240, v[6:7], off
.LBB0_1100:
	s_or_b64 exec, exec, s[14:15]
	v_add_u32_e32 v6, 0x80, v4
	v_cmp_lt_i32_e32 vcc, v6, v11
	s_and_saveexec_b64 s[14:15], vcc
	s_cbranch_execz .LBB0_1102
	v_ashrrev_i32_e32 v7, 31, v6
	v_lshl_add_u64 v[6:7], v[6:7], 2, v[2:3]
	global_load_dword v241, v[6:7], off
.LBB0_1102:
	s_or_b64 exec, exec, s[14:15]
	v_add_u32_e32 v6, 64, v4
	v_cmp_lt_i32_e32 vcc, v6, v11
	v_mov_b32_e32 v5, 0
	v_mov_b32_e32 v7, 0
	s_and_saveexec_b64 s[14:15], vcc
	s_cbranch_execz .LBB0_1104
	v_ashrrev_i32_e32 v7, 31, v6
	v_lshl_add_u64 v[6:7], v[6:7], 2, v[2:3]
	global_load_dword v242, v[6:7], off
.LBB0_1104:
	s_or_b64 exec, exec, s[14:15]
	v_add_u32_e32 v4, 0xc0, v4
	v_cmp_lt_i32_e32 vcc, v4, v11
	s_and_saveexec_b64 s[14:15], vcc
	s_cbranch_execz .LBB0_1106
	v_ashrrev_i32_e32 v5, 31, v4
	v_lshl_add_u64 v[2:3], v[4:5], 2, v[2:3]
	global_load_dword v243, v[2:3], off
.LBB0_1106:
	s_or_b64 exec, exec, s[14:15]
	s_waitcnt vmcnt(0)
	v_ashrrev_i32_e32 v9, 1, v240
	v_lshlrev_b32_e32 v241, 15, v241
	v_and_b32_e32 v10, 0xffff0000, v241
	v_ashrrev_i32_e32 v7, 1, v242
	v_lshlrev_b32_e32 v243, 15, v243
	v_and_b32_e32 v5, 0xffff0000, v243
	v_bfe_i32 v4, v8, 27, 1
	v_lshlrev_b32_e32 v2, 4, v8
	v_lshrrev_b32_e32 v4, 22, v4
	v_add_u32_e32 v4, v2, v4
	v_and_b32_e32 v4, 0xfffffc00, v4
	v_sub_u32_e32 v2, v2, v4
	v_ashrrev_i32_e32 v3, 31, v8
	v_lshrrev_b32_e32 v4, 4, v2
	v_lshrrev_b32_e32 v3, 26, v3
	v_bitop3_b32 v4, v4, v2, 32 bitop3:0x6c
	v_ashrrev_i32_e32 v2, 31, v2
	v_add_u32_e32 v3, v8, v3
	v_lshrrev_b32_e32 v2, 26, v2
	v_ashrrev_i32_e32 v3, 6, v3
	v_add_u32_e32 v2, v4, v2
	v_lshlrev_b32_e32 v6, 3, v3
	v_ashrrev_i32_e32 v2, 6, v2
	v_or_b32_e32 v128, v10, v9
	v_and_b32_e32 v6, -16, v6
	v_mul_i32_i24_e32 v10, 64, v2
	v_add_u32_e32 v6, v2, v6
	v_sub_u32_e32 v4, v4, v10
	v_mov_b32_e32 v10, 1
	s_and_b32 s64, s16, 1
	v_lshlrev_b32_e32 v3, 5, v3
	v_ashrrev_i16_sdwa v4, v10, sext(v4) dst_sel:DWORD dst_unused:UNUSED_PAD src0_sel:DWORD src1_sel:BYTE_0
	v_lshlrev_b32_e32 v10, 1, v6
	v_lshrrev_b32_e32 v11, 2, v6
	v_and_b32_e32 v2, 3, v2
	s_mov_b32 s14, 0x3fffe0
	v_lshlrev_b64 v[0:1], 19, v[0:1]
	v_and_b32_e32 v3, 32, v3
	v_bfe_i32 v4, v4, 0, 16
	v_and_b32_e32 v10, 24, v10
	v_and_b32_e32 v11, 4, v11
	v_and_or_b32 v2, v6, s14, v2
	v_lshl_add_u64 v[0:1], s[4:5], 0, v[0:1]
	s_lshl_b32 s14, s64, 18
	s_mov_b32 s15, 0
	s_ashr_i32 s19, s18, 6
	v_or3_b32 v2, v2, v11, v10
	v_add_lshl_u32 v3, v3, v4, 1
	v_lshl_add_u64 v[0:1], v[0:1], 0, s[14:15]
	v_lshl_add_u32 v134, v2, 10, v3
	s_lshl_b32 s35, s19, 10
	v_readfirstlane_b32 s23, v1
	v_readfirstlane_b32 s22, v0
	s_add_i32 s36, s35, 0
	v_mov_b32_e32 v0, v134
	s_mov_b64 s[16:17], s[22:23]
	s_ashr_i32 s20, s18, 8
	s_add_i32 m0, s36, 0x10000
	v_and_b32_e32 v135, 0x7e, v3
	global_load_lds_dwordx4 v0, s[16:17]
	s_add_u32 s16, s22, 0x10000
	v_mov_b32_e32 v0, v134
	s_addc_u32 s17, s23, 0
	s_add_i32 m0, s36, 0x12000
	s_mov_b32 s37, 0x3fffc00
	global_load_lds_dwordx4 v0, s[16:17]
	s_add_i32 m0, s36, 0x14000
	s_add_u32 s16, s22, 0x20000
	v_mov_b32_e32 v0, v134
	s_addc_u32 s17, s23, 0
	v_or_b32_e32 v129, v5, v7
	global_load_lds_dwordx4 v0, s[16:17]
	v_mov_b32_e32 v0, v134
	s_add_u32 s16, s22, 0x30000
	s_addc_u32 s17, s23, 0
	s_add_i32 m0, s36, 0x16000
	s_add_i32 s38, s36, 0x2000
	global_load_lds_dwordx4 v0, s[16:17]
	v_lshlrev_b32_e32 v0, 10, v9
	v_and_or_b32 v0, v0, s37, v135
	v_mov_b32_e32 v1, v0
	s_mov_b64 s[16:17], s[8:9]
	s_mov_b32 m0, s36
	s_add_i32 s39, s36, 0x4000
	global_load_lds_dwordx4 v1, s[16:17]
	v_lshlrev_b32_e32 v1, 10, v7
	v_and_or_b32 v1, v1, s37, v135
	v_mov_b32_e32 v2, v1
	s_mov_b64 s[16:17], s[8:9]
	s_mov_b32 m0, s38
	s_add_i32 s40, s36, 0x6000
	global_load_lds_dwordx4 v2, s[16:17]
	v_bfe_u32 v2, v128, 16, 16
	v_lshl_or_b32 v2, v2, 10, v135
	s_mov_b64 s[16:17], s[8:9]
	s_mov_b32 m0, s39
	s_cmp_eq_u32 s20, 1
	global_load_lds_dwordx4 v2, s[16:17]
	v_bfe_u32 v2, v129, 16, 16
	v_lshl_or_b32 v2, v2, 10, v135
	s_mov_b64 s[16:17], s[8:9]
	s_mov_b32 m0, s40
	s_nop 0
	global_load_lds_dwordx4 v2, s[16:17]
	s_cselect_b64 s[16:17], -1, 0
	s_cmp_lg_u32 s20, 1
	s_cbranch_scc1 .LBB0_1108
	s_barrier

.LBB0_1111:
	s_add_i32 s53, s53, 1
	s_mul_i32 s0, s53, s33
	s_add_i32 s14, s45, s0
	s_cmp_lt_i32 s14, s30
	s_cselect_b64 s[20:21], -1, 0
	s_ashr_i32 s60, s14, 1
	s_cmp_ge_i32 s14, s30
	s_cbranch_scc1 .LBB0_1121
	v_mbcnt_lo_u32_b32 v0, -1, 0
	v_mbcnt_hi_u32_b32 v0, -1, v0
	s_lshl_b32 s0, s60, 2
	v_add_u32_e32 v0, s31, v0
	s_add_i32 s0, s3, s0
	v_ashrrev_i32_e32 v2, 31, v0
	v_lshrrev_b32_e32 v2, 26, v2
	v_lshlrev_b32_e32 v1, 4, v0
	v_add_u32_e32 v2, v0, v2
	v_bfe_i32 v0, v0, 27, 1
	v_lshrrev_b32_e32 v0, 22, v0
	v_add_u32_e32 v0, v1, v0
	v_and_b32_e32 v0, 0xfffffc00, v0
	v_sub_u32_e32 v3, v1, v0
	v_ashrrev_i32_e32 v2, 6, v2
	v_lshrrev_b32_e32 v0, 4, v3
	v_and_b32_e32 v4, 32, v0
	v_lshlrev_b32_e32 v0, 3, v2
	v_and_b32_e32 v2, -16, v0
	v_mov_b32_e32 v0, s0
	ds_read2_b32 v[0:1], v0 offset0:64 offset1:224
	v_ashrrev_i32_e32 v5, 31, v3
	v_lshrrev_b32_e32 v5, 26, v5
	v_xad_u32 v3, v4, v3, v5
	v_ashrrev_i32_e32 v3, 6, v3
	s_waitcnt lgkmcnt(0)
	v_lshlrev_b32_e32 v4, 2, v0
	v_add_u32_e32 v4, s3, v4
	ds_read_b32 v8, v4 offset:4
	v_ashrrev_i32_e32 v5, 31, v0
	v_mov_b32_e32 v4, v0
	v_add3_u32 v2, v3, v2, v1
	v_lshlrev_b64 v[0:1], 16, v[4:5]
	v_lshl_add_u64 v[0:1], s[6:7], 0, v[0:1]
	s_waitcnt lgkmcnt(0)
	v_cmp_lt_i32_e32 vcc, v2, v8
	v_mov_b32_e32 v7, 0
	v_mov_b32_e32 v6, 0
	v_mov_b32_e32 v240, 0
	v_mov_b32_e32 v241, 0
	v_mov_b32_e32 v242, 0
	v_mov_b32_e32 v243, 0
	s_and_saveexec_b64 s[0:1], vcc
	s_cbranch_execz .LBB0_1114
	v_ashrrev_i32_e32 v3, 31, v2
	v_lshl_add_u64 v[4:5], v[2:3], 2, v[0:1]
	global_load_dword v240, v[4:5], off
.LBB0_1114:
	s_or_b64 exec, exec, s[0:1]
	v_add_u32_e32 v4, 0x80, v2
	v_cmp_lt_i32_e32 vcc, v4, v8
	s_and_saveexec_b64 s[0:1], vcc
	s_cbranch_execz .LBB0_1116
	v_ashrrev_i32_e32 v5, 31, v4
	v_lshl_add_u64 v[4:5], v[4:5], 2, v[0:1]
	global_load_dword v241, v[4:5], off
.LBB0_1116:
	s_or_b64 exec, exec, s[0:1]
	v_add_u32_e32 v4, 64, v2
	v_cmp_lt_i32_e32 vcc, v4, v8
	v_mov_b32_e32 v3, 0
	v_mov_b32_e32 v5, 0
	s_and_saveexec_b64 s[0:1], vcc
	s_cbranch_execz .LBB0_1118
	v_ashrrev_i32_e32 v5, 31, v4
	v_lshl_add_u64 v[4:5], v[4:5], 2, v[0:1]
	global_load_dword v242, v[4:5], off
.LBB0_1118:
	s_or_b64 exec, exec, s[0:1]
	v_add_u32_e32 v2, 0xc0, v2
	v_cmp_lt_i32_e32 vcc, v2, v8
	s_and_saveexec_b64 s[0:1], vcc
	s_cbranch_execz .LBB0_1120
	v_ashrrev_i32_e32 v3, 31, v2
	v_lshl_add_u64 v[0:1], v[2:3], 2, v[0:1]
	global_load_dword v243, v[0:1], off
.LBB0_1120:
	s_or_b64 exec, exec, s[0:1]
	s_waitcnt vmcnt(0)
	v_ashrrev_i32_e32 v6, 1, v240
	v_lshlrev_b32_e32 v241, 15, v241
	v_and_b32_e32 v7, 0xffff0000, v241
	v_ashrrev_i32_e32 v5, 1, v242
	v_lshlrev_b32_e32 v243, 15, v243
	v_and_b32_e32 v3, 0xffff0000, v243
	v_or_b32_e32 v141, v7, v6
	v_or_b32_e32 v142, v3, v5

.LBB0_1124:
	ds_read_b128 v[144:147], v137
	ds_read_b128 v[148:151], v137 offset:1024
	ds_read_b128 v[152:155], v137 offset:2048
	ds_read_b128 v[156:159], v137 offset:3072
	ds_read_b128 v[160:163], v138
	ds_read_b128 v[164:167], v138 offset:1024
	ds_read_b128 v[168:171], v138 offset:2048
	ds_read_b128 v[172:175], v138 offset:3072
	s_cmp_eq_u32 s70, 4
	s_cselect_b64 vcc, -1, 0
	s_and_b64 s[22:23], vcc, exec
	s_cselect_b32 s26, s8, s68
	s_cselect_b32 s27, s9, s69
	s_cselect_b32 s24, s20, s14
	s_cselect_b32 s25, s21, s65
	s_add_u32 s22, s26, 0x80
	s_addc_u32 s23, s27, 0
	s_add_u32 s72, s68, 0xffffff80
	s_addc_u32 s73, s69, -1
	v_mov_b32_e32 v132, v130
	s_mov_b32 m0, s49
	ds_read_b128 v[176:179], v139
	ds_read_b128 v[180:183], v139 offset:1024
	ds_read_b128 v[184:187], v139 offset:2048
	ds_read_b128 v[188:191], v139 offset:3072
	ds_read_b128 v[192:195], v139 offset:4096
	ds_read_b128 v[196:199], v139 offset:5120
	ds_read_b128 v[200:203], v139 offset:6144
	ds_read_b128 v[204:207], v139 offset:7168
	s_mov_b64 s[74:75], s[72:73]
	s_nop 0
	global_load_lds_dwordx4 v132, s[74:75]
	v_mov_b32_e32 v132, v131
	s_mov_b32 m0, s51
	s_nop 0
	global_load_lds_dwordx4 v132, s[72:73]
	s_waitcnt vmcnt(8)
	s_waitcnt lgkmcnt(0)
	s_barrier
	s_setprio 3
	v_mfma_f32_16x16x128_f8f6f4 v[124:127], v[144:151], v[176:183], v[124:127]
	v_mfma_f32_16x16x128_f8f6f4 v[116:119], v[152:159], v[176:183], v[116:119]
	v_mfma_f32_16x16x128_f8f6f4 v[108:111], v[144:151], v[184:191], v[108:111]
	v_mfma_f32_16x16x128_f8f6f4 v[100:103], v[152:159], v[184:191], v[100:103]
	v_mfma_f32_16x16x128_f8f6f4 v[92:95], v[144:151], v[192:199], v[92:95]
	v_mfma_f32_16x16x128_f8f6f4 v[84:87], v[152:159], v[192:199], v[84:87]
	v_mfma_f32_16x16x128_f8f6f4 v[76:79], v[144:151], v[200:207], v[76:79]
	v_mfma_f32_16x16x128_f8f6f4 v[68:71], v[152:159], v[200:207], v[68:71]
	v_mfma_f32_16x16x128_f8f6f4 v[120:123], v[160:167], v[176:183], v[120:123]
	v_mfma_f32_16x16x128_f8f6f4 v[112:115], v[168:175], v[176:183], v[112:115]
	v_mfma_f32_16x16x128_f8f6f4 v[104:107], v[160:167], v[184:191], v[104:107]
	v_mfma_f32_16x16x128_f8f6f4 v[96:99], v[168:175], v[184:191], v[96:99]
	v_mfma_f32_16x16x128_f8f6f4 v[88:91], v[160:167], v[192:199], v[88:91]
	v_mfma_f32_16x16x128_f8f6f4 v[80:83], v[168:175], v[192:199], v[80:83]
	v_mfma_f32_16x16x128_f8f6f4 v[72:75], v[160:167], v[200:207], v[72:75]
	v_mfma_f32_16x16x128_f8f6f4 v[64:67], v[168:175], v[200:207], v[64:67]
	s_setprio 0
	s_barrier
	v_mov_b32_e32 v132, v134
	s_mov_b64 s[72:73], s[24:25]
	s_mov_b32 m0, s52
	ds_read_b128 v[176:179], v139 offset:16384
	ds_read_b128 v[180:183], v139 offset:17408
	ds_read_b128 v[184:187], v139 offset:18432
	ds_read_b128 v[188:191], v139 offset:19456
	ds_read_b128 v[192:195], v139 offset:20480
	ds_read_b128 v[196:199], v139 offset:21504
	ds_read_b128 v[200:203], v139 offset:22528
	ds_read_b128 v[204:207], v139 offset:23552
	s_nop 0
	global_load_lds_dwordx4 v132, s[72:73]
	s_add_u32 s72, s24, 0x10000
	v_mov_b32_e32 v132, v134
	s_addc_u32 s73, s25, 0
	s_add_i32 m0, s52, 0x2000
	s_nop 0
	global_load_lds_dwordx4 v132, s[72:73]
	s_add_u32 s72, s24, 0x20000
	v_mov_b32_e32 v132, v134
	s_addc_u32 s73, s25, 0
	s_add_i32 s71, s48, s35
	s_mov_b32 m0, s71
	s_nop 0
	global_load_lds_dwordx4 v132, s[72:73]
	v_mov_b32_e32 v132, v134
	s_add_u32 s72, s24, 0x30000
	s_addc_u32 s73, s25, 0
	s_add_i32 m0, s71, 0x2000
	s_nop 0
	global_load_lds_dwordx4 v132, s[72:73]
	v_cndmask_b32_e32 v132, v128, v141, vcc
	v_lshlrev_b32_e32 v133, 10, v132
	v_and_or_b32 v133, v133, s37, v135
	v_mov_b32_e32 v143, v133
	s_mov_b64 s[72:73], s[26:27]
	s_mov_b32 m0, s36
	s_nop 0
	global_load_lds_dwordx4 v143, s[72:73]
	v_cndmask_b32_e32 v143, v129, v142, vcc
	v_lshlrev_b32_e32 v208, 10, v143
	v_and_or_b32 v208, v208, s37, v135
	v_mov_b32_e32 v209, v208
	s_mov_b64 s[72:73], s[26:27]
	s_mov_b32 m0, s38
	s_nop 0
	global_load_lds_dwordx4 v209, s[72:73]
	s_waitcnt vmcnt(8)
	s_waitcnt lgkmcnt(0)
	s_barrier
	s_setprio 3
	v_mfma_f32_16x16x128_f8f6f4 v[60:63], v[144:151], v[176:183], v[60:63]
	v_mfma_f32_16x16x128_f8f6f4 v[52:55], v[152:159], v[176:183], v[52:55]
	v_mfma_f32_16x16x128_f8f6f4 v[44:47], v[144:151], v[184:191], v[44:47]
	v_mfma_f32_16x16x128_f8f6f4 v[36:39], v[152:159], v[184:191], v[36:39]
	v_mfma_f32_16x16x128_f8f6f4 v[28:31], v[144:151], v[192:199], v[28:31]
	v_mfma_f32_16x16x128_f8f6f4 v[20:23], v[152:159], v[192:199], v[20:23]
	v_mfma_f32_16x16x128_f8f6f4 v[12:15], v[144:151], v[200:207], v[12:15]
	v_mfma_f32_16x16x128_f8f6f4 v[4:7], v[152:159], v[200:207], v[4:7]
	v_mfma_f32_16x16x128_f8f6f4 v[56:59], v[160:167], v[176:183], v[56:59]
	v_mfma_f32_16x16x128_f8f6f4 v[48:51], v[168:175], v[176:183], v[48:51]
	v_mfma_f32_16x16x128_f8f6f4 v[40:43], v[160:167], v[184:191], v[40:43]
	v_mfma_f32_16x16x128_f8f6f4 v[32:35], v[168:175], v[184:191], v[32:35]
	v_mfma_f32_16x16x128_f8f6f4 v[24:27], v[160:167], v[192:199], v[24:27]
	v_mfma_f32_16x16x128_f8f6f4 v[16:19], v[168:175], v[192:199], v[16:19]
	v_mfma_f32_16x16x128_f8f6f4 v[8:11], v[160:167], v[200:207], v[8:11]
	v_mfma_f32_16x16x128_f8f6f4 v[0:3], v[168:175], v[200:207], v[0:3]
	s_setprio 0
	s_barrier
	s_add_i32 s71, 0, 0x18000
	s_add_i32 s74, 0, 0x1c000
	v_add_u32_e32 v156, s71, v136
	v_add_u32_e32 v172, s74, v136
	ds_read_b128 v[144:147], v156
	ds_read_b128 v[148:151], v156 offset:1024
	ds_read_b128 v[152:155], v156 offset:2048
	ds_read_b128 v[156:159], v156 offset:3072
	ds_read_b128 v[160:163], v172
	ds_read_b128 v[164:167], v172 offset:1024
	ds_read_b128 v[168:171], v172 offset:2048
	ds_read_b128 v[172:175], v172 offset:3072
	v_bfe_u32 v132, v132, 16, 16
	v_lshl_or_b32 v132, v132, 10, v135
	s_mov_b32 m0, s39
	ds_read_b128 v[176:179], v139 offset:32768
	ds_read_b128 v[180:183], v139 offset:33792
	ds_read_b128 v[184:187], v139 offset:34816
	ds_read_b128 v[188:191], v139 offset:35840
	ds_read_b128 v[192:195], v139 offset:36864
	ds_read_b128 v[196:199], v139 offset:37888
	ds_read_b128 v[200:203], v139 offset:38912
	ds_read_b128 v[204:207], v139 offset:39936
	s_mov_b64 s[72:73], s[26:27]
	s_nop 0
	global_load_lds_dwordx4 v132, s[72:73]
	v_bfe_u32 v132, v143, 16, 16
	v_lshl_or_b32 v132, v132, 10, v135
	s_mov_b32 m0, s40
	s_nop 0
	global_load_lds_dwordx4 v132, s[26:27]
	s_waitcnt vmcnt(8)
	s_waitcnt lgkmcnt(0)
	s_barrier
	s_setprio 3
	v_mfma_f32_16x16x128_f8f6f4 v[124:127], v[144:151], v[176:183], v[124:127]
	v_mfma_f32_16x16x128_f8f6f4 v[116:119], v[152:159], v[176:183], v[116:119]
	v_mfma_f32_16x16x128_f8f6f4 v[108:111], v[144:151], v[184:191], v[108:111]
	v_mfma_f32_16x16x128_f8f6f4 v[100:103], v[152:159], v[184:191], v[100:103]
	v_mfma_f32_16x16x128_f8f6f4 v[92:95], v[144:151], v[192:199], v[92:95]
	v_mfma_f32_16x16x128_f8f6f4 v[84:87], v[152:159], v[192:199], v[84:87]
	v_mfma_f32_16x16x128_f8f6f4 v[76:79], v[144:151], v[200:207], v[76:79]
	v_mfma_f32_16x16x128_f8f6f4 v[68:71], v[152:159], v[200:207], v[68:71]
	v_mfma_f32_16x16x128_f8f6f4 v[120:123], v[160:167], v[176:183], v[120:123]
	v_mfma_f32_16x16x128_f8f6f4 v[112:115], v[168:175], v[176:183], v[112:115]
	v_mfma_f32_16x16x128_f8f6f4 v[104:107], v[160:167], v[184:191], v[104:107]
	v_mfma_f32_16x16x128_f8f6f4 v[96:99], v[168:175], v[184:191], v[96:99]
	v_mfma_f32_16x16x128_f8f6f4 v[88:91], v[160:167], v[192:199], v[88:91]
	v_mfma_f32_16x16x128_f8f6f4 v[80:83], v[168:175], v[192:199], v[80:83]
	v_mfma_f32_16x16x128_f8f6f4 v[72:75], v[160:167], v[200:207], v[72:75]
	v_mfma_f32_16x16x128_f8f6f4 v[64:67], v[168:175], v[200:207], v[64:67]
	s_setprio 0
	s_barrier
	s_add_u32 s26, s24, 0x80
	s_addc_u32 s27, s25, 0
	v_mov_b32_e32 v132, v134
	s_add_i32 s71, s71, s35
	ds_read_b128 v[176:179], v139 offset:49152
	ds_read_b128 v[180:183], v139 offset:50176
	ds_read_b128 v[184:187], v139 offset:51200
	ds_read_b128 v[188:191], v139 offset:52224
	ds_read_b128 v[192:195], v139 offset:53248
	ds_read_b128 v[196:199], v139 offset:54272
	ds_read_b128 v[200:203], v139 offset:55296
	ds_read_b128 v[204:207], v139 offset:56320
	s_mov_b32 m0, s71
	s_nop 0
	global_load_lds_dwordx4 v132, s[26:27]
	s_add_u32 s26, s24, 0x10080
	v_mov_b32_e32 v132, v134
	s_addc_u32 s27, s25, 0
	s_add_i32 m0, s71, 0x2000
	s_nop 0
	global_load_lds_dwordx4 v132, s[26:27]
	s_add_u32 s26, s24, 0x20080
	v_mov_b32_e32 v132, v134
	s_addc_u32 s27, s25, 0
	s_add_i32 s71, s74, s35
	s_mov_b32 m0, s71
	s_add_u32 s24, s24, 0x30080
	s_addc_u32 s25, s25, 0
	global_load_lds_dwordx4 v132, s[26:27]
	v_mov_b32_e32 v132, v134
	s_add_i32 m0, s71, 0x2000
	s_nop 0
	global_load_lds_dwordx4 v132, s[24:25]
	s_mov_b64 s[24:25], s[22:23]
	s_mov_b32 m0, s43
	s_nop 0
	global_load_lds_dwordx4 v133, s[24:25]
	s_mov_b32 m0, s44
	s_nop 0
	global_load_lds_dwordx4 v208, s[22:23]
	s_waitcnt vmcnt(8)
	s_waitcnt lgkmcnt(0)
	s_barrier
	s_setprio 3
	v_mfma_f32_16x16x128_f8f6f4 v[60:63], v[144:151], v[176:183], v[60:63]
	v_mfma_f32_16x16x128_f8f6f4 v[52:55], v[152:159], v[176:183], v[52:55]
	v_mfma_f32_16x16x128_f8f6f4 v[44:47], v[144:151], v[184:191], v[44:47]
	v_mfma_f32_16x16x128_f8f6f4 v[36:39], v[152:159], v[184:191], v[36:39]
	v_mfma_f32_16x16x128_f8f6f4 v[28:31], v[144:151], v[192:199], v[28:31]
	v_mfma_f32_16x16x128_f8f6f4 v[20:23], v[152:159], v[192:199], v[20:23]
	v_mfma_f32_16x16x128_f8f6f4 v[12:15], v[144:151], v[200:207], v[12:15]
	v_mfma_f32_16x16x128_f8f6f4 v[4:7], v[152:159], v[200:207], v[4:7]
	v_mfma_f32_16x16x128_f8f6f4 v[56:59], v[160:167], v[176:183], v[56:59]
	v_mfma_f32_16x16x128_f8f6f4 v[48:51], v[168:175], v[176:183], v[48:51]
	v_mfma_f32_16x16x128_f8f6f4 v[40:43], v[160:167], v[184:191], v[40:43]
	v_mfma_f32_16x16x128_f8f6f4 v[32:35], v[168:175], v[184:191], v[32:35]
	v_mfma_f32_16x16x128_f8f6f4 v[24:27], v[160:167], v[192:199], v[24:27]
	v_mfma_f32_16x16x128_f8f6f4 v[16:19], v[168:175], v[192:199], v[16:19]
	v_mfma_f32_16x16x128_f8f6f4 v[8:11], v[160:167], v[200:207], v[8:11]
	v_mfma_f32_16x16x128_f8f6f4 v[0:3], v[168:175], v[200:207], v[0:3]
	s_setprio 0
	s_barrier
	s_add_i32 s70, s70, 2
	s_add_u32 s14, s14, 0x100
	s_addc_u32 s65, s65, 0
	s_add_u32 s68, s68, 0x100
	s_addc_u32 s69, s69, 0
	s_cmp_gt_u32 s70, 5
	s_cbranch_scc0 .LBB0_1124
	s_and_b64 vcc, exec, s[18:19]
	s_cbranch_vccz .LBB0_1127
	s_barrier
.LBB0_1127:
	s_mov_b32 s14, 0
	s_lshl_b32 s14, s34, 2
	s_add_i32 s14, s3, s14
	v_mbcnt_lo_u32_b32 v146, -1, 0
	v_mbcnt_hi_u32_b32 v146, -1, v146
	v_mov_b32_e32 v128, s14
	ds_read2_b32 v[128:129], v128 offset0:64 offset1:224
	v_and_b32_e32 v143, 15, v146
	v_or_b32_e32 v144, s41, v143
	v_mov_b32_e32 v147, 0
	s_waitcnt lgkmcnt(0)
	v_lshlrev_b32_e32 v130, 2, v128
	v_add_u32_e32 v130, s3, v130
	ds_read_b32 v145, v130 offset:4
	v_ashrrev_i32_e32 v133, 31, v128
	v_mov_b32_e32 v132, v128
	v_add_u32_e32 v130, v129, v144
	v_lshlrev_b64 v[132:133], 16, v[132:133]
	s_waitcnt lgkmcnt(0)
	v_cmp_lt_i32_e32 vcc, v130, v145
	v_mov_b32_e32 v128, 0
	v_lshl_add_u64 v[132:133], s[10:11], 0, v[132:133]
	v_ashrrev_i32_e32 v131, 31, v130
	v_readlane_b32 s72, v249, 55
	v_readlane_b32 s73, v249, 56
	v_readlane_b32 s74, v249, 57
	v_readlane_b32 s75, v249, 58
	v_readlane_b32 s76, v249, 59
	v_readlane_b32 s77, v249, 60
	v_readlane_b32 s78, v249, 61
	v_readlane_b32 s79, v249, 62
	v_bfe_u32 v148, v146, 4, 2
	s_lshl_b32 s14, s64, 7
	v_lshl_add_u64 v[152:153], v[130:131], 2, v[132:133]
	v_lshl_or_b32 v149, v148, 3, s14
	global_load_dword v154, v[152:153], off
	global_load_dword v155, v[152:153], off offset:64
	global_load_dword v156, v[152:153], off offset:128
	global_load_dword v157, v[152:153], off offset:192
	global_load_dword v158, v[152:153], off offset:512
	global_load_dword v159, v[152:153], off offset:576
	global_load_dword v160, v[152:153], off offset:640
	global_load_dword v161, v[152:153], off offset:704
	s_lshl_b32 s14, s34, 8
	v_or_b32_e32 v149, s42, v149
	v_add_u32_e32 v150, s14, v144
	v_lshl_add_u32 v150, v150, 8, v149
	v_cmp_lt_i32_e32 vcc, v130, v145
	s_waitcnt vmcnt(7)
	v_mul_f32_e32 v163, 0x3c800000, v154
	v_mul_f32_e32 v164, 0xbd38aa3b, v124
	v_mul_f32_e32 v165, 0xbd38aa3b, v125
	v_mul_f32_e32 v166, 0xbd38aa3b, v126
	v_mul_f32_e32 v167, 0xbd38aa3b, v127
	v_mul_f32_e32 v168, 0xbd38aa3b, v116
	v_mul_f32_e32 v169, 0xbd38aa3b, v117
	v_mul_f32_e32 v170, 0xbd38aa3b, v118
	v_mul_f32_e32 v171, 0xbd38aa3b, v119
	v_exp_f32_e32 v164, v164
	v_exp_f32_e32 v165, v165
	v_exp_f32_e32 v166, v166
	v_exp_f32_e32 v167, v167
	v_exp_f32_e32 v168, v168
	v_exp_f32_e32 v169, v169
	v_exp_f32_e32 v170, v170
	v_exp_f32_e32 v171, v171
	v_add_f32_e32 v164, 1.0, v164
	v_add_f32_e32 v165, 1.0, v165
	v_add_f32_e32 v166, 1.0, v166
	v_add_f32_e32 v167, 1.0, v167
	v_add_f32_e32 v168, 1.0, v168
	v_add_f32_e32 v169, 1.0, v169
	v_add_f32_e32 v170, 1.0, v170
	v_add_f32_e32 v171, 1.0, v171
	v_rcp_f32_e32 v164, v164
	v_rcp_f32_e32 v165, v165
	v_rcp_f32_e32 v166, v166
	v_rcp_f32_e32 v167, v167
	v_rcp_f32_e32 v168, v168
	v_rcp_f32_e32 v169, v169
	v_rcp_f32_e32 v170, v170
	v_rcp_f32_e32 v171, v171
	v_mul_f32_e32 v164, v124, v164
	v_mul_f32_e32 v165, v125, v165
	v_mul_f32_e32 v166, v126, v166
	v_mul_f32_e32 v167, v127, v167
	v_mul_f32_e32 v168, v116, v168
	v_mul_f32_e32 v169, v117, v169
	v_mul_f32_e32 v170, v118, v170
	v_mul_f32_e32 v171, v119, v171
	v_mul_f32_e32 v164, v164, v120
	v_mul_f32_e32 v165, v165, v121
	v_mul_f32_e32 v166, v166, v122
	v_mul_f32_e32 v167, v167, v123
	v_mul_f32_e32 v168, v168, v112
	v_mul_f32_e32 v169, v169, v113
	v_mul_f32_e32 v170, v170, v114
	v_mul_f32_e32 v171, v171, v115
	v_mul_f32_e32 v164, v164, v163
	v_mul_f32_e32 v165, v165, v163
	v_mul_f32_e32 v166, v166, v163
	v_mul_f32_e32 v167, v167, v163
	v_mul_f32_e32 v168, v168, v163
	v_mul_f32_e32 v169, v169, v163
	v_mul_f32_e32 v170, v170, v163
	v_mul_f32_e32 v171, v171, v163
	v_max_f32_e32 v164, 0xc3e00000, v164
	v_max_f32_e32 v165, 0xc3e00000, v165
	v_max_f32_e32 v166, 0xc3e00000, v166
	v_max_f32_e32 v167, 0xc3e00000, v167
	v_max_f32_e32 v168, 0xc3e00000, v168
	v_max_f32_e32 v169, 0xc3e00000, v169
	v_max_f32_e32 v170, 0xc3e00000, v170
	v_max_f32_e32 v171, 0xc3e00000, v171
	v_min_f32_e32 v164, 0x43e00000, v164
	v_min_f32_e32 v165, 0x43e00000, v165
	v_min_f32_e32 v166, 0x43e00000, v166
	v_min_f32_e32 v167, 0x43e00000, v167
	v_min_f32_e32 v168, 0x43e00000, v168
	v_min_f32_e32 v169, 0x43e00000, v169
	v_min_f32_e32 v170, 0x43e00000, v170
	v_min_f32_e32 v171, 0x43e00000, v171
	v_cndmask_b32_e32 v164, 0, v164, vcc
	v_cndmask_b32_e32 v165, 0, v165, vcc
	v_cndmask_b32_e32 v166, 0, v166, vcc
	v_cndmask_b32_e32 v167, 0, v167, vcc
	v_cndmask_b32_e32 v168, 0, v168, vcc
	v_cndmask_b32_e32 v169, 0, v169, vcc
	v_cndmask_b32_e32 v170, 0, v170, vcc
	v_cndmask_b32_e32 v171, 0, v171, vcc
	v_mov_b32_e32 v188, 0
	v_mov_b32_e32 v189, 0
	v_cvt_pk_fp8_f32 v188, v164, v165
	v_cvt_pk_fp8_f32 v189, v168, v169
	v_mov_b32_e32 v192, v150
	v_cvt_pk_fp8_f32 v188, v166, v167 op_sel:[0,0,1]
	v_cvt_pk_fp8_f32 v189, v170, v171 op_sel:[0,0,1]
	s_nop 1
	global_store_dwordx2 v192, v[188:189], s[12:13] sc1
	v_add_u32_e32 v162, 0x10, v130
	v_cmp_lt_i32_e32 vcc, v162, v145
	s_waitcnt vmcnt(7)
	v_mul_f32_e32 v163, 0x3c800000, v155
	v_mul_f32_e32 v164, 0xbd38aa3b, v108
	v_mul_f32_e32 v165, 0xbd38aa3b, v109
	v_mul_f32_e32 v166, 0xbd38aa3b, v110
	v_mul_f32_e32 v167, 0xbd38aa3b, v111
	v_mul_f32_e32 v168, 0xbd38aa3b, v100
	v_mul_f32_e32 v169, 0xbd38aa3b, v101
	v_mul_f32_e32 v170, 0xbd38aa3b, v102
	v_mul_f32_e32 v171, 0xbd38aa3b, v103
	v_exp_f32_e32 v164, v164
	v_exp_f32_e32 v165, v165
	v_exp_f32_e32 v166, v166
	v_exp_f32_e32 v167, v167
	v_exp_f32_e32 v168, v168
	v_exp_f32_e32 v169, v169
	v_exp_f32_e32 v170, v170
	v_exp_f32_e32 v171, v171
	v_add_f32_e32 v164, 1.0, v164
	v_add_f32_e32 v165, 1.0, v165
	v_add_f32_e32 v166, 1.0, v166
	v_add_f32_e32 v167, 1.0, v167
	v_add_f32_e32 v168, 1.0, v168
	v_add_f32_e32 v169, 1.0, v169
	v_add_f32_e32 v170, 1.0, v170
	v_add_f32_e32 v171, 1.0, v171
	v_rcp_f32_e32 v164, v164
	v_rcp_f32_e32 v165, v165
	v_rcp_f32_e32 v166, v166
	v_rcp_f32_e32 v167, v167
	v_rcp_f32_e32 v168, v168
	v_rcp_f32_e32 v169, v169
	v_rcp_f32_e32 v170, v170
	v_rcp_f32_e32 v171, v171
	v_mul_f32_e32 v164, v108, v164
	v_mul_f32_e32 v165, v109, v165
	v_mul_f32_e32 v166, v110, v166
	v_mul_f32_e32 v167, v111, v167
	v_mul_f32_e32 v168, v100, v168
	v_mul_f32_e32 v169, v101, v169
	v_mul_f32_e32 v170, v102, v170
	v_mul_f32_e32 v171, v103, v171
	v_mul_f32_e32 v164, v164, v104
	v_mul_f32_e32 v165, v165, v105
	v_mul_f32_e32 v166, v166, v106
	v_mul_f32_e32 v167, v167, v107
	v_mul_f32_e32 v168, v168, v96
	v_mul_f32_e32 v169, v169, v97
	v_mul_f32_e32 v170, v170, v98
	v_mul_f32_e32 v171, v171, v99
	v_mul_f32_e32 v164, v164, v163
	v_mul_f32_e32 v165, v165, v163
	v_mul_f32_e32 v166, v166, v163
	v_mul_f32_e32 v167, v167, v163
	v_mul_f32_e32 v168, v168, v163
	v_mul_f32_e32 v169, v169, v163
	v_mul_f32_e32 v170, v170, v163
	v_mul_f32_e32 v171, v171, v163
	v_max_f32_e32 v164, 0xc3e00000, v164
	v_max_f32_e32 v165, 0xc3e00000, v165
	v_max_f32_e32 v166, 0xc3e00000, v166
	v_max_f32_e32 v167, 0xc3e00000, v167
	v_max_f32_e32 v168, 0xc3e00000, v168
	v_max_f32_e32 v169, 0xc3e00000, v169
	v_max_f32_e32 v170, 0xc3e00000, v170
	v_max_f32_e32 v171, 0xc3e00000, v171
	v_min_f32_e32 v164, 0x43e00000, v164
	v_min_f32_e32 v165, 0x43e00000, v165
	v_min_f32_e32 v166, 0x43e00000, v166
	v_min_f32_e32 v167, 0x43e00000, v167
	v_min_f32_e32 v168, 0x43e00000, v168
	v_min_f32_e32 v169, 0x43e00000, v169
	v_min_f32_e32 v170, 0x43e00000, v170
	v_min_f32_e32 v171, 0x43e00000, v171
	v_cndmask_b32_e32 v164, 0, v164, vcc
	v_cndmask_b32_e32 v165, 0, v165, vcc
	v_cndmask_b32_e32 v166, 0, v166, vcc
	v_cndmask_b32_e32 v167, 0, v167, vcc
	v_cndmask_b32_e32 v168, 0, v168, vcc
	v_cndmask_b32_e32 v169, 0, v169, vcc
	v_cndmask_b32_e32 v170, 0, v170, vcc
	v_cndmask_b32_e32 v171, 0, v171, vcc
	v_mov_b32_e32 v190, 0
	v_mov_b32_e32 v191, 0
	v_cvt_pk_fp8_f32 v190, v164, v165
	v_cvt_pk_fp8_f32 v191, v168, v169
	v_add_u32_e32 v192, 0x1000, v150
	v_cvt_pk_fp8_f32 v190, v166, v167 op_sel:[0,0,1]
	v_cvt_pk_fp8_f32 v191, v170, v171 op_sel:[0,0,1]
	s_nop 1
	global_store_dwordx2 v192, v[190:191], s[12:13] sc1
	v_add_u32_e32 v162, 0x20, v130
	v_cmp_lt_i32_e32 vcc, v162, v145
	s_waitcnt vmcnt(7)
	v_mul_f32_e32 v163, 0x3c800000, v156
	v_mul_f32_e32 v164, 0xbd38aa3b, v92
	v_mul_f32_e32 v165, 0xbd38aa3b, v93
	v_mul_f32_e32 v166, 0xbd38aa3b, v94
	v_mul_f32_e32 v167, 0xbd38aa3b, v95
	v_mul_f32_e32 v168, 0xbd38aa3b, v84
	v_mul_f32_e32 v169, 0xbd38aa3b, v85
	v_mul_f32_e32 v170, 0xbd38aa3b, v86
	v_mul_f32_e32 v171, 0xbd38aa3b, v87
	v_exp_f32_e32 v164, v164
	v_exp_f32_e32 v165, v165
	v_exp_f32_e32 v166, v166
	v_exp_f32_e32 v167, v167
	v_exp_f32_e32 v168, v168
	v_exp_f32_e32 v169, v169
	v_exp_f32_e32 v170, v170
	v_exp_f32_e32 v171, v171
	v_add_f32_e32 v164, 1.0, v164
	v_add_f32_e32 v165, 1.0, v165
	v_add_f32_e32 v166, 1.0, v166
	v_add_f32_e32 v167, 1.0, v167
	v_add_f32_e32 v168, 1.0, v168
	v_add_f32_e32 v169, 1.0, v169
	v_add_f32_e32 v170, 1.0, v170
	v_add_f32_e32 v171, 1.0, v171
	v_rcp_f32_e32 v164, v164
	v_rcp_f32_e32 v165, v165
	v_rcp_f32_e32 v166, v166
	v_rcp_f32_e32 v167, v167
	v_rcp_f32_e32 v168, v168
	v_rcp_f32_e32 v169, v169
	v_rcp_f32_e32 v170, v170
	v_rcp_f32_e32 v171, v171
	v_mul_f32_e32 v164, v92, v164
	v_mul_f32_e32 v165, v93, v165
	v_mul_f32_e32 v166, v94, v166
	v_mul_f32_e32 v167, v95, v167
	v_mul_f32_e32 v168, v84, v168
	v_mul_f32_e32 v169, v85, v169
	v_mul_f32_e32 v170, v86, v170
	v_mul_f32_e32 v171, v87, v171
	v_mul_f32_e32 v164, v164, v88
	v_mul_f32_e32 v165, v165, v89
	v_mul_f32_e32 v166, v166, v90
	v_mul_f32_e32 v167, v167, v91
	v_mul_f32_e32 v168, v168, v80
	v_mul_f32_e32 v169, v169, v81
	v_mul_f32_e32 v170, v170, v82
	v_mul_f32_e32 v171, v171, v83
	v_mul_f32_e32 v164, v164, v163
	v_mul_f32_e32 v165, v165, v163
	v_mul_f32_e32 v166, v166, v163
	v_mul_f32_e32 v167, v167, v163
	v_mul_f32_e32 v168, v168, v163
	v_mul_f32_e32 v169, v169, v163
	v_mul_f32_e32 v170, v170, v163
	v_mul_f32_e32 v171, v171, v163
	v_max_f32_e32 v164, 0xc3e00000, v164
	v_max_f32_e32 v165, 0xc3e00000, v165
	v_max_f32_e32 v166, 0xc3e00000, v166
	v_max_f32_e32 v167, 0xc3e00000, v167
	v_max_f32_e32 v168, 0xc3e00000, v168
	v_max_f32_e32 v169, 0xc3e00000, v169
	v_max_f32_e32 v170, 0xc3e00000, v170
	v_max_f32_e32 v171, 0xc3e00000, v171
	v_min_f32_e32 v164, 0x43e00000, v164
	v_min_f32_e32 v165, 0x43e00000, v165
	v_min_f32_e32 v166, 0x43e00000, v166
	v_min_f32_e32 v167, 0x43e00000, v167
	v_min_f32_e32 v168, 0x43e00000, v168
	v_min_f32_e32 v169, 0x43e00000, v169
	v_min_f32_e32 v170, 0x43e00000, v170
	v_min_f32_e32 v171, 0x43e00000, v171
	v_cndmask_b32_e32 v164, 0, v164, vcc
	v_cndmask_b32_e32 v165, 0, v165, vcc
	v_cndmask_b32_e32 v166, 0, v166, vcc
	v_cndmask_b32_e32 v167, 0, v167, vcc
	v_cndmask_b32_e32 v168, 0, v168, vcc
	v_cndmask_b32_e32 v169, 0, v169, vcc
	v_cndmask_b32_e32 v170, 0, v170, vcc
	v_cndmask_b32_e32 v171, 0, v171, vcc
	v_mov_b32_e32 v188, 0
	v_mov_b32_e32 v189, 0
	v_cvt_pk_fp8_f32 v188, v164, v165
	v_cvt_pk_fp8_f32 v189, v168, v169
	v_add_u32_e32 v192, 0x2000, v150
	v_cvt_pk_fp8_f32 v188, v166, v167 op_sel:[0,0,1]
	v_cvt_pk_fp8_f32 v189, v170, v171 op_sel:[0,0,1]
	s_nop 1
	global_store_dwordx2 v192, v[188:189], s[12:13] sc1
	v_add_u32_e32 v162, 0x30, v130
	v_cmp_lt_i32_e32 vcc, v162, v145
	s_waitcnt vmcnt(7)
	v_mul_f32_e32 v163, 0x3c800000, v157
	v_mul_f32_e32 v164, 0xbd38aa3b, v76
	v_mul_f32_e32 v165, 0xbd38aa3b, v77
	v_mul_f32_e32 v166, 0xbd38aa3b, v78
	v_mul_f32_e32 v167, 0xbd38aa3b, v79
	v_mul_f32_e32 v168, 0xbd38aa3b, v68
	v_mul_f32_e32 v169, 0xbd38aa3b, v69
	v_mul_f32_e32 v170, 0xbd38aa3b, v70
	v_mul_f32_e32 v171, 0xbd38aa3b, v71
	v_exp_f32_e32 v164, v164
	v_exp_f32_e32 v165, v165
	v_exp_f32_e32 v166, v166
	v_exp_f32_e32 v167, v167
	v_exp_f32_e32 v168, v168
	v_exp_f32_e32 v169, v169
	v_exp_f32_e32 v170, v170
	v_exp_f32_e32 v171, v171
	v_add_f32_e32 v164, 1.0, v164
	v_add_f32_e32 v165, 1.0, v165
	v_add_f32_e32 v166, 1.0, v166
	v_add_f32_e32 v167, 1.0, v167
	v_add_f32_e32 v168, 1.0, v168
	v_add_f32_e32 v169, 1.0, v169
	v_add_f32_e32 v170, 1.0, v170
	v_add_f32_e32 v171, 1.0, v171
	v_rcp_f32_e32 v164, v164
	v_rcp_f32_e32 v165, v165
	v_rcp_f32_e32 v166, v166
	v_rcp_f32_e32 v167, v167
	v_rcp_f32_e32 v168, v168
	v_rcp_f32_e32 v169, v169
	v_rcp_f32_e32 v170, v170
	v_rcp_f32_e32 v171, v171
	v_mul_f32_e32 v164, v76, v164
	v_mul_f32_e32 v165, v77, v165
	v_mul_f32_e32 v166, v78, v166
	v_mul_f32_e32 v167, v79, v167
	v_mul_f32_e32 v168, v68, v168
	v_mul_f32_e32 v169, v69, v169
	v_mul_f32_e32 v170, v70, v170
	v_mul_f32_e32 v171, v71, v171
	v_mul_f32_e32 v164, v164, v72
	v_mul_f32_e32 v165, v165, v73
	v_mul_f32_e32 v166, v166, v74
	v_mul_f32_e32 v167, v167, v75
	v_mul_f32_e32 v168, v168, v64
	v_mul_f32_e32 v169, v169, v65
	v_mul_f32_e32 v170, v170, v66
	v_mul_f32_e32 v171, v171, v67
	v_mul_f32_e32 v164, v164, v163
	v_mul_f32_e32 v165, v165, v163
	v_mul_f32_e32 v166, v166, v163
	v_mul_f32_e32 v167, v167, v163
	v_mul_f32_e32 v168, v168, v163
	v_mul_f32_e32 v169, v169, v163
	v_mul_f32_e32 v170, v170, v163
	v_mul_f32_e32 v171, v171, v163
	v_max_f32_e32 v164, 0xc3e00000, v164
	v_max_f32_e32 v165, 0xc3e00000, v165
	v_max_f32_e32 v166, 0xc3e00000, v166
	v_max_f32_e32 v167, 0xc3e00000, v167
	v_max_f32_e32 v168, 0xc3e00000, v168
	v_max_f32_e32 v169, 0xc3e00000, v169
	v_max_f32_e32 v170, 0xc3e00000, v170
	v_max_f32_e32 v171, 0xc3e00000, v171
	v_min_f32_e32 v164, 0x43e00000, v164
	v_min_f32_e32 v165, 0x43e00000, v165
	v_min_f32_e32 v166, 0x43e00000, v166
	v_min_f32_e32 v167, 0x43e00000, v167
	v_min_f32_e32 v168, 0x43e00000, v168
	v_min_f32_e32 v169, 0x43e00000, v169
	v_min_f32_e32 v170, 0x43e00000, v170
	v_min_f32_e32 v171, 0x43e00000, v171
	v_cndmask_b32_e32 v164, 0, v164, vcc
	v_cndmask_b32_e32 v165, 0, v165, vcc
	v_cndmask_b32_e32 v166, 0, v166, vcc
	v_cndmask_b32_e32 v167, 0, v167, vcc
	v_cndmask_b32_e32 v168, 0, v168, vcc
	v_cndmask_b32_e32 v169, 0, v169, vcc
	v_cndmask_b32_e32 v170, 0, v170, vcc
	v_cndmask_b32_e32 v171, 0, v171, vcc
	v_mov_b32_e32 v190, 0
	v_mov_b32_e32 v191, 0
	v_cvt_pk_fp8_f32 v190, v164, v165
	v_cvt_pk_fp8_f32 v191, v168, v169
	v_add_u32_e32 v192, 0x3000, v150
	v_cvt_pk_fp8_f32 v190, v166, v167 op_sel:[0,0,1]
	v_cvt_pk_fp8_f32 v191, v170, v171 op_sel:[0,0,1]
	s_nop 1
	global_store_dwordx2 v192, v[190:191], s[12:13] sc1
	v_add_u32_e32 v162, 0x80, v130
	v_cmp_lt_i32_e32 vcc, v162, v145
	s_waitcnt vmcnt(7)
	v_mul_f32_e32 v163, 0x3c800000, v158
	v_mul_f32_e32 v164, 0xbd38aa3b, v60
	v_mul_f32_e32 v165, 0xbd38aa3b, v61
	v_mul_f32_e32 v166, 0xbd38aa3b, v62
	v_mul_f32_e32 v167, 0xbd38aa3b, v63
	v_mul_f32_e32 v168, 0xbd38aa3b, v52
	v_mul_f32_e32 v169, 0xbd38aa3b, v53
	v_mul_f32_e32 v170, 0xbd38aa3b, v54
	v_mul_f32_e32 v171, 0xbd38aa3b, v55
	v_exp_f32_e32 v164, v164
	v_exp_f32_e32 v165, v165
	v_exp_f32_e32 v166, v166
	v_exp_f32_e32 v167, v167
	v_exp_f32_e32 v168, v168
	v_exp_f32_e32 v169, v169
	v_exp_f32_e32 v170, v170
	v_exp_f32_e32 v171, v171
	v_add_f32_e32 v164, 1.0, v164
	v_add_f32_e32 v165, 1.0, v165
	v_add_f32_e32 v166, 1.0, v166
	v_add_f32_e32 v167, 1.0, v167
	v_add_f32_e32 v168, 1.0, v168
	v_add_f32_e32 v169, 1.0, v169
	v_add_f32_e32 v170, 1.0, v170
	v_add_f32_e32 v171, 1.0, v171
	v_rcp_f32_e32 v164, v164
	v_rcp_f32_e32 v165, v165
	v_rcp_f32_e32 v166, v166
	v_rcp_f32_e32 v167, v167
	v_rcp_f32_e32 v168, v168
	v_rcp_f32_e32 v169, v169
	v_rcp_f32_e32 v170, v170
	v_rcp_f32_e32 v171, v171
	v_mul_f32_e32 v164, v60, v164
	v_mul_f32_e32 v165, v61, v165
	v_mul_f32_e32 v166, v62, v166
	v_mul_f32_e32 v167, v63, v167
	v_mul_f32_e32 v168, v52, v168
	v_mul_f32_e32 v169, v53, v169
	v_mul_f32_e32 v170, v54, v170
	v_mul_f32_e32 v171, v55, v171
	v_mul_f32_e32 v164, v164, v56
	v_mul_f32_e32 v165, v165, v57
	v_mul_f32_e32 v166, v166, v58
	v_mul_f32_e32 v167, v167, v59
	v_mul_f32_e32 v168, v168, v48
	v_mul_f32_e32 v169, v169, v49
	v_mul_f32_e32 v170, v170, v50
	v_mul_f32_e32 v171, v171, v51
	v_mul_f32_e32 v164, v164, v163
	v_mul_f32_e32 v165, v165, v163
	v_mul_f32_e32 v166, v166, v163
	v_mul_f32_e32 v167, v167, v163
	v_mul_f32_e32 v168, v168, v163
	v_mul_f32_e32 v169, v169, v163
	v_mul_f32_e32 v170, v170, v163
	v_mul_f32_e32 v171, v171, v163
	v_max_f32_e32 v164, 0xc3e00000, v164
	v_max_f32_e32 v165, 0xc3e00000, v165
	v_max_f32_e32 v166, 0xc3e00000, v166
	v_max_f32_e32 v167, 0xc3e00000, v167
	v_max_f32_e32 v168, 0xc3e00000, v168
	v_max_f32_e32 v169, 0xc3e00000, v169
	v_max_f32_e32 v170, 0xc3e00000, v170
	v_max_f32_e32 v171, 0xc3e00000, v171
	v_min_f32_e32 v164, 0x43e00000, v164
	v_min_f32_e32 v165, 0x43e00000, v165
	v_min_f32_e32 v166, 0x43e00000, v166
	v_min_f32_e32 v167, 0x43e00000, v167
	v_min_f32_e32 v168, 0x43e00000, v168
	v_min_f32_e32 v169, 0x43e00000, v169
	v_min_f32_e32 v170, 0x43e00000, v170
	v_min_f32_e32 v171, 0x43e00000, v171
	v_cndmask_b32_e32 v164, 0, v164, vcc
	v_cndmask_b32_e32 v165, 0, v165, vcc
	v_cndmask_b32_e32 v166, 0, v166, vcc
	v_cndmask_b32_e32 v167, 0, v167, vcc
	v_cndmask_b32_e32 v168, 0, v168, vcc
	v_cndmask_b32_e32 v169, 0, v169, vcc
	v_cndmask_b32_e32 v170, 0, v170, vcc
	v_cndmask_b32_e32 v171, 0, v171, vcc
	v_mov_b32_e32 v188, 0
	v_mov_b32_e32 v189, 0
	v_cvt_pk_fp8_f32 v188, v164, v165
	v_cvt_pk_fp8_f32 v189, v168, v169
	v_add_u32_e32 v192, 0x8000, v150
	v_cvt_pk_fp8_f32 v188, v166, v167 op_sel:[0,0,1]
	v_cvt_pk_fp8_f32 v189, v170, v171 op_sel:[0,0,1]
	s_nop 1
	global_store_dwordx2 v192, v[188:189], s[12:13] sc1
	v_add_u32_e32 v162, 0x90, v130
	v_cmp_lt_i32_e32 vcc, v162, v145
	s_waitcnt vmcnt(7)
	v_mul_f32_e32 v163, 0x3c800000, v159
	v_mul_f32_e32 v164, 0xbd38aa3b, v44
	v_mul_f32_e32 v165, 0xbd38aa3b, v45
	v_mul_f32_e32 v166, 0xbd38aa3b, v46
	v_mul_f32_e32 v167, 0xbd38aa3b, v47
	v_mul_f32_e32 v168, 0xbd38aa3b, v36
	v_mul_f32_e32 v169, 0xbd38aa3b, v37
	v_mul_f32_e32 v170, 0xbd38aa3b, v38
	v_mul_f32_e32 v171, 0xbd38aa3b, v39
	v_exp_f32_e32 v164, v164
	v_exp_f32_e32 v165, v165
	v_exp_f32_e32 v166, v166
	v_exp_f32_e32 v167, v167
	v_exp_f32_e32 v168, v168
	v_exp_f32_e32 v169, v169
	v_exp_f32_e32 v170, v170
	v_exp_f32_e32 v171, v171
	v_add_f32_e32 v164, 1.0, v164
	v_add_f32_e32 v165, 1.0, v165
	v_add_f32_e32 v166, 1.0, v166
	v_add_f32_e32 v167, 1.0, v167
	v_add_f32_e32 v168, 1.0, v168
	v_add_f32_e32 v169, 1.0, v169
	v_add_f32_e32 v170, 1.0, v170
	v_add_f32_e32 v171, 1.0, v171
	v_rcp_f32_e32 v164, v164
	v_rcp_f32_e32 v165, v165
	v_rcp_f32_e32 v166, v166
	v_rcp_f32_e32 v167, v167
	v_rcp_f32_e32 v168, v168
	v_rcp_f32_e32 v169, v169
	v_rcp_f32_e32 v170, v170
	v_rcp_f32_e32 v171, v171
	v_mul_f32_e32 v164, v44, v164
	v_mul_f32_e32 v165, v45, v165
	v_mul_f32_e32 v166, v46, v166
	v_mul_f32_e32 v167, v47, v167
	v_mul_f32_e32 v168, v36, v168
	v_mul_f32_e32 v169, v37, v169
	v_mul_f32_e32 v170, v38, v170
	v_mul_f32_e32 v171, v39, v171
	v_mul_f32_e32 v164, v164, v40
	v_mul_f32_e32 v165, v165, v41
	v_mul_f32_e32 v166, v166, v42
	v_mul_f32_e32 v167, v167, v43
	v_mul_f32_e32 v168, v168, v32
	v_mul_f32_e32 v169, v169, v33
	v_mul_f32_e32 v170, v170, v34
	v_mul_f32_e32 v171, v171, v35
	v_mul_f32_e32 v164, v164, v163
	v_mul_f32_e32 v165, v165, v163
	v_mul_f32_e32 v166, v166, v163
	v_mul_f32_e32 v167, v167, v163
	v_mul_f32_e32 v168, v168, v163
	v_mul_f32_e32 v169, v169, v163
	v_mul_f32_e32 v170, v170, v163
	v_mul_f32_e32 v171, v171, v163
	v_max_f32_e32 v164, 0xc3e00000, v164
	v_max_f32_e32 v165, 0xc3e00000, v165
	v_max_f32_e32 v166, 0xc3e00000, v166
	v_max_f32_e32 v167, 0xc3e00000, v167
	v_max_f32_e32 v168, 0xc3e00000, v168
	v_max_f32_e32 v169, 0xc3e00000, v169
	v_max_f32_e32 v170, 0xc3e00000, v170
	v_max_f32_e32 v171, 0xc3e00000, v171
	v_min_f32_e32 v164, 0x43e00000, v164
	v_min_f32_e32 v165, 0x43e00000, v165
	v_min_f32_e32 v166, 0x43e00000, v166
	v_min_f32_e32 v167, 0x43e00000, v167
	v_min_f32_e32 v168, 0x43e00000, v168
	v_min_f32_e32 v169, 0x43e00000, v169
	v_min_f32_e32 v170, 0x43e00000, v170
	v_min_f32_e32 v171, 0x43e00000, v171
	v_cndmask_b32_e32 v164, 0, v164, vcc
	v_cndmask_b32_e32 v165, 0, v165, vcc
	v_cndmask_b32_e32 v166, 0, v166, vcc
	v_cndmask_b32_e32 v167, 0, v167, vcc
	v_cndmask_b32_e32 v168, 0, v168, vcc
	v_cndmask_b32_e32 v169, 0, v169, vcc
	v_cndmask_b32_e32 v170, 0, v170, vcc
	v_cndmask_b32_e32 v171, 0, v171, vcc
	v_mov_b32_e32 v190, 0
	v_mov_b32_e32 v191, 0
	v_cvt_pk_fp8_f32 v190, v164, v165
	v_cvt_pk_fp8_f32 v191, v168, v169
	v_add_u32_e32 v192, 0x9000, v150
	v_cvt_pk_fp8_f32 v190, v166, v167 op_sel:[0,0,1]
	v_cvt_pk_fp8_f32 v191, v170, v171 op_sel:[0,0,1]
	s_nop 1
	global_store_dwordx2 v192, v[190:191], s[12:13] sc1
	v_add_u32_e32 v162, 0xa0, v130
	v_cmp_lt_i32_e32 vcc, v162, v145
	s_waitcnt vmcnt(7)
	v_mul_f32_e32 v163, 0x3c800000, v160
	v_mul_f32_e32 v164, 0xbd38aa3b, v28
	v_mul_f32_e32 v165, 0xbd38aa3b, v29
	v_mul_f32_e32 v166, 0xbd38aa3b, v30
	v_mul_f32_e32 v167, 0xbd38aa3b, v31
	v_mul_f32_e32 v168, 0xbd38aa3b, v20
	v_mul_f32_e32 v169, 0xbd38aa3b, v21
	v_mul_f32_e32 v170, 0xbd38aa3b, v22
	v_mul_f32_e32 v171, 0xbd38aa3b, v23
	v_exp_f32_e32 v164, v164
	v_exp_f32_e32 v165, v165
	v_exp_f32_e32 v166, v166
	v_exp_f32_e32 v167, v167
	v_exp_f32_e32 v168, v168
	v_exp_f32_e32 v169, v169
	v_exp_f32_e32 v170, v170
	v_exp_f32_e32 v171, v171
	v_add_f32_e32 v164, 1.0, v164
	v_add_f32_e32 v165, 1.0, v165
	v_add_f32_e32 v166, 1.0, v166
	v_add_f32_e32 v167, 1.0, v167
	v_add_f32_e32 v168, 1.0, v168
	v_add_f32_e32 v169, 1.0, v169
	v_add_f32_e32 v170, 1.0, v170
	v_add_f32_e32 v171, 1.0, v171
	v_rcp_f32_e32 v164, v164
	v_rcp_f32_e32 v165, v165
	v_rcp_f32_e32 v166, v166
	v_rcp_f32_e32 v167, v167
	v_rcp_f32_e32 v168, v168
	v_rcp_f32_e32 v169, v169
	v_rcp_f32_e32 v170, v170
	v_rcp_f32_e32 v171, v171
	v_mul_f32_e32 v164, v28, v164
	v_mul_f32_e32 v165, v29, v165
	v_mul_f32_e32 v166, v30, v166
	v_mul_f32_e32 v167, v31, v167
	v_mul_f32_e32 v168, v20, v168
	v_mul_f32_e32 v169, v21, v169
	v_mul_f32_e32 v170, v22, v170
	v_mul_f32_e32 v171, v23, v171
	v_mul_f32_e32 v164, v164, v24
	v_mul_f32_e32 v165, v165, v25
	v_mul_f32_e32 v166, v166, v26
	v_mul_f32_e32 v167, v167, v27
	v_mul_f32_e32 v168, v168, v16
	v_mul_f32_e32 v169, v169, v17
	v_mul_f32_e32 v170, v170, v18
	v_mul_f32_e32 v171, v171, v19
	v_mul_f32_e32 v164, v164, v163
	v_mul_f32_e32 v165, v165, v163
	v_mul_f32_e32 v166, v166, v163
	v_mul_f32_e32 v167, v167, v163
	v_mul_f32_e32 v168, v168, v163
	v_mul_f32_e32 v169, v169, v163
	v_mul_f32_e32 v170, v170, v163
	v_mul_f32_e32 v171, v171, v163
	v_max_f32_e32 v164, 0xc3e00000, v164
	v_max_f32_e32 v165, 0xc3e00000, v165
	v_max_f32_e32 v166, 0xc3e00000, v166
	v_max_f32_e32 v167, 0xc3e00000, v167
	v_max_f32_e32 v168, 0xc3e00000, v168
	v_max_f32_e32 v169, 0xc3e00000, v169
	v_max_f32_e32 v170, 0xc3e00000, v170
	v_max_f32_e32 v171, 0xc3e00000, v171
	v_min_f32_e32 v164, 0x43e00000, v164
	v_min_f32_e32 v165, 0x43e00000, v165
	v_min_f32_e32 v166, 0x43e00000, v166
	v_min_f32_e32 v167, 0x43e00000, v167
	v_min_f32_e32 v168, 0x43e00000, v168
	v_min_f32_e32 v169, 0x43e00000, v169
	v_min_f32_e32 v170, 0x43e00000, v170
	v_min_f32_e32 v171, 0x43e00000, v171
	v_cndmask_b32_e32 v164, 0, v164, vcc
	v_cndmask_b32_e32 v165, 0, v165, vcc
	v_cndmask_b32_e32 v166, 0, v166, vcc
	v_cndmask_b32_e32 v167, 0, v167, vcc
	v_cndmask_b32_e32 v168, 0, v168, vcc
	v_cndmask_b32_e32 v169, 0, v169, vcc
	v_cndmask_b32_e32 v170, 0, v170, vcc
	v_cndmask_b32_e32 v171, 0, v171, vcc
	v_mov_b32_e32 v188, 0
	v_mov_b32_e32 v189, 0
	v_cvt_pk_fp8_f32 v188, v164, v165
	v_cvt_pk_fp8_f32 v189, v168, v169
	v_add_u32_e32 v192, 0xa000, v150
	v_cvt_pk_fp8_f32 v188, v166, v167 op_sel:[0,0,1]
	v_cvt_pk_fp8_f32 v189, v170, v171 op_sel:[0,0,1]
	s_nop 1
	global_store_dwordx2 v192, v[188:189], s[12:13] sc1
	v_add_u32_e32 v162, 0xb0, v130
	v_cmp_lt_i32_e32 vcc, v162, v145
	s_waitcnt vmcnt(7)
	v_mul_f32_e32 v163, 0x3c800000, v161
	v_mul_f32_e32 v164, 0xbd38aa3b, v12
	v_mul_f32_e32 v165, 0xbd38aa3b, v13
	v_mul_f32_e32 v166, 0xbd38aa3b, v14
	v_mul_f32_e32 v167, 0xbd38aa3b, v15
	v_mul_f32_e32 v168, 0xbd38aa3b, v4
	v_mul_f32_e32 v169, 0xbd38aa3b, v5
	v_mul_f32_e32 v170, 0xbd38aa3b, v6
	v_mul_f32_e32 v171, 0xbd38aa3b, v7
	v_exp_f32_e32 v164, v164
	v_exp_f32_e32 v165, v165
	v_exp_f32_e32 v166, v166
	v_exp_f32_e32 v167, v167
	v_exp_f32_e32 v168, v168
	v_exp_f32_e32 v169, v169
	v_exp_f32_e32 v170, v170
	v_exp_f32_e32 v171, v171
	v_add_f32_e32 v164, 1.0, v164
	v_add_f32_e32 v165, 1.0, v165
	v_add_f32_e32 v166, 1.0, v166
	v_add_f32_e32 v167, 1.0, v167
	v_add_f32_e32 v168, 1.0, v168
	v_add_f32_e32 v169, 1.0, v169
	v_add_f32_e32 v170, 1.0, v170
	v_add_f32_e32 v171, 1.0, v171
	v_rcp_f32_e32 v164, v164
	v_rcp_f32_e32 v165, v165
	v_rcp_f32_e32 v166, v166
	v_rcp_f32_e32 v167, v167
	v_rcp_f32_e32 v168, v168
	v_rcp_f32_e32 v169, v169
	v_rcp_f32_e32 v170, v170
	v_rcp_f32_e32 v171, v171
	v_mul_f32_e32 v164, v12, v164
	v_mul_f32_e32 v165, v13, v165
	v_mul_f32_e32 v166, v14, v166
	v_mul_f32_e32 v167, v15, v167
	v_mul_f32_e32 v168, v4, v168
	v_mul_f32_e32 v169, v5, v169
	v_mul_f32_e32 v170, v6, v170
	v_mul_f32_e32 v171, v7, v171
	v_mul_f32_e32 v164, v164, v8
	v_mul_f32_e32 v165, v165, v9
	v_mul_f32_e32 v166, v166, v10
	v_mul_f32_e32 v167, v167, v11
	v_mul_f32_e32 v168, v168, v0
	v_mul_f32_e32 v169, v169, v1
	v_mul_f32_e32 v170, v170, v2
	v_mul_f32_e32 v171, v171, v3
	v_mul_f32_e32 v164, v164, v163
	v_mul_f32_e32 v165, v165, v163
	v_mul_f32_e32 v166, v166, v163
	v_mul_f32_e32 v167, v167, v163
	v_mul_f32_e32 v168, v168, v163
	v_mul_f32_e32 v169, v169, v163
	v_mul_f32_e32 v170, v170, v163
	v_mul_f32_e32 v171, v171, v163
	v_max_f32_e32 v164, 0xc3e00000, v164
	v_max_f32_e32 v165, 0xc3e00000, v165
	v_max_f32_e32 v166, 0xc3e00000, v166
	v_max_f32_e32 v167, 0xc3e00000, v167
	v_max_f32_e32 v168, 0xc3e00000, v168
	v_max_f32_e32 v169, 0xc3e00000, v169
	v_max_f32_e32 v170, 0xc3e00000, v170
	v_max_f32_e32 v171, 0xc3e00000, v171
	v_min_f32_e32 v164, 0x43e00000, v164
	v_min_f32_e32 v165, 0x43e00000, v165
	v_min_f32_e32 v166, 0x43e00000, v166
	v_min_f32_e32 v167, 0x43e00000, v167
	v_min_f32_e32 v168, 0x43e00000, v168
	v_min_f32_e32 v169, 0x43e00000, v169
	v_min_f32_e32 v170, 0x43e00000, v170
	v_min_f32_e32 v171, 0x43e00000, v171
	v_cndmask_b32_e32 v164, 0, v164, vcc
	v_cndmask_b32_e32 v165, 0, v165, vcc
	v_cndmask_b32_e32 v166, 0, v166, vcc
	v_cndmask_b32_e32 v167, 0, v167, vcc
	v_cndmask_b32_e32 v168, 0, v168, vcc
	v_cndmask_b32_e32 v169, 0, v169, vcc
	v_cndmask_b32_e32 v170, 0, v170, vcc
	v_cndmask_b32_e32 v171, 0, v171, vcc
	v_mov_b32_e32 v190, 0
	v_mov_b32_e32 v191, 0
	v_cvt_pk_fp8_f32 v190, v164, v165
	v_cvt_pk_fp8_f32 v191, v168, v169
	v_add_u32_e32 v192, 0xb000, v150
	v_cvt_pk_fp8_f32 v190, v166, v167 op_sel:[0,0,1]
	v_cvt_pk_fp8_f32 v191, v170, v171 op_sel:[0,0,1]
	s_nop 1
	global_store_dwordx2 v192, v[190:191], s[12:13] sc1
	v_bfe_u32 v114, v146, 4, 2
	s_waitcnt vmcnt(0)
	v_or_b32_e32 v0, v114, v143
	v_cmp_eq_u32_e32 vcc, 0, v0
	s_and_saveexec_b64 s[22:23], vcc
	s_cbranch_execz .LBB0_1274
	s_mov_b64 s[24:25], exec
	v_mbcnt_lo_u32_b32 v0, s24, 0
	v_mbcnt_hi_u32_b32 v0, s25, v0
	v_cmp_eq_u32_e32 vcc, 0, v0
	s_and_b64 s[26:27], exec, vcc
	s_mov_b64 exec, s[26:27]
	s_cbranch_execz .LBB0_1274
	s_lshl_b32 s26, s34, 5
	s_ashr_i32 s27, s26, 31
	s_lshl_b64 s[26:27], s[26:27], 2
	s_add_u32 s26, s29, s26
	s_addc_u32 s27, s50, s27
	s_bcnt1_i32_b64 s14, s[24:25]
	s_lshl_b32 s14, s14, 1
	v_mov_b32_e32 v0, s14
	global_atomic_add v140, v0, s[26:27]

.LBB0_1286:
	ds_read_b128 v[72:75], v67
	ds_read_b128 v[76:79], v67 offset:1024
	ds_read_b128 v[80:83], v67 offset:2048
	ds_read_b128 v[84:87], v67 offset:3072
	ds_read_b128 v[88:91], v68
	ds_read_b128 v[92:95], v68 offset:1024
	ds_read_b128 v[96:99], v68 offset:2048
	ds_read_b128 v[100:103], v68 offset:3072
	s_cmp_eq_u32 s37, 4
	s_cselect_b32 s16, s8, s35
	s_cselect_b32 s17, s9, s36
	s_cselect_b32 s14, s0, s31
	s_cselect_b32 s15, s1, s34
	s_add_u32 s4, s16, 0x80
	s_addc_u32 s5, s17, 0
	ds_read_b128 v[104:107], v69
	ds_read_b128 v[108:111], v69 offset:1024
	ds_read_b128 v[112:115], v69 offset:2048
	ds_read_b128 v[116:119], v69 offset:3072
	ds_read_b128 v[120:123], v69 offset:4096
	ds_read_b128 v[124:127], v69 offset:5120
	ds_read_b128 v[128:131], v69 offset:6144
	ds_read_b128 v[132:135], v69 offset:7168
	s_waitcnt vmcnt(6)
	s_waitcnt lgkmcnt(0)
	s_barrier
	s_setprio 3
	v_mfma_f32_16x16x128_f8f6f4 v[60:63], v[72:79], v[104:111], v[60:63]
	v_mfma_f32_16x16x128_f8f6f4 v[52:55], v[80:87], v[104:111], v[52:55]
	v_mfma_f32_16x16x128_f8f6f4 v[44:47], v[72:79], v[112:119], v[44:47]
	v_mfma_f32_16x16x128_f8f6f4 v[36:39], v[80:87], v[112:119], v[36:39]
	v_mfma_f32_16x16x128_f8f6f4 v[28:31], v[72:79], v[120:127], v[28:31]
	v_mfma_f32_16x16x128_f8f6f4 v[20:23], v[80:87], v[120:127], v[20:23]
	v_mfma_f32_16x16x128_f8f6f4 v[12:15], v[72:79], v[128:135], v[12:15]
	v_mfma_f32_16x16x128_f8f6f4 v[136:139], v[80:87], v[128:135], v[4:7]
	v_mfma_f32_16x16x128_f8f6f4 v[56:59], v[88:95], v[104:111], v[56:59]
	v_mfma_f32_16x16x128_f8f6f4 v[48:51], v[96:103], v[104:111], v[48:51]
	v_mfma_f32_16x16x128_f8f6f4 v[40:43], v[88:95], v[112:119], v[40:43]
	v_mfma_f32_16x16x128_f8f6f4 v[32:35], v[96:103], v[112:119], v[32:35]
	v_mfma_f32_16x16x128_f8f6f4 v[24:27], v[88:95], v[120:127], v[24:27]
	v_mfma_f32_16x16x128_f8f6f4 v[16:19], v[96:103], v[120:127], v[16:19]
	v_mfma_f32_16x16x128_f8f6f4 v[8:11], v[88:95], v[128:135], v[8:11]
	v_mfma_f32_16x16x128_f8f6f4 v[128:131], v[96:103], v[128:135], v[0:3]
	s_setprio 0
	s_barrier
	s_nop 4
	v_mov_b32_e32 v0, v64
	s_mov_b64 s[48:49], s[14:15]
	s_mov_b32 m0, s38
	s_nop 0
	global_load_lds_dwordx4 v0, s[48:49]
	s_add_u32 s48, s14, 0x10000
	v_mov_b32_e32 v0, v64
	s_addc_u32 s49, s15, 0
	s_mov_b32 m0, s39
	s_nop 0
	global_load_lds_dwordx4 v0, s[48:49]
	s_add_u32 s48, s14, 0x20000
	v_mov_b32_e32 v0, v64
	s_addc_u32 s49, s15, 0
	s_mov_b32 m0, s40
	s_nop 0
	global_load_lds_dwordx4 v0, s[48:49]
	v_mov_b32_e32 v0, v64
	s_add_u32 s48, s14, 0x30000
	s_addc_u32 s49, s15, 0
	s_mov_b32 m0, s41
	s_nop 0
	global_load_lds_dwordx4 v0, s[48:49]
	v_mov_b32_e32 v0, v65
	s_mov_b64 s[48:49], s[16:17]
	s_mov_b32 m0, s23
	s_nop 0
	global_load_lds_dwordx4 v0, s[48:49]
	v_mov_b32_e32 v0, v66
	s_mov_b32 m0, s25
	s_nop 0
	global_load_lds_dwordx4 v0, s[16:17]
	s_waitcnt vmcnt(6)
	s_waitcnt lgkmcnt(0)
	s_barrier
	s_barrier
	ds_read_b128 v[0:3], v70
	ds_read_b128 v[4:7], v70 offset:1024
	ds_read_b128 v[72:75], v70 offset:2048
	ds_read_b128 v[76:79], v70 offset:3072
	ds_read_b128 v[80:83], v71
	ds_read_b128 v[84:87], v71 offset:1024
	ds_read_b128 v[88:91], v71 offset:2048
	ds_read_b128 v[92:95], v71 offset:3072
	ds_read_b128 v[96:99], v69 offset:32768
	ds_read_b128 v[100:103], v69 offset:33792
	ds_read_b128 v[104:107], v69 offset:34816
	ds_read_b128 v[108:111], v69 offset:35840
	ds_read_b128 v[112:115], v69 offset:36864
	ds_read_b128 v[116:119], v69 offset:37888
	ds_read_b128 v[120:123], v69 offset:38912
	ds_read_b128 v[124:127], v69 offset:39936
	s_waitcnt vmcnt(6)
	s_waitcnt lgkmcnt(0)
	s_barrier
	s_setprio 3
	v_mfma_f32_16x16x128_f8f6f4 v[60:63], v[0:7], v[96:103], v[60:63]
	v_mfma_f32_16x16x128_f8f6f4 v[52:55], v[72:79], v[96:103], v[52:55]
	v_mfma_f32_16x16x128_f8f6f4 v[44:47], v[0:7], v[104:111], v[44:47]
	v_mfma_f32_16x16x128_f8f6f4 v[36:39], v[72:79], v[104:111], v[36:39]
	v_mfma_f32_16x16x128_f8f6f4 v[28:31], v[0:7], v[112:119], v[28:31]
	v_mfma_f32_16x16x128_f8f6f4 v[20:23], v[72:79], v[112:119], v[20:23]
	v_mfma_f32_16x16x128_f8f6f4 v[12:15], v[0:7], v[120:127], v[12:15]
	v_mfma_f32_16x16x128_f8f6f4 v[4:7], v[72:79], v[120:127], v[136:139]
	v_mfma_f32_16x16x128_f8f6f4 v[56:59], v[80:87], v[96:103], v[56:59]
	s_add_u32 s16, s14, 0x80
	s_addc_u32 s17, s15, 0
	v_mfma_f32_16x16x128_f8f6f4 v[48:51], v[88:95], v[96:103], v[48:51]
	v_mfma_f32_16x16x128_f8f6f4 v[40:43], v[80:87], v[104:111], v[40:43]
	v_mfma_f32_16x16x128_f8f6f4 v[32:35], v[88:95], v[104:111], v[32:35]
	v_mfma_f32_16x16x128_f8f6f4 v[24:27], v[80:87], v[112:119], v[24:27]
	v_mfma_f32_16x16x128_f8f6f4 v[16:19], v[88:95], v[112:119], v[16:19]
	v_mfma_f32_16x16x128_f8f6f4 v[8:11], v[80:87], v[120:127], v[8:11]
	v_mfma_f32_16x16x128_f8f6f4 v[0:3], v[88:95], v[120:127], v[128:131]
	s_setprio 0
	s_barrier
	v_mov_b32_e32 v72, v64
	s_mov_b32 m0, s42
	s_nop 0
	global_load_lds_dwordx4 v72, s[16:17]
	s_add_u32 s16, s14, 0x10080
	v_mov_b32_e32 v72, v64
	s_addc_u32 s17, s15, 0
	s_mov_b32 m0, s43
	s_nop 0
	global_load_lds_dwordx4 v72, s[16:17]
	v_mov_b32_e32 v72, v64
	s_add_u32 s16, s14, 0x20080
	s_addc_u32 s17, s15, 0
	s_mov_b32 m0, s44
	s_add_u32 s14, s14, 0x30080
	global_load_lds_dwordx4 v72, s[16:17]
	v_mov_b32_e32 v72, v64
	s_addc_u32 s15, s15, 0
	s_mov_b32 m0, s45
	s_nop 0
	global_load_lds_dwordx4 v72, s[14:15]
	v_mov_b32_e32 v72, v65
	s_mov_b64 s[14:15], s[4:5]
	s_mov_b32 m0, s26
	s_nop 0
	global_load_lds_dwordx4 v72, s[14:15]
	v_mov_b32_e32 v72, v66
	s_mov_b32 m0, s27
	s_nop 0
	global_load_lds_dwordx4 v72, s[4:5]
	s_waitcnt vmcnt(6)
	s_waitcnt lgkmcnt(0)
	s_barrier
	s_barrier
	s_add_i32 s37, s37, 2
	s_add_u32 s31, s31, 0x100
	s_addc_u32 s34, s34, 0
	s_add_u32 s35, s35, 0x100
	s_addc_u32 s36, s36, 0
	s_cmp_gt_u32 s37, 5
	s_cbranch_scc0 .LBB0_1286
	s_cmpk_lt_u32 s22, 0x100
	s_cbranch_scc0 .LBB0_1289
	s_barrier

.LBB0_1402:
	s_waitcnt vmcnt(0)
	ds_read_b128 v[56:59], v197
	ds_read_b128 v[60:63], v197 offset:1024
	ds_read_b128 v[80:83], v197 offset:2048
	ds_read_b128 v[84:87], v197 offset:3072
	ds_read_b128 v[0:3], v198
	ds_read_b128 v[4:7], v198 offset:1024
	ds_read_b128 v[8:11], v198 offset:2048
	ds_read_b128 v[12:15], v198 offset:3072
	s_add_u32 s44, s36, 0x80
	s_addc_u32 s45, s37, 0
	s_add_u32 s48, s16, 0x80
	s_addc_u32 s49, s17, 0
	s_add_u32 s78, s42, 0x8080
	v_mov_b32_e32 v16, v195
	s_addc_u32 s79, s43, 0
	s_add_i32 m0, s52, 0xc000
	ds_read_b128 v[64:67], v199
	ds_read_b128 v[68:71], v199 offset:1024
	ds_read_b128 v[72:75], v199 offset:2048
	ds_read_b128 v[76:79], v199 offset:3072
	ds_read_b128 v[88:91], v199 offset:4096
	ds_read_b128 v[92:95], v199 offset:5120
	ds_read_b128 v[96:99], v199 offset:6144
	ds_read_b128 v[100:103], v199 offset:7168
	s_add_u32 s42, s42, 0xc080
	s_addc_u32 s43, s43, 0
	global_load_lds_dwordx4 v16, s[78:79] sc1
	v_mov_b32_e32 v16, v195
	s_add_i32 m0, s52, 0xe000
	s_nop 0
	global_load_lds_dwordx4 v16, s[42:43] sc1
	s_waitcnt vmcnt(8)
	s_waitcnt lgkmcnt(0)
	s_barrier
	s_setprio 3
	v_mfma_f32_16x16x128_f8f6f4 v[16:19], v[56:63], v[64:71], 0
	v_mfma_f32_16x16x128_f8f6f4 v[20:23], v[80:87], v[64:71], 0
	v_mfma_f32_16x16x128_f8f6f4 v[24:27], v[56:63], v[72:79], 0
	v_mfma_f32_16x16x128_f8f6f4 v[28:31], v[80:87], v[72:79], 0
	v_mfma_f32_16x16x128_f8f6f4 v[32:35], v[56:63], v[88:95], 0
	v_mfma_f32_16x16x128_f8f6f4 v[36:39], v[80:87], v[88:95], 0
	v_mfma_f32_16x16x128_f8f6f4 v[40:43], v[56:63], v[96:103], 0
	v_mfma_f32_16x16x128_f8f6f4 v[44:47], v[80:87], v[96:103], 0
	v_mfma_f32_16x16x128_f8f6f4 v[48:51], v[0:7], v[64:71], 0
	v_mfma_f32_16x16x128_f8f6f4 v[52:55], v[8:15], v[64:71], 0
	v_mfma_f32_16x16x128_f8f6f4 v[64:67], v[0:7], v[72:79], 0
	v_mfma_f32_16x16x128_f8f6f4 v[68:71], v[8:15], v[72:79], 0
	v_mfma_f32_16x16x128_f8f6f4 v[72:75], v[0:7], v[88:95], 0
	v_mfma_f32_16x16x128_f8f6f4 v[76:79], v[8:15], v[88:95], 0
	v_mfma_f32_16x16x128_f8f6f4 v[128:131], v[0:7], v[96:103], 0
	v_mfma_f32_16x16x128_f8f6f4 v[132:135], v[8:15], v[96:103], 0
	s_setprio 0
	s_barrier
	v_mov_b32_e32 v120, v194
	s_mov_b64 s[42:43], s[16:17]
	s_add_i32 s21, s73, s51
	ds_read_b128 v[88:91], v199 offset:16384
	ds_read_b128 v[92:95], v199 offset:17408
	ds_read_b128 v[96:99], v199 offset:18432
	ds_read_b128 v[100:103], v199 offset:19456
	ds_read_b128 v[104:107], v199 offset:20480
	ds_read_b128 v[108:111], v199 offset:21504
	ds_read_b128 v[112:115], v199 offset:22528
	ds_read_b128 v[116:119], v199 offset:23552
	s_mov_b32 m0, s21
	s_nop 0
	global_load_lds_dwordx4 v120, s[42:43]
	s_add_u32 s42, s16, 0x4000
	v_mov_b32_e32 v120, v194
	s_addc_u32 s43, s17, 0
	s_add_i32 m0, s21, 0x2000
	s_nop 0
	global_load_lds_dwordx4 v120, s[42:43]
	s_add_u32 s42, s16, 0x8000
	v_mov_b32_e32 v120, v194
	s_addc_u32 s43, s17, 0
	s_add_i32 s21, s74, s51
	s_mov_b32 m0, s21
	s_nop 0
	global_load_lds_dwordx4 v120, s[42:43]
	s_add_u32 s42, s16, 0xc000
	v_mov_b32_e32 v120, v194
	s_addc_u32 s43, s17, 0
	s_add_i32 m0, s21, 0x2000
	s_nop 0
	global_load_lds_dwordx4 v120, s[42:43]
	v_mov_b32_e32 v120, v195
	s_mov_b64 s[42:43], s[36:37]
	s_mov_b32 m0, s52
	s_nop 0
	global_load_lds_dwordx4 v120, s[42:43] sc1
	s_add_u32 s42, s36, 0x4000
	v_mov_b32_e32 v120, v195
	s_addc_u32 s43, s37, 0
	s_mov_b32 m0, s53
	s_nop 0
	global_load_lds_dwordx4 v120, s[42:43] sc1
	s_waitcnt vmcnt(8)
	s_waitcnt lgkmcnt(0)
	s_barrier
	s_setprio 3
	v_mfma_f32_16x16x128_f8f6f4 v[136:139], v[56:63], v[88:95], 0
	v_mfma_f32_16x16x128_f8f6f4 v[140:143], v[80:87], v[88:95], 0
	v_mfma_f32_16x16x128_f8f6f4 v[144:147], v[56:63], v[96:103], 0
	v_mfma_f32_16x16x128_f8f6f4 v[148:151], v[80:87], v[96:103], 0
	v_mfma_f32_16x16x128_f8f6f4 v[152:155], v[56:63], v[104:111], 0
	v_mfma_f32_16x16x128_f8f6f4 v[156:159], v[80:87], v[104:111], 0
	v_mfma_f32_16x16x128_f8f6f4 v[160:163], v[56:63], v[112:119], 0
	v_mfma_f32_16x16x128_f8f6f4 v[164:167], v[80:87], v[112:119], 0
	v_mfma_f32_16x16x128_f8f6f4 v[168:171], v[0:7], v[88:95], 0
	v_mfma_f32_16x16x128_f8f6f4 v[176:179], v[0:7], v[96:103], 0
	v_mfma_f32_16x16x128_f8f6f4 v[184:187], v[0:7], v[104:111], 0
	v_mfma_f32_16x16x128_f8f6f4 v[0:3], v[0:7], v[112:119], 0
	v_mfma_f32_16x16x128_f8f6f4 v[4:7], v[8:15], v[112:119], 0
	v_mfma_f32_16x16x128_f8f6f4 v[172:175], v[8:15], v[88:95], 0
	v_mfma_f32_16x16x128_f8f6f4 v[180:183], v[8:15], v[96:103], 0
	v_mfma_f32_16x16x128_f8f6f4 v[188:191], v[8:15], v[104:111], 0
	s_setprio 0
	s_barrier
	s_add_i32 s21, 0, 0x18000
	v_add_u32_e32 v56, s21, v196
	s_add_i32 s31, 0, 0x1c000
	ds_read_b128 v[8:11], v56
	ds_read_b128 v[12:15], v56 offset:1024
	ds_read_b128 v[200:203], v56 offset:2048
	ds_read_b128 v[204:207], v56 offset:3072
	v_add_u32_e32 v56, s31, v196
	ds_read_b128 v[208:211], v56
	ds_read_b128 v[212:215], v56 offset:1024
	ds_read_b128 v[216:219], v56 offset:2048
	ds_read_b128 v[220:223], v56 offset:3072
	s_add_u32 s42, s36, 0x8000
	v_mov_b32_e32 v56, v195
	s_addc_u32 s43, s37, 0
	s_mov_b32 m0, s60
	ds_read_b128 v[88:91], v199 offset:32768
	ds_read_b128 v[92:95], v199 offset:33792
	ds_read_b128 v[224:227], v199 offset:34816
	ds_read_b128 v[228:231], v199 offset:35840
	ds_read_b128 v[232:235], v199 offset:36864
	ds_read_b128 v[236:239], v199 offset:37888
	ds_read_b128 v[240:243], v199 offset:38912
	ds_read_b128 v[244:247], v199 offset:39936
	s_nop 0
	global_load_lds_dwordx4 v56, s[42:43] sc1
	s_add_u32 s42, s36, 0xc000
	v_mov_b32_e32 v56, v195
	s_addc_u32 s43, s37, 0
	s_mov_b32 m0, s61
	s_nop 0
	global_load_lds_dwordx4 v56, s[42:43] sc1
	s_waitcnt vmcnt(8)
	s_waitcnt lgkmcnt(0)
	s_barrier
	s_setprio 3
	v_mfma_f32_16x16x128_f8f6f4 v[112:115], v[8:15], v[88:95], v[16:19]
	v_mfma_f32_16x16x128_f8f6f4 v[116:119], v[200:207], v[88:95], v[20:23]
	v_mfma_f32_16x16x128_f8f6f4 v[96:99], v[8:15], v[224:231], v[24:27]
	v_mfma_f32_16x16x128_f8f6f4 v[100:103], v[200:207], v[224:231], v[28:31]
	v_mfma_f32_16x16x128_f8f6f4 v[80:83], v[8:15], v[232:239], v[32:35]
	v_mfma_f32_16x16x128_f8f6f4 v[84:87], v[200:207], v[232:239], v[36:39]
	v_mfma_f32_16x16x128_f8f6f4 v[56:59], v[8:15], v[240:247], v[40:43]
	v_mfma_f32_16x16x128_f8f6f4 v[60:63], v[200:207], v[240:247], v[44:47]
	v_mfma_f32_16x16x128_f8f6f4 v[120:123], v[208:215], v[88:95], v[48:51]
	v_mfma_f32_16x16x128_f8f6f4 v[124:127], v[216:223], v[88:95], v[52:55]
	v_mfma_f32_16x16x128_f8f6f4 v[104:107], v[208:215], v[224:231], v[64:67]
	v_mfma_f32_16x16x128_f8f6f4 v[108:111], v[216:223], v[224:231], v[68:71]
	v_mfma_f32_16x16x128_f8f6f4 v[88:91], v[208:215], v[232:239], v[72:75]
	v_mfma_f32_16x16x128_f8f6f4 v[92:95], v[216:223], v[232:239], v[76:79]
	v_mfma_f32_16x16x128_f8f6f4 v[64:67], v[208:215], v[240:247], v[128:131]
	v_mfma_f32_16x16x128_f8f6f4 v[68:71], v[216:223], v[240:247], v[132:135]
	s_setprio 0
	s_barrier
	v_mov_b32_e32 v24, v194
	s_add_i32 s21, s21, s51
	ds_read_b128 v[16:19], v199 offset:49152
	ds_read_b128 v[20:23], v199 offset:50176
	ds_read_b128 v[128:131], v199 offset:51200
	ds_read_b128 v[132:135], v199 offset:52224
	ds_read_b128 v[224:227], v199 offset:53248
	ds_read_b128 v[228:231], v199 offset:54272
	ds_read_b128 v[232:235], v199 offset:55296
	ds_read_b128 v[236:239], v199 offset:56320
	s_mov_b32 m0, s21
	s_add_u32 s42, s16, 0x4080
	s_addc_u32 s43, s17, 0
	global_load_lds_dwordx4 v24, s[48:49]
	v_mov_b32_e32 v24, v194
	s_add_i32 m0, s21, 0x2000
	s_nop 0
	global_load_lds_dwordx4 v24, s[42:43]
	s_add_u32 s42, s16, 0x8080
	v_mov_b32_e32 v24, v194
	s_addc_u32 s43, s17, 0
	s_add_i32 s21, s31, s51
	s_mov_b32 m0, s21
	s_nop 0
	global_load_lds_dwordx4 v24, s[42:43]
	v_mov_b32_e32 v24, v194
	s_add_u32 s42, s16, 0xc080
	s_addc_u32 s43, s17, 0
	s_add_i32 m0, s21, 0x2000
	s_nop 0
	global_load_lds_dwordx4 v24, s[42:43]
	v_mov_b32_e32 v24, v195
	s_mov_b32 m0, s68
	s_add_u32 s42, s36, 0x4080
	s_addc_u32 s43, s37, 0
	global_load_lds_dwordx4 v24, s[44:45] sc1
	v_mov_b32_e32 v24, v195
	s_mov_b32 m0, s69
	s_nop 0
	global_load_lds_dwordx4 v24, s[42:43] sc1
	s_waitcnt vmcnt(8)
	s_waitcnt lgkmcnt(0)
	s_barrier
	s_setprio 3
	v_mfma_f32_16x16x128_f8f6f4 v[48:51], v[8:15], v[16:23], v[136:139]
	v_mfma_f32_16x16x128_f8f6f4 v[52:55], v[200:207], v[16:23], v[140:143]
	v_mfma_f32_16x16x128_f8f6f4 v[32:35], v[8:15], v[128:135], v[144:147]
	v_mfma_f32_16x16x128_f8f6f4 v[36:39], v[200:207], v[128:135], v[148:151]
	v_mfma_f32_16x16x128_f8f6f4 v[24:27], v[8:15], v[224:231], v[152:155]
	v_mfma_f32_16x16x128_f8f6f4 v[28:31], v[200:207], v[224:231], v[156:159]
	v_mfma_f32_16x16x128_f8f6f4 v[8:11], v[8:15], v[232:239], v[160:163]
	v_mfma_f32_16x16x128_f8f6f4 v[12:15], v[200:207], v[232:239], v[164:167]
	v_mfma_f32_16x16x128_f8f6f4 v[72:75], v[208:215], v[16:23], v[168:171]
	v_mfma_f32_16x16x128_f8f6f4 v[76:79], v[216:223], v[16:23], v[172:175]
	v_mfma_f32_16x16x128_f8f6f4 v[40:43], v[208:215], v[128:135], v[176:179]
	v_mfma_f32_16x16x128_f8f6f4 v[44:47], v[216:223], v[128:135], v[180:183]
	v_mfma_f32_16x16x128_f8f6f4 v[16:19], v[208:215], v[224:231], v[184:187]
	v_mfma_f32_16x16x128_f8f6f4 v[20:23], v[216:223], v[224:231], v[188:191]
	v_mfma_f32_16x16x128_f8f6f4 v[0:3], v[208:215], v[232:239], v[0:3]
	v_mfma_f32_16x16x128_f8f6f4 v[4:7], v[216:223], v[232:239], v[4:7]
	s_setprio 0
	s_barrier
	s_andn2_b64 vcc, exec, s[24:25]
	s_cbranch_vccnz .LBB0_1404
	s_barrier

.LBB0_1412:
	s_or_b64 exec, exec, s[40:41]
	v_mov_b32_e32 v240, -1
	v_mov_b32_e32 v241, -1
	v_mov_b32_e32 v242, -1
	v_mov_b32_e32 v243, -1
	v_add_u32_e32 v244, 0x80, v139
	v_cmp_lt_i32_e32 vcc, v244, v138
	s_and_saveexec_b64 s[40:41], vcc
	global_load_dword v240, v[130:131], off offset:512
	s_or_b64 exec, exec, s[40:41]
	v_add_u32_e32 v244, 0x90, v139
	v_cmp_lt_i32_e32 vcc, v244, v138
	s_and_saveexec_b64 s[40:41], vcc
	global_load_dword v241, v[130:131], off offset:576
	s_or_b64 exec, exec, s[40:41]
	v_add_u32_e32 v244, 0xa0, v139
	v_cmp_lt_i32_e32 vcc, v244, v138
	s_and_saveexec_b64 s[40:41], vcc
	global_load_dword v242, v[130:131], off offset:640
	s_or_b64 exec, exec, s[40:41]
	v_add_u32_e32 v244, 0xb0, v139
	v_cmp_lt_i32_e32 vcc, v244, v138
	s_and_saveexec_b64 s[40:41], vcc
	global_load_dword v243, v[130:131], off offset:704
	s_or_b64 exec, exec, s[40:41]
	s_lshl_b32 s21, s38, 8
	v_lshrrev_b32_e32 v128, 1, v128
	v_and_or_b32 v128, v128, 24, s21
	v_or_b32_e32 v128, s65, v128
	v_ashrrev_i32_e32 v129, 31, v128
	s_waitcnt vmcnt(0)
	v_cmp_lt_i32_e32 vcc, -1, v192
	s_and_saveexec_b64 s[38:39], vcc
	s_cbranch_execz .LBB0_1414
	v_pk_mul_f32 v[112:113], v[112:113], s[28:29] op_sel_hi:[1,0]
	v_pk_mul_f32 v[116:117], v[116:117], s[28:29] op_sel_hi:[1,0]
	v_mov_b32_e32 v142, v193
	v_mov_b32_e32 v143, v193
	v_cvt_pk_fp8_f32 v142, v112, v113
	v_cvt_pk_fp8_f32 v143, v116, v117
	v_pk_mul_f32 v[112:113], v[114:115], s[28:29] op_sel_hi:[1,0]
	v_pk_mul_f32 v[114:115], v[118:119], s[28:29] op_sel_hi:[1,0]
	v_cvt_pk_fp8_f32 v142, v112, v113 op_sel:[0,0,1]
	v_cvt_pk_fp8_f32 v143, v114, v115 op_sel:[0,0,1]
	v_pk_mul_f32 v[112:113], v[120:121], s[28:29] op_sel_hi:[1,0]
	v_pk_mul_f32 v[114:115], v[124:125], s[28:29] op_sel_hi:[1,0]
	v_mov_b32_e32 v116, v193
	v_mov_b32_e32 v117, v193
	v_cvt_pk_fp8_f32 v116, v112, v113
	v_cvt_pk_fp8_f32 v117, v114, v115
	v_pk_mul_f32 v[112:113], v[122:123], s[28:29] op_sel_hi:[1,0]
	v_pk_mul_f32 v[114:115], v[126:127], s[28:29] op_sel_hi:[1,0]
	v_lshlrev_b64 v[140:141], 10, v[192:193]
	v_cvt_pk_fp8_f32 v116, v112, v113 op_sel:[0,0,1]
	v_cvt_pk_fp8_f32 v117, v114, v115 op_sel:[0,0,1]
	v_lshl_add_u64 v[112:113], s[22:23], 0, v[140:141]
	v_lshl_add_u64 v[112:113], v[112:113], 0, v[128:129]
	global_store_dwordx2 v[112:113], v[142:143], off
	global_store_dwordx2 v[112:113], v[116:117], off offset:128

.LBB0_1420:
	s_or_b64 exec, exec, s[38:39]
	v_mov_b32_e32 v192, v240
	v_mov_b32_e32 v60, v241
	v_mov_b32_e32 v58, v242
	v_mov_b32_e32 v56, v243
	v_cmp_lt_i32_e32 vcc, -1, v192
	s_and_saveexec_b64 s[38:39], vcc
	s_cbranch_execz .LBB0_1430
	v_pk_mul_f32 v[48:49], v[48:49], s[28:29] op_sel_hi:[1,0]
	v_pk_mul_f32 v[52:53], v[52:53], s[28:29] op_sel_hi:[1,0]
	v_mov_b32_e32 v64, v193
	v_mov_b32_e32 v65, v193
	v_cvt_pk_fp8_f32 v64, v48, v49
	v_cvt_pk_fp8_f32 v65, v52, v53
	v_pk_mul_f32 v[48:49], v[50:51], s[28:29] op_sel_hi:[1,0]
	v_pk_mul_f32 v[50:51], v[54:55], s[28:29] op_sel_hi:[1,0]
	v_cvt_pk_fp8_f32 v64, v48, v49 op_sel:[0,0,1]
	v_cvt_pk_fp8_f32 v65, v50, v51 op_sel:[0,0,1]
	v_pk_mul_f32 v[48:49], v[72:73], s[28:29] op_sel_hi:[1,0]
	v_pk_mul_f32 v[50:51], v[76:77], s[28:29] op_sel_hi:[1,0]
	v_mov_b32_e32 v52, v193
	v_mov_b32_e32 v53, v193
	v_cvt_pk_fp8_f32 v52, v48, v49
	v_cvt_pk_fp8_f32 v53, v50, v51
	v_pk_mul_f32 v[48:49], v[74:75], s[28:29] op_sel_hi:[1,0]
	v_pk_mul_f32 v[50:51], v[78:79], s[28:29] op_sel_hi:[1,0]
	v_lshlrev_b64 v[62:63], 10, v[192:193]
	v_cvt_pk_fp8_f32 v52, v48, v49 op_sel:[0,0,1]
	v_cvt_pk_fp8_f32 v53, v50, v51 op_sel:[0,0,1]
	v_lshl_add_u64 v[48:49], s[22:23], 0, v[62:63]
	v_lshl_add_u64 v[48:49], v[48:49], 0, v[128:129]
	global_store_dwordx2 v[48:49], v[64:65], off
	global_store_dwordx2 v[48:49], v[52:53], off offset:128

.LBB0_1769:
	ds_read_b128 v[56:59], v155
	ds_read_b128 v[60:63], v155 offset:1024
	ds_read_b128 v[68:71], v155 offset:2048
	ds_read_b128 v[76:79], v155 offset:3072
	ds_read_b128 v[146:149], v156
	ds_read_b128 v[160:163], v156 offset:1024
	ds_read_b128 v[164:167], v156 offset:2048
	ds_read_b128 v[168:171], v156 offset:3072
	s_add_u32 s69, s6, 0xfffa0080
	s_addc_u32 s70, s7, -1
	s_cmp_eq_u32 s53, 12
	s_cselect_b32 s71, s61, s70
	s_cselect_b32 s70, s60, s69
	s_cselect_b32 s74, s64, s5
	s_cselect_b32 s75, s65, s51
	s_add_u32 s72, s70, 0x80
	s_addc_u32 s73, s71, 0
	s_add_u32 s80, s6, 0xfffe0000
	v_mov_b32_e32 v150, v153
	s_addc_u32 s81, s7, -1
	ds_read_b128 v[172:175], v157
	ds_read_b128 v[176:179], v157 offset:1024
	ds_read_b128 v[180:183], v157 offset:2048
	ds_read_b128 v[184:187], v157 offset:3072
	ds_read_b128 v[188:191], v157 offset:4096
	ds_read_b128 v[192:195], v157 offset:5120
	ds_read_b128 v[196:199], v157 offset:6144
	ds_read_b128 v[200:203], v157 offset:7168
	s_add_i32 m0, s25, 0xc000
	s_nop 0
	global_load_lds_dwordx4 v150, s[80:81]
	v_mov_b32_e32 v150, v153
	s_mov_b64 s[80:81], s[6:7]
	s_add_i32 m0, s25, 0xe000
	s_nop 0
	global_load_lds_dwordx4 v150, s[80:81]
	s_waitcnt vmcnt(8)
	s_waitcnt lgkmcnt(0)
	s_barrier
	s_setprio 3
	v_mfma_f32_16x16x32_bf16 v[140:143], v[56:59], v[172:175], v[140:143]
	v_mfma_f32_16x16x32_bf16 v[136:139], v[68:71], v[172:175], v[136:139]
	v_mfma_f32_16x16x32_bf16 v[124:127], v[56:59], v[180:183], v[124:127]
	v_mfma_f32_16x16x32_bf16 v[120:123], v[68:71], v[180:183], v[120:123]
	v_mfma_f32_16x16x32_bf16 v[108:111], v[56:59], v[188:191], v[108:111]
	v_mfma_f32_16x16x32_bf16 v[104:107], v[68:71], v[188:191], v[104:107]
	v_mfma_f32_16x16x32_bf16 v[92:95], v[56:59], v[196:199], v[92:95]
	v_mfma_f32_16x16x32_bf16 v[88:91], v[68:71], v[196:199], v[88:91]
	v_mfma_f32_16x16x32_bf16 v[140:143], v[60:63], v[176:179], v[140:143]
	v_mfma_f32_16x16x32_bf16 v[136:139], v[76:79], v[176:179], v[136:139]
	v_mfma_f32_16x16x32_bf16 v[124:127], v[60:63], v[184:187], v[124:127]
	v_mfma_f32_16x16x32_bf16 v[120:123], v[76:79], v[184:187], v[120:123]
	v_mfma_f32_16x16x32_bf16 v[108:111], v[60:63], v[192:195], v[108:111]
	v_mfma_f32_16x16x32_bf16 v[104:107], v[76:79], v[192:195], v[104:107]
	v_mfma_f32_16x16x32_bf16 v[92:95], v[60:63], v[200:203], v[92:95]
	v_mfma_f32_16x16x32_bf16 v[88:91], v[76:79], v[200:203], v[88:91]
	v_mfma_f32_16x16x32_bf16 v[132:135], v[146:149], v[172:175], v[132:135]
	v_mfma_f32_16x16x32_bf16 v[128:131], v[164:167], v[172:175], v[128:131]
	v_mfma_f32_16x16x32_bf16 v[116:119], v[146:149], v[180:183], v[116:119]
	v_mfma_f32_16x16x32_bf16 v[112:115], v[164:167], v[180:183], v[112:115]
	v_mfma_f32_16x16x32_bf16 v[100:103], v[146:149], v[188:191], v[100:103]
	v_mfma_f32_16x16x32_bf16 v[96:99], v[164:167], v[188:191], v[96:99]
	v_mfma_f32_16x16x32_bf16 v[84:87], v[146:149], v[196:199], v[84:87]
	v_mfma_f32_16x16x32_bf16 v[80:83], v[164:167], v[196:199], v[80:83]
	v_mfma_f32_16x16x32_bf16 v[132:135], v[160:163], v[176:179], v[132:135]
	v_mfma_f32_16x16x32_bf16 v[128:131], v[168:171], v[176:179], v[128:131]
	v_mfma_f32_16x16x32_bf16 v[116:119], v[160:163], v[184:187], v[116:119]
	v_mfma_f32_16x16x32_bf16 v[112:115], v[168:171], v[184:187], v[112:115]
	v_mfma_f32_16x16x32_bf16 v[100:103], v[160:163], v[192:195], v[100:103]
	v_mfma_f32_16x16x32_bf16 v[96:99], v[168:171], v[192:195], v[96:99]
	v_mfma_f32_16x16x32_bf16 v[84:87], v[160:163], v[200:203], v[84:87]
	v_mfma_f32_16x16x32_bf16 v[80:83], v[168:171], v[200:203], v[80:83]
	s_setprio 0
	s_barrier
	v_mov_b32_e32 v150, v152
	s_mov_b64 s[80:81], s[74:75]
	s_add_i32 s69, s49, s23
	ds_read_b128 v[172:175], v157 offset:16384
	ds_read_b128 v[176:179], v157 offset:17408
	ds_read_b128 v[180:183], v157 offset:18432
	ds_read_b128 v[184:187], v157 offset:19456
	ds_read_b128 v[188:191], v157 offset:20480
	ds_read_b128 v[192:195], v157 offset:21504
	ds_read_b128 v[196:199], v157 offset:22528
	ds_read_b128 v[200:203], v157 offset:23552
	s_mov_b32 m0, s69
	s_nop 0
	global_load_lds_dwordx4 v150, s[80:81]
	s_add_u32 s80, s74, 0x20000
	v_mov_b32_e32 v150, v152
	s_addc_u32 s81, s75, 0
	s_add_i32 m0, s69, 0x2000
	s_nop 0
	global_load_lds_dwordx4 v150, s[80:81]
	s_add_u32 s80, s74, 0x40000
	v_mov_b32_e32 v150, v152
	s_addc_u32 s81, s75, 0
	s_add_i32 s69, s77, s23
	s_mov_b32 m0, s69
	s_nop 0
	global_load_lds_dwordx4 v150, s[80:81]
	s_add_u32 s80, s74, 0x60000
	v_mov_b32_e32 v150, v152
	s_addc_u32 s81, s75, 0
	s_add_i32 m0, s69, 0x2000
	s_nop 0
	global_load_lds_dwordx4 v150, s[80:81]
	v_mov_b32_e32 v150, v153
	s_mov_b64 s[80:81], s[70:71]
	s_mov_b32 m0, s25
	s_nop 0
	global_load_lds_dwordx4 v150, s[80:81]
	s_add_u32 s80, s70, 0x20000
	v_mov_b32_e32 v150, v153
	s_addc_u32 s81, s71, 0
	s_mov_b32 m0, s27
	s_nop 0
	global_load_lds_dwordx4 v150, s[80:81]
	s_waitcnt vmcnt(8)
	s_waitcnt lgkmcnt(0)
	s_barrier
	s_setprio 3
	v_mfma_f32_16x16x32_bf16 v[72:75], v[56:59], v[172:175], v[72:75]
	v_mfma_f32_16x16x32_bf16 v[64:67], v[68:71], v[172:175], v[64:67]
	v_mfma_f32_16x16x32_bf16 v[44:47], v[56:59], v[180:183], v[44:47]
	v_mfma_f32_16x16x32_bf16 v[40:43], v[68:71], v[180:183], v[40:43]
	v_mfma_f32_16x16x32_bf16 v[28:31], v[56:59], v[188:191], v[28:31]
	v_mfma_f32_16x16x32_bf16 v[24:27], v[68:71], v[188:191], v[24:27]
	v_mfma_f32_16x16x32_bf16 v[12:15], v[56:59], v[196:199], v[12:15]
	v_mfma_f32_16x16x32_bf16 v[8:11], v[68:71], v[196:199], v[8:11]
	v_mfma_f32_16x16x32_bf16 v[72:75], v[60:63], v[176:179], v[72:75]
	v_mfma_f32_16x16x32_bf16 v[64:67], v[76:79], v[176:179], v[64:67]
	v_mfma_f32_16x16x32_bf16 v[44:47], v[60:63], v[184:187], v[44:47]
	v_mfma_f32_16x16x32_bf16 v[40:43], v[76:79], v[184:187], v[40:43]
	v_mfma_f32_16x16x32_bf16 v[28:31], v[60:63], v[192:195], v[28:31]
	v_mfma_f32_16x16x32_bf16 v[24:27], v[76:79], v[192:195], v[24:27]
	v_mfma_f32_16x16x32_bf16 v[12:15], v[60:63], v[200:203], v[12:15]
	v_mfma_f32_16x16x32_bf16 v[8:11], v[76:79], v[200:203], v[8:11]
	v_mfma_f32_16x16x32_bf16 v[52:55], v[146:149], v[172:175], v[52:55]
	v_mfma_f32_16x16x32_bf16 v[48:51], v[164:167], v[172:175], v[48:51]
	v_mfma_f32_16x16x32_bf16 v[36:39], v[146:149], v[180:183], v[36:39]
	v_mfma_f32_16x16x32_bf16 v[32:35], v[164:167], v[180:183], v[32:35]
	v_mfma_f32_16x16x32_bf16 v[20:23], v[146:149], v[188:191], v[20:23]
	v_mfma_f32_16x16x32_bf16 v[16:19], v[164:167], v[188:191], v[16:19]
	v_mfma_f32_16x16x32_bf16 v[4:7], v[146:149], v[196:199], v[4:7]
	v_mfma_f32_16x16x32_bf16 v[0:3], v[164:167], v[196:199], v[0:3]
	v_mfma_f32_16x16x32_bf16 v[52:55], v[160:163], v[176:179], v[52:55]
	v_mfma_f32_16x16x32_bf16 v[48:51], v[168:171], v[176:179], v[48:51]
	v_mfma_f32_16x16x32_bf16 v[36:39], v[160:163], v[184:187], v[36:39]
	v_mfma_f32_16x16x32_bf16 v[32:35], v[168:171], v[184:187], v[32:35]
	v_mfma_f32_16x16x32_bf16 v[20:23], v[160:163], v[192:195], v[20:23]
	v_mfma_f32_16x16x32_bf16 v[16:19], v[168:171], v[192:195], v[16:19]
	v_mfma_f32_16x16x32_bf16 v[4:7], v[160:163], v[200:203], v[4:7]
	v_mfma_f32_16x16x32_bf16 v[0:3], v[168:171], v[200:203], v[0:3]
	s_setprio 0
	s_barrier
	s_add_i32 s69, 0, 0x18000
	s_add_i32 s82, 0, 0x1c000
	v_add_u32_e32 v76, s69, v154
	v_add_u32_e32 v150, s82, v154
	ds_read_b128 v[56:59], v76
	ds_read_b128 v[60:63], v76 offset:1024
	ds_read_b128 v[68:71], v76 offset:2048
	ds_read_b128 v[76:79], v76 offset:3072
	ds_read_b128 v[146:149], v150
	ds_read_b128 v[160:163], v150 offset:1024
	ds_read_b128 v[164:167], v150 offset:2048
	ds_read_b128 v[168:171], v150 offset:3072
	s_add_u32 s80, s70, 0x40000
	v_mov_b32_e32 v150, v153
	s_addc_u32 s81, s71, 0
	s_mov_b32 m0, s29
	ds_read_b128 v[172:175], v157 offset:32768
	ds_read_b128 v[176:179], v157 offset:33792
	ds_read_b128 v[180:183], v157 offset:34816
	ds_read_b128 v[184:187], v157 offset:35840
	ds_read_b128 v[188:191], v157 offset:36864
	ds_read_b128 v[192:195], v157 offset:37888
	ds_read_b128 v[196:199], v157 offset:38912
	ds_read_b128 v[200:203], v157 offset:39936
	s_nop 0
	global_load_lds_dwordx4 v150, s[80:81]
	s_add_u32 s80, s70, 0x60000
	v_mov_b32_e32 v150, v153
	s_addc_u32 s81, s71, 0
	s_mov_b32 m0, s31
	s_nop 0
	global_load_lds_dwordx4 v150, s[80:81]
	s_waitcnt vmcnt(8)
	s_waitcnt lgkmcnt(0)
	s_barrier
	s_setprio 3
	v_mfma_f32_16x16x32_bf16 v[140:143], v[56:59], v[172:175], v[140:143]
	v_mfma_f32_16x16x32_bf16 v[136:139], v[68:71], v[172:175], v[136:139]
	v_mfma_f32_16x16x32_bf16 v[124:127], v[56:59], v[180:183], v[124:127]
	v_mfma_f32_16x16x32_bf16 v[120:123], v[68:71], v[180:183], v[120:123]
	v_mfma_f32_16x16x32_bf16 v[108:111], v[56:59], v[188:191], v[108:111]
	v_mfma_f32_16x16x32_bf16 v[104:107], v[68:71], v[188:191], v[104:107]
	v_mfma_f32_16x16x32_bf16 v[92:95], v[56:59], v[196:199], v[92:95]
	v_mfma_f32_16x16x32_bf16 v[88:91], v[68:71], v[196:199], v[88:91]
	v_mfma_f32_16x16x32_bf16 v[140:143], v[60:63], v[176:179], v[140:143]
	v_mfma_f32_16x16x32_bf16 v[136:139], v[76:79], v[176:179], v[136:139]
	v_mfma_f32_16x16x32_bf16 v[124:127], v[60:63], v[184:187], v[124:127]
	v_mfma_f32_16x16x32_bf16 v[120:123], v[76:79], v[184:187], v[120:123]
	v_mfma_f32_16x16x32_bf16 v[108:111], v[60:63], v[192:195], v[108:111]
	v_mfma_f32_16x16x32_bf16 v[104:107], v[76:79], v[192:195], v[104:107]
	v_mfma_f32_16x16x32_bf16 v[92:95], v[60:63], v[200:203], v[92:95]
	v_mfma_f32_16x16x32_bf16 v[88:91], v[76:79], v[200:203], v[88:91]
	v_mfma_f32_16x16x32_bf16 v[132:135], v[146:149], v[172:175], v[132:135]
	v_mfma_f32_16x16x32_bf16 v[128:131], v[164:167], v[172:175], v[128:131]
	v_mfma_f32_16x16x32_bf16 v[116:119], v[146:149], v[180:183], v[116:119]
	v_mfma_f32_16x16x32_bf16 v[112:115], v[164:167], v[180:183], v[112:115]
	v_mfma_f32_16x16x32_bf16 v[100:103], v[146:149], v[188:191], v[100:103]
	v_mfma_f32_16x16x32_bf16 v[96:99], v[164:167], v[188:191], v[96:99]
	v_mfma_f32_16x16x32_bf16 v[84:87], v[146:149], v[196:199], v[84:87]
	v_mfma_f32_16x16x32_bf16 v[80:83], v[164:167], v[196:199], v[80:83]
	v_mfma_f32_16x16x32_bf16 v[132:135], v[160:163], v[176:179], v[132:135]
	v_mfma_f32_16x16x32_bf16 v[128:131], v[168:171], v[176:179], v[128:131]
	v_mfma_f32_16x16x32_bf16 v[116:119], v[160:163], v[184:187], v[116:119]
	v_mfma_f32_16x16x32_bf16 v[112:115], v[168:171], v[184:187], v[112:115]
	v_mfma_f32_16x16x32_bf16 v[100:103], v[160:163], v[192:195], v[100:103]
	v_mfma_f32_16x16x32_bf16 v[96:99], v[168:171], v[192:195], v[96:99]
	v_mfma_f32_16x16x32_bf16 v[84:87], v[160:163], v[200:203], v[84:87]
	v_mfma_f32_16x16x32_bf16 v[80:83], v[168:171], v[200:203], v[80:83]
	s_setprio 0
	s_barrier
	s_add_u32 s80, s74, 0x80
	s_addc_u32 s81, s75, 0
	v_mov_b32_e32 v150, v152
	s_add_i32 s69, s69, s23
	ds_read_b128 v[172:175], v157 offset:49152
	ds_read_b128 v[176:179], v157 offset:50176
	ds_read_b128 v[180:183], v157 offset:51200
	ds_read_b128 v[184:187], v157 offset:52224
	ds_read_b128 v[188:191], v157 offset:53248
	ds_read_b128 v[192:195], v157 offset:54272
	ds_read_b128 v[196:199], v157 offset:55296
	ds_read_b128 v[200:203], v157 offset:56320
	s_mov_b32 m0, s69
	s_nop 0
	global_load_lds_dwordx4 v150, s[80:81]
	s_add_u32 s80, s74, 0x20080
	v_mov_b32_e32 v150, v152
	s_addc_u32 s81, s75, 0
	s_add_i32 m0, s69, 0x2000
	s_nop 0
	global_load_lds_dwordx4 v150, s[80:81]
	s_add_u32 s80, s74, 0x40080
	v_mov_b32_e32 v150, v152
	s_addc_u32 s81, s75, 0
	s_add_i32 s69, s82, s23
	s_mov_b32 m0, s69
	s_add_u32 s74, s74, 0x60080
	global_load_lds_dwordx4 v150, s[80:81]
	v_mov_b32_e32 v150, v152
	s_addc_u32 s75, s75, 0
	s_add_i32 m0, s69, 0x2000
	s_add_u32 s70, s70, 0x20080
	global_load_lds_dwordx4 v150, s[74:75]
	v_mov_b32_e32 v150, v153
	s_mov_b32 m0, s43
	s_addc_u32 s71, s71, 0
	global_load_lds_dwordx4 v150, s[72:73]
	v_mov_b32_e32 v150, v153
	s_mov_b32 m0, s45
	s_nop 0
	global_load_lds_dwordx4 v150, s[70:71]
	s_waitcnt vmcnt(8)
	s_waitcnt lgkmcnt(0)
	s_barrier
	s_setprio 3
	v_mfma_f32_16x16x32_bf16 v[72:75], v[56:59], v[172:175], v[72:75]
	v_mfma_f32_16x16x32_bf16 v[64:67], v[68:71], v[172:175], v[64:67]
	v_mfma_f32_16x16x32_bf16 v[44:47], v[56:59], v[180:183], v[44:47]
	v_mfma_f32_16x16x32_bf16 v[40:43], v[68:71], v[180:183], v[40:43]
	v_mfma_f32_16x16x32_bf16 v[28:31], v[56:59], v[188:191], v[28:31]
	v_mfma_f32_16x16x32_bf16 v[24:27], v[68:71], v[188:191], v[24:27]
	v_mfma_f32_16x16x32_bf16 v[12:15], v[56:59], v[196:199], v[12:15]
	v_mfma_f32_16x16x32_bf16 v[8:11], v[68:71], v[196:199], v[8:11]
	v_mfma_f32_16x16x32_bf16 v[72:75], v[60:63], v[176:179], v[72:75]
	v_mfma_f32_16x16x32_bf16 v[64:67], v[76:79], v[176:179], v[64:67]
	v_mfma_f32_16x16x32_bf16 v[44:47], v[60:63], v[184:187], v[44:47]
	v_mfma_f32_16x16x32_bf16 v[40:43], v[76:79], v[184:187], v[40:43]
	v_mfma_f32_16x16x32_bf16 v[28:31], v[60:63], v[192:195], v[28:31]
	v_mfma_f32_16x16x32_bf16 v[24:27], v[76:79], v[192:195], v[24:27]
	v_mfma_f32_16x16x32_bf16 v[12:15], v[60:63], v[200:203], v[12:15]
	v_mfma_f32_16x16x32_bf16 v[8:11], v[76:79], v[200:203], v[8:11]
	v_mfma_f32_16x16x32_bf16 v[52:55], v[146:149], v[172:175], v[52:55]
	v_mfma_f32_16x16x32_bf16 v[48:51], v[164:167], v[172:175], v[48:51]
	v_mfma_f32_16x16x32_bf16 v[36:39], v[146:149], v[180:183], v[36:39]
	v_mfma_f32_16x16x32_bf16 v[32:35], v[164:167], v[180:183], v[32:35]
	v_mfma_f32_16x16x32_bf16 v[20:23], v[146:149], v[188:191], v[20:23]
	v_mfma_f32_16x16x32_bf16 v[16:19], v[164:167], v[188:191], v[16:19]
	v_mfma_f32_16x16x32_bf16 v[4:7], v[146:149], v[196:199], v[4:7]
	v_mfma_f32_16x16x32_bf16 v[0:3], v[164:167], v[196:199], v[0:3]
	v_mfma_f32_16x16x32_bf16 v[52:55], v[160:163], v[176:179], v[52:55]
	v_mfma_f32_16x16x32_bf16 v[48:51], v[168:171], v[176:179], v[48:51]
	v_mfma_f32_16x16x32_bf16 v[36:39], v[160:163], v[184:187], v[36:39]
	v_mfma_f32_16x16x32_bf16 v[32:35], v[168:171], v[184:187], v[32:35]
	v_mfma_f32_16x16x32_bf16 v[20:23], v[160:163], v[192:195], v[20:23]
	v_mfma_f32_16x16x32_bf16 v[16:19], v[168:171], v[192:195], v[16:19]
	v_mfma_f32_16x16x32_bf16 v[4:7], v[160:163], v[200:203], v[4:7]
	v_mfma_f32_16x16x32_bf16 v[0:3], v[168:171], v[200:203], v[0:3]
	s_setprio 0
	s_barrier
	s_add_i32 s53, s53, 2
	s_add_u32 s5, s5, 0x100
	s_addc_u32 s51, s51, 0
	s_add_u32 s6, s6, 0x100
	s_addc_u32 s7, s7, 0
	s_cmp_gt_u32 s53, 13
	s_cbranch_scc0 .LBB0_1769
	s_mov_b64 s[46:47], s[94:95]
	s_and_b64 vcc, exec, s[18:19]
	s_cbranch_vccz .LBB0_1772
	s_barrier

.LBB0_2137:
	ds_read_b128 v[8:11], v177
	ds_read_b128 v[12:15], v177 offset:1024
	ds_read_b128 v[136:139], v177 offset:2048
	ds_read_b128 v[140:143], v177 offset:3072
	ds_read_b128 v[146:149], v178
	ds_read_b128 v[150:153], v178 offset:1024
	ds_read_b128 v[154:157], v178 offset:2048
	ds_read_b128 v[158:161], v178 offset:3072
	s_add_u32 s30, s28, 0xfffa0080
	s_addc_u32 s31, s29, -1
	s_cmp_eq_u32 s65, 12
	s_cselect_b32 s30, s22, s30
	s_cselect_b32 s31, s23, s31
	s_cselect_b32 s36, s24, s19
	s_cselect_b32 s37, s25, s21
	s_add_u32 s34, s30, 0x80
	s_addc_u32 s35, s31, 0
	s_add_u32 s68, s28, 0xfffe0000
	v_mov_b32_e32 v170, v175
	s_addc_u32 s69, s29, -1
	ds_read_b128 v[162:165], v179
	ds_read_b128 v[166:169], v179 offset:1024
	ds_read_b128 v[180:183], v179 offset:2048
	ds_read_b128 v[184:187], v179 offset:3072
	ds_read_b128 v[188:191], v179 offset:4096
	ds_read_b128 v[192:195], v179 offset:5120
	ds_read_b128 v[196:199], v179 offset:6144
	ds_read_b128 v[200:203], v179 offset:7168
	s_add_i32 m0, s27, 0xc000
	s_nop 0
	global_load_lds_dwordx4 v170, s[68:69]
	v_mov_b32_e32 v170, v175
	s_mov_b64 s[68:69], s[28:29]
	s_add_i32 m0, s27, 0xe000
	s_nop 0
	global_load_lds_dwordx4 v170, s[68:69]
	s_waitcnt vmcnt(8)
	s_waitcnt lgkmcnt(0)
	s_barrier
	s_setprio 3
	v_mfma_f32_16x16x128_f8f6f4 v[132:135], v[8:15], v[162:169], v[132:135]
	v_mfma_f32_16x16x128_f8f6f4 v[128:131], v[136:143], v[162:169], v[128:131]
	v_mfma_f32_16x16x128_f8f6f4 v[116:119], v[8:15], v[180:187], v[116:119]
	v_mfma_f32_16x16x128_f8f6f4 v[112:115], v[136:143], v[180:187], v[112:115]
	v_mfma_f32_16x16x128_f8f6f4 v[100:103], v[8:15], v[188:195], v[100:103]
	v_mfma_f32_16x16x128_f8f6f4 v[96:99], v[136:143], v[188:195], v[96:99]
	v_mfma_f32_16x16x128_f8f6f4 v[84:87], v[8:15], v[196:203], v[84:87]
	v_mfma_f32_16x16x128_f8f6f4 v[80:83], v[136:143], v[196:203], v[80:83]
	v_mfma_f32_16x16x128_f8f6f4 v[124:127], v[146:153], v[162:169], v[124:127]
	v_mfma_f32_16x16x128_f8f6f4 v[120:123], v[154:161], v[162:169], v[120:123]
	v_mfma_f32_16x16x128_f8f6f4 v[108:111], v[146:153], v[180:187], v[108:111]
	v_mfma_f32_16x16x128_f8f6f4 v[104:107], v[154:161], v[180:187], v[104:107]
	v_mfma_f32_16x16x128_f8f6f4 v[92:95], v[146:153], v[188:195], v[92:95]
	v_mfma_f32_16x16x128_f8f6f4 v[88:91], v[154:161], v[188:195], v[88:91]
	v_mfma_f32_16x16x128_f8f6f4 v[76:79], v[146:153], v[196:203], v[76:79]
	v_mfma_f32_16x16x128_f8f6f4 v[72:75], v[154:161], v[196:203], v[72:75]
	s_setprio 0
	s_barrier
	v_mov_b32_e32 v170, v174
	s_mov_b64 s[68:69], s[36:37]
	s_add_i32 s70, s60, s39
	ds_read_b128 v[162:165], v179 offset:16384
	ds_read_b128 v[166:169], v179 offset:17408
	ds_read_b128 v[180:183], v179 offset:18432
	ds_read_b128 v[184:187], v179 offset:19456
	ds_read_b128 v[188:191], v179 offset:20480
	ds_read_b128 v[192:195], v179 offset:21504
	ds_read_b128 v[196:199], v179 offset:22528
	ds_read_b128 v[200:203], v179 offset:23552
	s_mov_b32 m0, s70
	s_nop 0
	global_load_lds_dwordx4 v170, s[68:69]
	s_add_u32 s68, s36, 0x20000
	v_mov_b32_e32 v170, v174
	s_addc_u32 s69, s37, 0
	s_add_i32 m0, s70, 0x2000
	s_nop 0
	global_load_lds_dwordx4 v170, s[68:69]
	s_add_u32 s68, s36, 0x40000
	v_mov_b32_e32 v170, v174
	s_addc_u32 s69, s37, 0
	s_add_i32 s70, s61, s39
	s_mov_b32 m0, s70
	s_nop 0
	global_load_lds_dwordx4 v170, s[68:69]
	s_add_u32 s68, s36, 0x60000
	v_mov_b32_e32 v170, v174
	s_addc_u32 s69, s37, 0
	s_add_i32 m0, s70, 0x2000
	s_nop 0
	global_load_lds_dwordx4 v170, s[68:69]
	v_mov_b32_e32 v170, v175
	s_mov_b64 s[68:69], s[30:31]
	s_mov_b32 m0, s27
	s_nop 0
	global_load_lds_dwordx4 v170, s[68:69]
	s_add_u32 s68, s30, 0x20000
	v_mov_b32_e32 v170, v175
	s_addc_u32 s69, s31, 0
	s_mov_b32 m0, s41
	s_nop 0
	global_load_lds_dwordx4 v170, s[68:69]
	s_waitcnt vmcnt(8)
	s_waitcnt lgkmcnt(0)
	s_barrier
	s_setprio 3
	v_mfma_f32_16x16x128_f8f6f4 v[68:71], v[8:15], v[162:169], v[68:71]
	v_mfma_f32_16x16x128_f8f6f4 v[64:67], v[136:143], v[162:169], v[64:67]
	v_mfma_f32_16x16x128_f8f6f4 v[52:55], v[8:15], v[180:187], v[52:55]
	v_mfma_f32_16x16x128_f8f6f4 v[48:51], v[136:143], v[180:187], v[48:51]
	v_mfma_f32_16x16x128_f8f6f4 v[36:39], v[8:15], v[188:195], v[36:39]
	v_mfma_f32_16x16x128_f8f6f4 v[32:35], v[136:143], v[188:195], v[32:35]
	v_mfma_f32_16x16x128_f8f6f4 v[20:23], v[8:15], v[196:203], v[20:23]
	v_mfma_f32_16x16x128_f8f6f4 v[16:19], v[136:143], v[196:203], v[16:19]
	v_mfma_f32_16x16x128_f8f6f4 v[60:63], v[146:153], v[162:169], v[60:63]
	v_mfma_f32_16x16x128_f8f6f4 v[56:59], v[154:161], v[162:169], v[56:59]
	v_mfma_f32_16x16x128_f8f6f4 v[44:47], v[146:153], v[180:187], v[44:47]
	v_mfma_f32_16x16x128_f8f6f4 v[40:43], v[154:161], v[180:187], v[40:43]
	v_mfma_f32_16x16x128_f8f6f4 v[28:31], v[146:153], v[188:195], v[28:31]
	v_mfma_f32_16x16x128_f8f6f4 v[24:27], v[154:161], v[188:195], v[24:27]
	v_mfma_f32_16x16x128_f8f6f4 v[136:139], v[146:153], v[196:203], v[4:7]
	v_mfma_f32_16x16x128_f8f6f4 v[140:143], v[154:161], v[196:203], v[0:3]
	s_setprio 0
	s_barrier
	s_add_i32 s70, 0, 0x18000
	s_add_i32 s71, 0, 0x1c000
	s_nop 2
	v_add_u32_e32 v0, s70, v176
	v_add_u32_e32 v12, s71, v176
	ds_read_b128 v[146:149], v0
	ds_read_b128 v[150:153], v0 offset:1024
	ds_read_b128 v[154:157], v0 offset:2048
	ds_read_b128 v[158:161], v0 offset:3072
	ds_read_b128 v[0:3], v12
	ds_read_b128 v[4:7], v12 offset:1024
	ds_read_b128 v[8:11], v12 offset:2048
	ds_read_b128 v[12:15], v12 offset:3072
	s_add_u32 s68, s30, 0x40000
	v_mov_b32_e32 v170, v175
	s_addc_u32 s69, s31, 0
	s_mov_b32 m0, s42
	ds_read_b128 v[162:165], v179 offset:32768
	ds_read_b128 v[166:169], v179 offset:33792
	ds_read_b128 v[180:183], v179 offset:34816
	ds_read_b128 v[184:187], v179 offset:35840
	ds_read_b128 v[188:191], v179 offset:36864
	ds_read_b128 v[192:195], v179 offset:37888
	ds_read_b128 v[196:199], v179 offset:38912
	ds_read_b128 v[200:203], v179 offset:39936
	s_nop 0
	global_load_lds_dwordx4 v170, s[68:69]
	s_add_u32 s68, s30, 0x60000
	v_mov_b32_e32 v170, v175
	s_addc_u32 s69, s31, 0
	s_mov_b32 m0, s43
	s_nop 0
	global_load_lds_dwordx4 v170, s[68:69]
	s_waitcnt vmcnt(8)
	s_waitcnt lgkmcnt(0)
	s_barrier
	s_setprio 3
	v_mfma_f32_16x16x128_f8f6f4 v[132:135], v[146:153], v[162:169], v[132:135]
	v_mfma_f32_16x16x128_f8f6f4 v[128:131], v[154:161], v[162:169], v[128:131]
	v_mfma_f32_16x16x128_f8f6f4 v[116:119], v[146:153], v[180:187], v[116:119]
	v_mfma_f32_16x16x128_f8f6f4 v[112:115], v[154:161], v[180:187], v[112:115]
	v_mfma_f32_16x16x128_f8f6f4 v[100:103], v[146:153], v[188:195], v[100:103]
	v_mfma_f32_16x16x128_f8f6f4 v[96:99], v[154:161], v[188:195], v[96:99]
	v_mfma_f32_16x16x128_f8f6f4 v[84:87], v[146:153], v[196:203], v[84:87]
	v_mfma_f32_16x16x128_f8f6f4 v[80:83], v[154:161], v[196:203], v[80:83]
	v_mfma_f32_16x16x128_f8f6f4 v[124:127], v[0:7], v[162:169], v[124:127]
	v_mfma_f32_16x16x128_f8f6f4 v[120:123], v[8:15], v[162:169], v[120:123]
	v_mfma_f32_16x16x128_f8f6f4 v[108:111], v[0:7], v[180:187], v[108:111]
	v_mfma_f32_16x16x128_f8f6f4 v[104:107], v[8:15], v[180:187], v[104:107]
	v_mfma_f32_16x16x128_f8f6f4 v[92:95], v[0:7], v[188:195], v[92:95]
	v_mfma_f32_16x16x128_f8f6f4 v[88:91], v[8:15], v[188:195], v[88:91]
	v_mfma_f32_16x16x128_f8f6f4 v[76:79], v[0:7], v[196:203], v[76:79]
	v_mfma_f32_16x16x128_f8f6f4 v[72:75], v[8:15], v[196:203], v[72:75]
	s_setprio 0
	s_barrier
	s_add_u32 s68, s36, 0x80
	s_addc_u32 s69, s37, 0
	v_mov_b32_e32 v170, v174
	s_add_i32 s70, s70, s39
	ds_read_b128 v[162:165], v179 offset:49152
	ds_read_b128 v[166:169], v179 offset:50176
	ds_read_b128 v[180:183], v179 offset:51200
	ds_read_b128 v[184:187], v179 offset:52224
	ds_read_b128 v[188:191], v179 offset:53248
	ds_read_b128 v[192:195], v179 offset:54272
	ds_read_b128 v[196:199], v179 offset:55296
	ds_read_b128 v[200:203], v179 offset:56320
	s_mov_b32 m0, s70
	s_nop 0
	global_load_lds_dwordx4 v170, s[68:69]
	s_add_u32 s68, s36, 0x20080
	v_mov_b32_e32 v170, v174
	s_addc_u32 s69, s37, 0
	s_add_i32 m0, s70, 0x2000
	s_nop 0
	global_load_lds_dwordx4 v170, s[68:69]
	s_add_u32 s68, s36, 0x40080
	v_mov_b32_e32 v170, v174
	s_addc_u32 s69, s37, 0
	s_add_i32 s70, s71, s39
	s_mov_b32 m0, s70
	s_add_u32 s36, s36, 0x60080
	global_load_lds_dwordx4 v170, s[68:69]
	v_mov_b32_e32 v170, v174
	s_addc_u32 s37, s37, 0
	s_add_i32 m0, s70, 0x2000
	s_add_u32 s30, s30, 0x20080
	global_load_lds_dwordx4 v170, s[36:37]
	v_mov_b32_e32 v170, v175
	s_mov_b32 m0, s53
	s_addc_u32 s31, s31, 0
	global_load_lds_dwordx4 v170, s[34:35]
	v_mov_b32_e32 v170, v175
	s_mov_b32 m0, s54
	s_nop 0
	global_load_lds_dwordx4 v170, s[30:31]
	s_waitcnt vmcnt(8)
	s_waitcnt lgkmcnt(0)
	s_barrier
	s_setprio 3
	v_mfma_f32_16x16x128_f8f6f4 v[68:71], v[146:153], v[162:169], v[68:71]
	v_mfma_f32_16x16x128_f8f6f4 v[64:67], v[154:161], v[162:169], v[64:67]
	v_mfma_f32_16x16x128_f8f6f4 v[52:55], v[146:153], v[180:187], v[52:55]
	v_mfma_f32_16x16x128_f8f6f4 v[48:51], v[154:161], v[180:187], v[48:51]
	v_mfma_f32_16x16x128_f8f6f4 v[36:39], v[146:153], v[188:195], v[36:39]
	v_mfma_f32_16x16x128_f8f6f4 v[32:35], v[154:161], v[188:195], v[32:35]
	v_mfma_f32_16x16x128_f8f6f4 v[20:23], v[146:153], v[196:203], v[20:23]
	v_mfma_f32_16x16x128_f8f6f4 v[16:19], v[154:161], v[196:203], v[16:19]
	v_mfma_f32_16x16x128_f8f6f4 v[60:63], v[0:7], v[162:169], v[60:63]
	v_mfma_f32_16x16x128_f8f6f4 v[56:59], v[8:15], v[162:169], v[56:59]
	v_mfma_f32_16x16x128_f8f6f4 v[44:47], v[0:7], v[180:187], v[44:47]
	v_mfma_f32_16x16x128_f8f6f4 v[40:43], v[8:15], v[180:187], v[40:43]
	v_mfma_f32_16x16x128_f8f6f4 v[28:31], v[0:7], v[188:195], v[28:31]
	v_mfma_f32_16x16x128_f8f6f4 v[24:27], v[8:15], v[188:195], v[24:27]
	v_mfma_f32_16x16x128_f8f6f4 v[4:7], v[0:7], v[196:203], v[136:139]
	v_mfma_f32_16x16x128_f8f6f4 v[0:3], v[8:15], v[196:203], v[140:143]
	s_setprio 0
	s_barrier
	s_add_i32 s65, s65, 2
	s_add_u32 s19, s19, 0x100
	s_addc_u32 s21, s21, 0
	s_add_u32 s28, s28, 0x100
	s_addc_u32 s29, s29, 0
	s_cmp_gt_u32 s65, 13
	s_cbranch_scc0 .LBB0_2137
	s_and_b64 vcc, exec, s[12:13]
	s_cbranch_vccz .LBB0_2140
	s_barrier

.LBB0_2419:
	s_add_u32 s48, s78, 0xe000
	s_addc_u32 s49, s79, 0
	s_lshl_b32 s28, s4, 1
	s_min_i32 s29, s28, s33
	s_add_u32 s4, s78, 0x3500000
	s_addc_u32 s5, s79, 0
	s_add_u32 s12, s78, 0x16500000
	s_addc_u32 s13, s79, 0
	s_cmp_ge_i32 s16, s29
	s_cbranch_scc1 .LBB0_2600
	s_and_b32 s30, s18, 0xffffffc0
	v_mbcnt_lo_u32_b32 v0, -1, 0
	v_mbcnt_hi_u32_b32 v0, -1, v0
	s_ashr_i32 s31, s16, 1
	v_add_u32_e32 v0, s30, v0
	s_lshl_b32 s14, s31, 2
	v_ashrrev_i32_e32 v2, 31, v0
	v_lshrrev_b32_e32 v2, 26, v2
	v_add_u32_e32 v2, v0, v2
	v_lshlrev_b32_e32 v1, 4, v0
	v_ashrrev_i32_e32 v2, 6, v2
	v_bfe_i32 v0, v0, 27, 1
	v_lshrrev_b32_e32 v0, 22, v0
	v_lshlrev_b32_e32 v2, 3, v2
	s_add_i32 s14, s3, s14
	v_add_u32_e32 v0, v1, v0
	v_and_b32_e32 v4, -16, v2
	v_mov_b32_e32 v2, s14
	v_and_b32_e32 v0, 0xfffffc00, v0
	ds_read2_b32 v[2:3], v2 offset0:64 offset1:224
	v_sub_u32_e32 v0, v1, v0
	v_lshrrev_b32_e32 v1, 4, v0
	v_ashrrev_i32_e32 v5, 31, v0
	v_and_b32_e32 v1, 32, v1
	v_lshrrev_b32_e32 v5, 26, v5
	v_xad_u32 v0, v1, v0, v5
	v_ashrrev_i32_e32 v5, 6, v0
	s_waitcnt lgkmcnt(0)
	v_lshlrev_b32_e32 v0, 2, v2
	v_add_u32_e32 v0, s3, v0
	ds_read_b32 v11, v0 offset:4
	v_ashrrev_i32_e32 v1, 31, v2
	v_mov_b32_e32 v0, v2
	v_add3_u32 v4, v5, v4, v3
	v_lshlrev_b64 v[2:3], 16, v[0:1]
	v_lshl_add_u64 v[2:3], s[6:7], 0, v[2:3]
	s_waitcnt lgkmcnt(0)
	v_cmp_lt_i32_e32 vcc, v4, v11
	v_mov_b32_e32 v10, 0
	v_mov_b32_e32 v9, 0
	v_mov_b32_e32 v240, 0
	v_mov_b32_e32 v241, 0
	v_mov_b32_e32 v242, 0
	v_mov_b32_e32 v243, 0
	s_and_saveexec_b64 s[14:15], vcc
	s_cbranch_execz .LBB0_2422
	v_ashrrev_i32_e32 v5, 31, v4
	v_lshl_add_u64 v[6:7], v[4:5], 2, v[2:3]
	global_load_dword v240, v[6:7], off

.LBB0_2428:
	s_or_b64 exec, exec, s[14:15]
	s_waitcnt vmcnt(0)
	v_ashrrev_i32_e32 v9, 1, v240
	v_lshlrev_b32_e32 v241, 15, v241
	v_and_b32_e32 v10, 0xffff0000, v241
	v_ashrrev_i32_e32 v7, 1, v242
	v_lshlrev_b32_e32 v243, 15, v243
	v_and_b32_e32 v5, 0xffff0000, v243
	v_bfe_i32 v4, v8, 27, 1
	v_lshlrev_b32_e32 v2, 4, v8
	v_lshrrev_b32_e32 v4, 22, v4
	v_add_u32_e32 v4, v2, v4
	v_and_b32_e32 v4, 0xfffffc00, v4
	v_sub_u32_e32 v2, v2, v4
	v_ashrrev_i32_e32 v3, 31, v8
	v_lshrrev_b32_e32 v4, 4, v2
	v_lshrrev_b32_e32 v3, 26, v3
	v_bitop3_b32 v4, v4, v2, 32 bitop3:0x6c
	v_ashrrev_i32_e32 v2, 31, v2
	v_add_u32_e32 v3, v8, v3
	v_lshrrev_b32_e32 v2, 26, v2
	v_ashrrev_i32_e32 v3, 6, v3
	v_add_u32_e32 v2, v4, v2
	v_lshlrev_b32_e32 v6, 3, v3
	v_ashrrev_i32_e32 v2, 6, v2
	v_or_b32_e32 v128, v10, v9
	v_and_b32_e32 v6, -16, v6
	v_mul_i32_i24_e32 v10, 64, v2
	v_add_u32_e32 v6, v2, v6
	v_sub_u32_e32 v4, v4, v10
	v_mov_b32_e32 v10, 1
	s_and_b32 s56, s16, 1
	v_lshlrev_b32_e32 v3, 5, v3
	v_ashrrev_i16_sdwa v4, v10, sext(v4) dst_sel:DWORD dst_unused:UNUSED_PAD src0_sel:DWORD src1_sel:BYTE_0
	v_lshlrev_b32_e32 v10, 1, v6
	v_lshrrev_b32_e32 v11, 2, v6
	v_and_b32_e32 v2, 3, v2
	s_mov_b32 s14, 0x3fffe0
	v_lshlrev_b64 v[0:1], 19, v[0:1]
	v_and_b32_e32 v3, 32, v3
	v_bfe_i32 v4, v4, 0, 16
	v_and_b32_e32 v10, 24, v10
	v_and_b32_e32 v11, 4, v11
	v_and_or_b32 v2, v6, s14, v2
	v_lshl_add_u64 v[0:1], s[4:5], 0, v[0:1]
	s_lshl_b32 s14, s56, 18
	s_mov_b32 s15, 0
	s_ashr_i32 s19, s18, 6
	v_or3_b32 v2, v2, v11, v10
	v_add_lshl_u32 v3, v3, v4, 1
	v_lshl_add_u64 v[0:1], v[0:1], 0, s[14:15]
	v_lshl_add_u32 v134, v2, 10, v3
	s_lshl_b32 s34, s19, 10
	v_readfirstlane_b32 s23, v1
	v_readfirstlane_b32 s22, v0
	s_add_i32 s35, s34, 0
	v_mov_b32_e32 v0, v134
	s_mov_b64 s[16:17], s[22:23]
	s_ashr_i32 s20, s18, 8
	s_add_i32 m0, s35, 0x10000
	v_and_b32_e32 v135, 0x7e, v3
	global_load_lds_dwordx4 v0, s[16:17]
	s_add_u32 s16, s22, 0x10000
	v_mov_b32_e32 v0, v134
	s_addc_u32 s17, s23, 0
	s_add_i32 m0, s35, 0x12000
	s_mov_b32 s36, 0x3fffc00
	global_load_lds_dwordx4 v0, s[16:17]
	s_add_i32 m0, s35, 0x14000
	s_add_u32 s16, s22, 0x20000
	v_mov_b32_e32 v0, v134
	s_addc_u32 s17, s23, 0
	v_or_b32_e32 v129, v5, v7
	global_load_lds_dwordx4 v0, s[16:17]
	v_mov_b32_e32 v0, v134
	s_add_u32 s16, s22, 0x30000
	s_addc_u32 s17, s23, 0
	s_add_i32 m0, s35, 0x16000
	s_add_i32 s37, s35, 0x2000
	global_load_lds_dwordx4 v0, s[16:17]
	v_lshlrev_b32_e32 v0, 10, v9
	v_and_or_b32 v0, v0, s36, v135
	v_mov_b32_e32 v1, v0
	s_mov_b64 s[16:17], s[8:9]
	s_mov_b32 m0, s35
	s_add_i32 s38, s35, 0x4000
	global_load_lds_dwordx4 v1, s[16:17]
	v_lshlrev_b32_e32 v1, 10, v7
	v_and_or_b32 v1, v1, s36, v135
	v_mov_b32_e32 v2, v1
	s_mov_b64 s[16:17], s[8:9]
	s_mov_b32 m0, s37
	s_add_i32 s39, s35, 0x6000
	global_load_lds_dwordx4 v2, s[16:17]
	v_bfe_u32 v2, v128, 16, 16
	v_lshl_or_b32 v2, v2, 10, v135
	s_mov_b64 s[16:17], s[8:9]
	s_mov_b32 m0, s38
	s_cmp_eq_u32 s20, 1
	global_load_lds_dwordx4 v2, s[16:17]
	v_bfe_u32 v2, v129, 16, 16
	v_lshl_or_b32 v2, v2, 10, v135
	s_mov_b64 s[16:17], s[8:9]
	s_mov_b32 m0, s39
	s_nop 0
	global_load_lds_dwordx4 v2, s[16:17]
	s_cselect_b64 s[16:17], -1, 0
	s_cmp_lg_u32 s20, 1
	s_cbranch_scc1 .LBB0_2430
	s_barrier

.LBB0_2433:
	s_add_i32 s53, s53, 1
	s_mul_i32 s0, s53, s33
	s_add_i32 s14, s44, s0
	s_cmp_lt_i32 s14, s29
	s_cselect_b64 s[20:21], -1, 0
	s_ashr_i32 s54, s14, 1
	s_cmp_ge_i32 s14, s29
	s_cbranch_scc1 .LBB0_2443
	v_mbcnt_lo_u32_b32 v0, -1, 0
	v_mbcnt_hi_u32_b32 v0, -1, v0
	s_lshl_b32 s0, s54, 2
	v_add_u32_e32 v0, s30, v0
	s_add_i32 s0, s3, s0
	v_ashrrev_i32_e32 v2, 31, v0
	v_lshrrev_b32_e32 v2, 26, v2
	v_lshlrev_b32_e32 v1, 4, v0
	v_add_u32_e32 v2, v0, v2
	v_bfe_i32 v0, v0, 27, 1
	v_lshrrev_b32_e32 v0, 22, v0
	v_add_u32_e32 v0, v1, v0
	v_and_b32_e32 v0, 0xfffffc00, v0
	v_sub_u32_e32 v3, v1, v0
	v_ashrrev_i32_e32 v2, 6, v2
	v_lshrrev_b32_e32 v0, 4, v3
	v_and_b32_e32 v4, 32, v0
	v_lshlrev_b32_e32 v0, 3, v2
	v_and_b32_e32 v2, -16, v0
	v_mov_b32_e32 v0, s0
	ds_read2_b32 v[0:1], v0 offset0:64 offset1:224
	v_ashrrev_i32_e32 v5, 31, v3
	v_lshrrev_b32_e32 v5, 26, v5
	v_xad_u32 v3, v4, v3, v5
	v_ashrrev_i32_e32 v3, 6, v3
	s_waitcnt lgkmcnt(0)
	v_lshlrev_b32_e32 v4, 2, v0
	v_add_u32_e32 v4, s3, v4
	ds_read_b32 v8, v4 offset:4
	v_ashrrev_i32_e32 v5, 31, v0
	v_mov_b32_e32 v4, v0
	v_add3_u32 v2, v3, v2, v1
	v_lshlrev_b64 v[0:1], 16, v[4:5]
	v_lshl_add_u64 v[0:1], s[6:7], 0, v[0:1]
	s_waitcnt lgkmcnt(0)
	v_cmp_lt_i32_e32 vcc, v2, v8
	v_mov_b32_e32 v7, 0
	v_mov_b32_e32 v6, 0
	v_mov_b32_e32 v240, 0
	v_mov_b32_e32 v241, 0
	v_mov_b32_e32 v242, 0
	v_mov_b32_e32 v243, 0
	s_and_saveexec_b64 s[0:1], vcc
	s_cbranch_execz .LBB0_2436
	v_ashrrev_i32_e32 v3, 31, v2
	v_lshl_add_u64 v[4:5], v[2:3], 2, v[0:1]
	global_load_dword v240, v[4:5], off

.LBB0_2446:
	ds_read_b128 v[144:147], v137
	ds_read_b128 v[148:151], v137 offset:1024
	ds_read_b128 v[152:155], v137 offset:2048
	ds_read_b128 v[156:159], v137 offset:3072
	ds_read_b128 v[160:163], v138
	ds_read_b128 v[164:167], v138 offset:1024
	ds_read_b128 v[168:171], v138 offset:2048
	ds_read_b128 v[172:175], v138 offset:3072
	s_cmp_eq_u32 s60, 4
	s_cselect_b64 vcc, -1, 0
	s_and_b64 s[22:23], vcc, exec
	s_cselect_b32 s26, s8, s58
	s_cselect_b32 s27, s9, s59
	s_cselect_b32 s24, s20, s14
	s_cselect_b32 s25, s21, s57
	s_add_u32 s22, s26, 0x80
	s_addc_u32 s23, s27, 0
	s_add_u32 s62, s58, 0xffffff80
	s_addc_u32 s63, s59, -1
	v_mov_b32_e32 v132, v130
	s_mov_b32 m0, s50
	ds_read_b128 v[176:179], v139
	ds_read_b128 v[180:183], v139 offset:1024
	ds_read_b128 v[184:187], v139 offset:2048
	ds_read_b128 v[188:191], v139 offset:3072
	ds_read_b128 v[192:195], v139 offset:4096
	ds_read_b128 v[196:199], v139 offset:5120
	ds_read_b128 v[200:203], v139 offset:6144
	ds_read_b128 v[204:207], v139 offset:7168
	s_mov_b64 s[64:65], s[62:63]
	s_nop 0
	global_load_lds_dwordx4 v132, s[64:65]
	v_mov_b32_e32 v132, v131
	s_mov_b32 m0, s51
	s_nop 0
	global_load_lds_dwordx4 v132, s[62:63]
	s_waitcnt vmcnt(8)
	s_waitcnt lgkmcnt(0)
	s_barrier
	s_setprio 3
	v_mfma_f32_16x16x128_f8f6f4 v[124:127], v[144:151], v[176:183], v[124:127]
	v_mfma_f32_16x16x128_f8f6f4 v[116:119], v[152:159], v[176:183], v[116:119]
	v_mfma_f32_16x16x128_f8f6f4 v[108:111], v[144:151], v[184:191], v[108:111]
	v_mfma_f32_16x16x128_f8f6f4 v[100:103], v[152:159], v[184:191], v[100:103]
	v_mfma_f32_16x16x128_f8f6f4 v[92:95], v[144:151], v[192:199], v[92:95]
	v_mfma_f32_16x16x128_f8f6f4 v[84:87], v[152:159], v[192:199], v[84:87]
	v_mfma_f32_16x16x128_f8f6f4 v[76:79], v[144:151], v[200:207], v[76:79]
	v_mfma_f32_16x16x128_f8f6f4 v[68:71], v[152:159], v[200:207], v[68:71]
	v_mfma_f32_16x16x128_f8f6f4 v[120:123], v[160:167], v[176:183], v[120:123]
	v_mfma_f32_16x16x128_f8f6f4 v[112:115], v[168:175], v[176:183], v[112:115]
	v_mfma_f32_16x16x128_f8f6f4 v[104:107], v[160:167], v[184:191], v[104:107]
	v_mfma_f32_16x16x128_f8f6f4 v[96:99], v[168:175], v[184:191], v[96:99]
	v_mfma_f32_16x16x128_f8f6f4 v[88:91], v[160:167], v[192:199], v[88:91]
	v_mfma_f32_16x16x128_f8f6f4 v[80:83], v[168:175], v[192:199], v[80:83]
	v_mfma_f32_16x16x128_f8f6f4 v[72:75], v[160:167], v[200:207], v[72:75]
	v_mfma_f32_16x16x128_f8f6f4 v[64:67], v[168:175], v[200:207], v[64:67]
	s_setprio 0
	s_barrier
	v_mov_b32_e32 v132, v134
	s_mov_b64 s[62:63], s[24:25]
	s_mov_b32 m0, s52
	ds_read_b128 v[176:179], v139 offset:16384
	ds_read_b128 v[180:183], v139 offset:17408
	ds_read_b128 v[184:187], v139 offset:18432
	ds_read_b128 v[188:191], v139 offset:19456
	ds_read_b128 v[192:195], v139 offset:20480
	ds_read_b128 v[196:199], v139 offset:21504
	ds_read_b128 v[200:203], v139 offset:22528
	ds_read_b128 v[204:207], v139 offset:23552
	s_nop 0
	global_load_lds_dwordx4 v132, s[62:63]
	s_add_u32 s62, s24, 0x10000
	v_mov_b32_e32 v132, v134
	s_addc_u32 s63, s25, 0
	s_add_i32 m0, s52, 0x2000
	s_nop 0
	global_load_lds_dwordx4 v132, s[62:63]
	s_add_u32 s62, s24, 0x20000
	v_mov_b32_e32 v132, v134
	s_addc_u32 s63, s25, 0
	s_add_i32 s61, s45, s34
	s_mov_b32 m0, s61
	s_nop 0
	global_load_lds_dwordx4 v132, s[62:63]
	v_mov_b32_e32 v132, v134
	s_add_u32 s62, s24, 0x30000
	s_addc_u32 s63, s25, 0
	s_add_i32 m0, s61, 0x2000
	s_nop 0
	global_load_lds_dwordx4 v132, s[62:63]
	v_cndmask_b32_e32 v132, v128, v141, vcc
	v_lshlrev_b32_e32 v133, 10, v132
	v_and_or_b32 v133, v133, s36, v135
	v_mov_b32_e32 v143, v133
	s_mov_b64 s[62:63], s[26:27]
	s_mov_b32 m0, s35
	s_nop 0
	global_load_lds_dwordx4 v143, s[62:63]
	v_cndmask_b32_e32 v143, v129, v142, vcc
	v_lshlrev_b32_e32 v208, 10, v143
	v_and_or_b32 v208, v208, s36, v135
	v_mov_b32_e32 v209, v208
	s_mov_b64 s[62:63], s[26:27]
	s_mov_b32 m0, s37
	s_nop 0
	global_load_lds_dwordx4 v209, s[62:63]
	s_waitcnt vmcnt(8)
	s_waitcnt lgkmcnt(0)
	s_barrier
	s_setprio 3
	v_mfma_f32_16x16x128_f8f6f4 v[60:63], v[144:151], v[176:183], v[60:63]
	v_mfma_f32_16x16x128_f8f6f4 v[52:55], v[152:159], v[176:183], v[52:55]
	v_mfma_f32_16x16x128_f8f6f4 v[44:47], v[144:151], v[184:191], v[44:47]
	v_mfma_f32_16x16x128_f8f6f4 v[36:39], v[152:159], v[184:191], v[36:39]
	v_mfma_f32_16x16x128_f8f6f4 v[28:31], v[144:151], v[192:199], v[28:31]
	v_mfma_f32_16x16x128_f8f6f4 v[20:23], v[152:159], v[192:199], v[20:23]
	v_mfma_f32_16x16x128_f8f6f4 v[12:15], v[144:151], v[200:207], v[12:15]
	v_mfma_f32_16x16x128_f8f6f4 v[4:7], v[152:159], v[200:207], v[4:7]
	v_mfma_f32_16x16x128_f8f6f4 v[56:59], v[160:167], v[176:183], v[56:59]
	v_mfma_f32_16x16x128_f8f6f4 v[48:51], v[168:175], v[176:183], v[48:51]
	v_mfma_f32_16x16x128_f8f6f4 v[40:43], v[160:167], v[184:191], v[40:43]
	v_mfma_f32_16x16x128_f8f6f4 v[32:35], v[168:175], v[184:191], v[32:35]
	v_mfma_f32_16x16x128_f8f6f4 v[24:27], v[160:167], v[192:199], v[24:27]
	v_mfma_f32_16x16x128_f8f6f4 v[16:19], v[168:175], v[192:199], v[16:19]
	v_mfma_f32_16x16x128_f8f6f4 v[8:11], v[160:167], v[200:207], v[8:11]
	v_mfma_f32_16x16x128_f8f6f4 v[0:3], v[168:175], v[200:207], v[0:3]
	s_setprio 0
	s_barrier
	s_add_i32 s61, 0, 0x18000
	s_add_i32 s64, 0, 0x1c000
	v_add_u32_e32 v156, s61, v136
	v_add_u32_e32 v172, s64, v136
	ds_read_b128 v[144:147], v156
	ds_read_b128 v[148:151], v156 offset:1024
	ds_read_b128 v[152:155], v156 offset:2048
	ds_read_b128 v[156:159], v156 offset:3072
	ds_read_b128 v[160:163], v172
	ds_read_b128 v[164:167], v172 offset:1024
	ds_read_b128 v[168:171], v172 offset:2048
	ds_read_b128 v[172:175], v172 offset:3072
	v_bfe_u32 v132, v132, 16, 16
	v_lshl_or_b32 v132, v132, 10, v135
	s_mov_b32 m0, s38
	ds_read_b128 v[176:179], v139 offset:32768
	ds_read_b128 v[180:183], v139 offset:33792
	ds_read_b128 v[184:187], v139 offset:34816
	ds_read_b128 v[188:191], v139 offset:35840
	ds_read_b128 v[192:195], v139 offset:36864
	ds_read_b128 v[196:199], v139 offset:37888
	ds_read_b128 v[200:203], v139 offset:38912
	ds_read_b128 v[204:207], v139 offset:39936
	s_mov_b64 s[62:63], s[26:27]
	s_nop 0
	global_load_lds_dwordx4 v132, s[62:63]
	v_bfe_u32 v132, v143, 16, 16
	v_lshl_or_b32 v132, v132, 10, v135
	s_mov_b32 m0, s39
	s_nop 0
	global_load_lds_dwordx4 v132, s[26:27]
	s_waitcnt vmcnt(8)
	s_waitcnt lgkmcnt(0)
	s_barrier
	s_setprio 3
	v_mfma_f32_16x16x128_f8f6f4 v[124:127], v[144:151], v[176:183], v[124:127]
	v_mfma_f32_16x16x128_f8f6f4 v[116:119], v[152:159], v[176:183], v[116:119]
	v_mfma_f32_16x16x128_f8f6f4 v[108:111], v[144:151], v[184:191], v[108:111]
	v_mfma_f32_16x16x128_f8f6f4 v[100:103], v[152:159], v[184:191], v[100:103]
	v_mfma_f32_16x16x128_f8f6f4 v[92:95], v[144:151], v[192:199], v[92:95]
	v_mfma_f32_16x16x128_f8f6f4 v[84:87], v[152:159], v[192:199], v[84:87]
	v_mfma_f32_16x16x128_f8f6f4 v[76:79], v[144:151], v[200:207], v[76:79]
	v_mfma_f32_16x16x128_f8f6f4 v[68:71], v[152:159], v[200:207], v[68:71]
	v_mfma_f32_16x16x128_f8f6f4 v[120:123], v[160:167], v[176:183], v[120:123]
	v_mfma_f32_16x16x128_f8f6f4 v[112:115], v[168:175], v[176:183], v[112:115]
	v_mfma_f32_16x16x128_f8f6f4 v[104:107], v[160:167], v[184:191], v[104:107]
	v_mfma_f32_16x16x128_f8f6f4 v[96:99], v[168:175], v[184:191], v[96:99]
	v_mfma_f32_16x16x128_f8f6f4 v[88:91], v[160:167], v[192:199], v[88:91]
	v_mfma_f32_16x16x128_f8f6f4 v[80:83], v[168:175], v[192:199], v[80:83]
	v_mfma_f32_16x16x128_f8f6f4 v[72:75], v[160:167], v[200:207], v[72:75]
	v_mfma_f32_16x16x128_f8f6f4 v[64:67], v[168:175], v[200:207], v[64:67]
	s_setprio 0
	s_barrier
	s_add_u32 s26, s24, 0x80
	s_addc_u32 s27, s25, 0
	v_mov_b32_e32 v132, v134
	s_add_i32 s61, s61, s34
	ds_read_b128 v[176:179], v139 offset:49152
	ds_read_b128 v[180:183], v139 offset:50176
	ds_read_b128 v[184:187], v139 offset:51200
	ds_read_b128 v[188:191], v139 offset:52224
	ds_read_b128 v[192:195], v139 offset:53248
	ds_read_b128 v[196:199], v139 offset:54272
	ds_read_b128 v[200:203], v139 offset:55296
	ds_read_b128 v[204:207], v139 offset:56320
	s_mov_b32 m0, s61
	s_nop 0
	global_load_lds_dwordx4 v132, s[26:27]
	s_add_u32 s26, s24, 0x10080
	v_mov_b32_e32 v132, v134
	s_addc_u32 s27, s25, 0
	s_add_i32 m0, s61, 0x2000
	s_nop 0
	global_load_lds_dwordx4 v132, s[26:27]
	s_add_u32 s26, s24, 0x20080
	v_mov_b32_e32 v132, v134
	s_addc_u32 s27, s25, 0
	s_add_i32 s61, s64, s34
	s_mov_b32 m0, s61
	s_add_u32 s24, s24, 0x30080
	s_addc_u32 s25, s25, 0
	global_load_lds_dwordx4 v132, s[26:27]
	v_mov_b32_e32 v132, v134
	s_add_i32 m0, s61, 0x2000
	s_nop 0
	global_load_lds_dwordx4 v132, s[24:25]
	s_mov_b64 s[24:25], s[22:23]
	s_mov_b32 m0, s42
	s_nop 0
	global_load_lds_dwordx4 v133, s[24:25]
	s_mov_b32 m0, s43
	s_nop 0
	global_load_lds_dwordx4 v208, s[22:23]
	s_waitcnt vmcnt(8)
	s_waitcnt lgkmcnt(0)
	s_barrier
	s_setprio 3
	v_mfma_f32_16x16x128_f8f6f4 v[60:63], v[144:151], v[176:183], v[60:63]
	v_mfma_f32_16x16x128_f8f6f4 v[52:55], v[152:159], v[176:183], v[52:55]
	v_mfma_f32_16x16x128_f8f6f4 v[44:47], v[144:151], v[184:191], v[44:47]
	v_mfma_f32_16x16x128_f8f6f4 v[36:39], v[152:159], v[184:191], v[36:39]
	v_mfma_f32_16x16x128_f8f6f4 v[28:31], v[144:151], v[192:199], v[28:31]
	v_mfma_f32_16x16x128_f8f6f4 v[20:23], v[152:159], v[192:199], v[20:23]
	v_mfma_f32_16x16x128_f8f6f4 v[12:15], v[144:151], v[200:207], v[12:15]
	v_mfma_f32_16x16x128_f8f6f4 v[4:7], v[152:159], v[200:207], v[4:7]
	v_mfma_f32_16x16x128_f8f6f4 v[56:59], v[160:167], v[176:183], v[56:59]
	v_mfma_f32_16x16x128_f8f6f4 v[48:51], v[168:175], v[176:183], v[48:51]
	v_mfma_f32_16x16x128_f8f6f4 v[40:43], v[160:167], v[184:191], v[40:43]
	v_mfma_f32_16x16x128_f8f6f4 v[32:35], v[168:175], v[184:191], v[32:35]
	v_mfma_f32_16x16x128_f8f6f4 v[24:27], v[160:167], v[192:199], v[24:27]
	v_mfma_f32_16x16x128_f8f6f4 v[16:19], v[168:175], v[192:199], v[16:19]
	v_mfma_f32_16x16x128_f8f6f4 v[8:11], v[160:167], v[200:207], v[8:11]
	v_mfma_f32_16x16x128_f8f6f4 v[0:3], v[168:175], v[200:207], v[0:3]
	s_setprio 0
	s_barrier
	s_add_i32 s60, s60, 2
	s_add_u32 s14, s14, 0x100
	s_addc_u32 s57, s57, 0
	s_add_u32 s58, s58, 0x100
	s_addc_u32 s59, s59, 0
	s_cmp_gt_u32 s60, 5
	s_cbranch_scc0 .LBB0_2446
	s_and_b64 vcc, exec, s[18:19]
	s_cbranch_vccz .LBB0_2449
	s_barrier
.LBB0_2449:
	s_mov_b32 s14, 0
	s_lshl_b32 s14, s31, 2
	s_add_i32 s14, s3, s14
	v_mbcnt_lo_u32_b32 v146, -1, 0
	v_mbcnt_hi_u32_b32 v146, -1, v146
	v_mov_b32_e32 v128, s14
	ds_read2_b32 v[128:129], v128 offset0:64 offset1:224
	v_and_b32_e32 v143, 15, v146
	v_or_b32_e32 v144, s40, v143
	v_mov_b32_e32 v147, 0
	s_waitcnt lgkmcnt(0)
	v_lshlrev_b32_e32 v130, 2, v128
	v_add_u32_e32 v130, s3, v130
	ds_read_b32 v145, v130 offset:4
	v_ashrrev_i32_e32 v133, 31, v128
	v_mov_b32_e32 v132, v128
	v_add_u32_e32 v130, v129, v144
	v_lshlrev_b64 v[132:133], 16, v[132:133]
	s_waitcnt lgkmcnt(0)
	v_cmp_lt_i32_e32 vcc, v130, v145
	v_mov_b32_e32 v128, 0
	v_lshl_add_u64 v[132:133], s[10:11], 0, v[132:133]
	v_ashrrev_i32_e32 v131, 31, v130
	v_bfe_u32 v148, v146, 4, 2
	s_lshl_b32 s14, s56, 7
	v_lshl_add_u64 v[152:153], v[130:131], 2, v[132:133]
	v_lshl_or_b32 v149, v148, 3, s14
	global_load_dword v154, v[152:153], off
	global_load_dword v155, v[152:153], off offset:64
	global_load_dword v156, v[152:153], off offset:128
	global_load_dword v157, v[152:153], off offset:192
	global_load_dword v158, v[152:153], off offset:512
	global_load_dword v159, v[152:153], off offset:576
	global_load_dword v160, v[152:153], off offset:640
	global_load_dword v161, v[152:153], off offset:704
	s_lshl_b32 s14, s31, 8
	v_or_b32_e32 v149, s41, v149
	v_add_u32_e32 v150, s14, v144
	v_lshl_add_u32 v150, v150, 8, v149
	v_cmp_lt_i32_e32 vcc, v130, v145
	s_waitcnt vmcnt(7)
	v_mul_f32_e32 v163, 0x3c800000, v154
	v_mul_f32_e32 v164, 0xbd38aa3b, v124
	v_mul_f32_e32 v165, 0xbd38aa3b, v125
	v_mul_f32_e32 v166, 0xbd38aa3b, v126
	v_mul_f32_e32 v167, 0xbd38aa3b, v127
	v_mul_f32_e32 v168, 0xbd38aa3b, v116
	v_mul_f32_e32 v169, 0xbd38aa3b, v117
	v_mul_f32_e32 v170, 0xbd38aa3b, v118
	v_mul_f32_e32 v171, 0xbd38aa3b, v119
	v_exp_f32_e32 v164, v164
	v_exp_f32_e32 v165, v165
	v_exp_f32_e32 v166, v166
	v_exp_f32_e32 v167, v167
	v_exp_f32_e32 v168, v168
	v_exp_f32_e32 v169, v169
	v_exp_f32_e32 v170, v170
	v_exp_f32_e32 v171, v171
	v_add_f32_e32 v164, 1.0, v164
	v_add_f32_e32 v165, 1.0, v165
	v_add_f32_e32 v166, 1.0, v166
	v_add_f32_e32 v167, 1.0, v167
	v_add_f32_e32 v168, 1.0, v168
	v_add_f32_e32 v169, 1.0, v169
	v_add_f32_e32 v170, 1.0, v170
	v_add_f32_e32 v171, 1.0, v171
	v_rcp_f32_e32 v164, v164
	v_rcp_f32_e32 v165, v165
	v_rcp_f32_e32 v166, v166
	v_rcp_f32_e32 v167, v167
	v_rcp_f32_e32 v168, v168
	v_rcp_f32_e32 v169, v169
	v_rcp_f32_e32 v170, v170
	v_rcp_f32_e32 v171, v171
	v_mul_f32_e32 v164, v124, v164
	v_mul_f32_e32 v165, v125, v165
	v_mul_f32_e32 v166, v126, v166
	v_mul_f32_e32 v167, v127, v167
	v_mul_f32_e32 v168, v116, v168
	v_mul_f32_e32 v169, v117, v169
	v_mul_f32_e32 v170, v118, v170
	v_mul_f32_e32 v171, v119, v171
	v_mul_f32_e32 v164, v164, v120
	v_mul_f32_e32 v165, v165, v121
	v_mul_f32_e32 v166, v166, v122
	v_mul_f32_e32 v167, v167, v123
	v_mul_f32_e32 v168, v168, v112
	v_mul_f32_e32 v169, v169, v113
	v_mul_f32_e32 v170, v170, v114
	v_mul_f32_e32 v171, v171, v115
	v_mul_f32_e32 v164, v164, v163
	v_mul_f32_e32 v165, v165, v163
	v_mul_f32_e32 v166, v166, v163
	v_mul_f32_e32 v167, v167, v163
	v_mul_f32_e32 v168, v168, v163
	v_mul_f32_e32 v169, v169, v163
	v_mul_f32_e32 v170, v170, v163
	v_mul_f32_e32 v171, v171, v163
	v_max_f32_e32 v164, 0xc3e00000, v164
	v_max_f32_e32 v165, 0xc3e00000, v165
	v_max_f32_e32 v166, 0xc3e00000, v166
	v_max_f32_e32 v167, 0xc3e00000, v167
	v_max_f32_e32 v168, 0xc3e00000, v168
	v_max_f32_e32 v169, 0xc3e00000, v169
	v_max_f32_e32 v170, 0xc3e00000, v170
	v_max_f32_e32 v171, 0xc3e00000, v171
	v_min_f32_e32 v164, 0x43e00000, v164
	v_min_f32_e32 v165, 0x43e00000, v165
	v_min_f32_e32 v166, 0x43e00000, v166
	v_min_f32_e32 v167, 0x43e00000, v167
	v_min_f32_e32 v168, 0x43e00000, v168
	v_min_f32_e32 v169, 0x43e00000, v169
	v_min_f32_e32 v170, 0x43e00000, v170
	v_min_f32_e32 v171, 0x43e00000, v171
	v_cndmask_b32_e32 v164, 0, v164, vcc
	v_cndmask_b32_e32 v165, 0, v165, vcc
	v_cndmask_b32_e32 v166, 0, v166, vcc
	v_cndmask_b32_e32 v167, 0, v167, vcc
	v_cndmask_b32_e32 v168, 0, v168, vcc
	v_cndmask_b32_e32 v169, 0, v169, vcc
	v_cndmask_b32_e32 v170, 0, v170, vcc
	v_cndmask_b32_e32 v171, 0, v171, vcc
	v_mov_b32_e32 v188, 0
	v_mov_b32_e32 v189, 0
	v_cvt_pk_fp8_f32 v188, v164, v165
	v_cvt_pk_fp8_f32 v189, v168, v169
	v_mov_b32_e32 v192, v150
	v_cvt_pk_fp8_f32 v188, v166, v167 op_sel:[0,0,1]
	v_cvt_pk_fp8_f32 v189, v170, v171 op_sel:[0,0,1]
	s_nop 1
	global_store_dwordx2 v192, v[188:189], s[12:13] sc1
	v_add_u32_e32 v162, 0x10, v130
	v_cmp_lt_i32_e32 vcc, v162, v145
	s_waitcnt vmcnt(7)
	v_mul_f32_e32 v163, 0x3c800000, v155
	v_mul_f32_e32 v164, 0xbd38aa3b, v108
	v_mul_f32_e32 v165, 0xbd38aa3b, v109
	v_mul_f32_e32 v166, 0xbd38aa3b, v110
	v_mul_f32_e32 v167, 0xbd38aa3b, v111
	v_mul_f32_e32 v168, 0xbd38aa3b, v100
	v_mul_f32_e32 v169, 0xbd38aa3b, v101
	v_mul_f32_e32 v170, 0xbd38aa3b, v102
	v_mul_f32_e32 v171, 0xbd38aa3b, v103
	v_exp_f32_e32 v164, v164
	v_exp_f32_e32 v165, v165
	v_exp_f32_e32 v166, v166
	v_exp_f32_e32 v167, v167
	v_exp_f32_e32 v168, v168
	v_exp_f32_e32 v169, v169
	v_exp_f32_e32 v170, v170
	v_exp_f32_e32 v171, v171
	v_add_f32_e32 v164, 1.0, v164
	v_add_f32_e32 v165, 1.0, v165
	v_add_f32_e32 v166, 1.0, v166
	v_add_f32_e32 v167, 1.0, v167
	v_add_f32_e32 v168, 1.0, v168
	v_add_f32_e32 v169, 1.0, v169
	v_add_f32_e32 v170, 1.0, v170
	v_add_f32_e32 v171, 1.0, v171
	v_rcp_f32_e32 v164, v164
	v_rcp_f32_e32 v165, v165
	v_rcp_f32_e32 v166, v166
	v_rcp_f32_e32 v167, v167
	v_rcp_f32_e32 v168, v168
	v_rcp_f32_e32 v169, v169
	v_rcp_f32_e32 v170, v170
	v_rcp_f32_e32 v171, v171
	v_mul_f32_e32 v164, v108, v164
	v_mul_f32_e32 v165, v109, v165
	v_mul_f32_e32 v166, v110, v166
	v_mul_f32_e32 v167, v111, v167
	v_mul_f32_e32 v168, v100, v168
	v_mul_f32_e32 v169, v101, v169
	v_mul_f32_e32 v170, v102, v170
	v_mul_f32_e32 v171, v103, v171
	v_mul_f32_e32 v164, v164, v104
	v_mul_f32_e32 v165, v165, v105
	v_mul_f32_e32 v166, v166, v106
	v_mul_f32_e32 v167, v167, v107
	v_mul_f32_e32 v168, v168, v96
	v_mul_f32_e32 v169, v169, v97
	v_mul_f32_e32 v170, v170, v98
	v_mul_f32_e32 v171, v171, v99
	v_mul_f32_e32 v164, v164, v163
	v_mul_f32_e32 v165, v165, v163
	v_mul_f32_e32 v166, v166, v163
	v_mul_f32_e32 v167, v167, v163
	v_mul_f32_e32 v168, v168, v163
	v_mul_f32_e32 v169, v169, v163
	v_mul_f32_e32 v170, v170, v163
	v_mul_f32_e32 v171, v171, v163
	v_max_f32_e32 v164, 0xc3e00000, v164
	v_max_f32_e32 v165, 0xc3e00000, v165
	v_max_f32_e32 v166, 0xc3e00000, v166
	v_max_f32_e32 v167, 0xc3e00000, v167
	v_max_f32_e32 v168, 0xc3e00000, v168
	v_max_f32_e32 v169, 0xc3e00000, v169
	v_max_f32_e32 v170, 0xc3e00000, v170
	v_max_f32_e32 v171, 0xc3e00000, v171
	v_min_f32_e32 v164, 0x43e00000, v164
	v_min_f32_e32 v165, 0x43e00000, v165
	v_min_f32_e32 v166, 0x43e00000, v166
	v_min_f32_e32 v167, 0x43e00000, v167
	v_min_f32_e32 v168, 0x43e00000, v168
	v_min_f32_e32 v169, 0x43e00000, v169
	v_min_f32_e32 v170, 0x43e00000, v170
	v_min_f32_e32 v171, 0x43e00000, v171
	v_cndmask_b32_e32 v164, 0, v164, vcc
	v_cndmask_b32_e32 v165, 0, v165, vcc
	v_cndmask_b32_e32 v166, 0, v166, vcc
	v_cndmask_b32_e32 v167, 0, v167, vcc
	v_cndmask_b32_e32 v168, 0, v168, vcc
	v_cndmask_b32_e32 v169, 0, v169, vcc
	v_cndmask_b32_e32 v170, 0, v170, vcc
	v_cndmask_b32_e32 v171, 0, v171, vcc
	v_mov_b32_e32 v190, 0
	v_mov_b32_e32 v191, 0
	v_cvt_pk_fp8_f32 v190, v164, v165
	v_cvt_pk_fp8_f32 v191, v168, v169
	v_add_u32_e32 v192, 0x1000, v150
	v_cvt_pk_fp8_f32 v190, v166, v167 op_sel:[0,0,1]
	v_cvt_pk_fp8_f32 v191, v170, v171 op_sel:[0,0,1]
	s_nop 1
	global_store_dwordx2 v192, v[190:191], s[12:13] sc1
	v_add_u32_e32 v162, 0x20, v130
	v_cmp_lt_i32_e32 vcc, v162, v145
	s_waitcnt vmcnt(7)
	v_mul_f32_e32 v163, 0x3c800000, v156
	v_mul_f32_e32 v164, 0xbd38aa3b, v92
	v_mul_f32_e32 v165, 0xbd38aa3b, v93
	v_mul_f32_e32 v166, 0xbd38aa3b, v94
	v_mul_f32_e32 v167, 0xbd38aa3b, v95
	v_mul_f32_e32 v168, 0xbd38aa3b, v84
	v_mul_f32_e32 v169, 0xbd38aa3b, v85
	v_mul_f32_e32 v170, 0xbd38aa3b, v86
	v_mul_f32_e32 v171, 0xbd38aa3b, v87
	v_exp_f32_e32 v164, v164
	v_exp_f32_e32 v165, v165
	v_exp_f32_e32 v166, v166
	v_exp_f32_e32 v167, v167
	v_exp_f32_e32 v168, v168
	v_exp_f32_e32 v169, v169
	v_exp_f32_e32 v170, v170
	v_exp_f32_e32 v171, v171
	v_add_f32_e32 v164, 1.0, v164
	v_add_f32_e32 v165, 1.0, v165
	v_add_f32_e32 v166, 1.0, v166
	v_add_f32_e32 v167, 1.0, v167
	v_add_f32_e32 v168, 1.0, v168
	v_add_f32_e32 v169, 1.0, v169
	v_add_f32_e32 v170, 1.0, v170
	v_add_f32_e32 v171, 1.0, v171
	v_rcp_f32_e32 v164, v164
	v_rcp_f32_e32 v165, v165
	v_rcp_f32_e32 v166, v166
	v_rcp_f32_e32 v167, v167
	v_rcp_f32_e32 v168, v168
	v_rcp_f32_e32 v169, v169
	v_rcp_f32_e32 v170, v170
	v_rcp_f32_e32 v171, v171
	v_mul_f32_e32 v164, v92, v164
	v_mul_f32_e32 v165, v93, v165
	v_mul_f32_e32 v166, v94, v166
	v_mul_f32_e32 v167, v95, v167
	v_mul_f32_e32 v168, v84, v168
	v_mul_f32_e32 v169, v85, v169
	v_mul_f32_e32 v170, v86, v170
	v_mul_f32_e32 v171, v87, v171
	v_mul_f32_e32 v164, v164, v88
	v_mul_f32_e32 v165, v165, v89
	v_mul_f32_e32 v166, v166, v90
	v_mul_f32_e32 v167, v167, v91
	v_mul_f32_e32 v168, v168, v80
	v_mul_f32_e32 v169, v169, v81
	v_mul_f32_e32 v170, v170, v82
	v_mul_f32_e32 v171, v171, v83
	v_mul_f32_e32 v164, v164, v163
	v_mul_f32_e32 v165, v165, v163
	v_mul_f32_e32 v166, v166, v163
	v_mul_f32_e32 v167, v167, v163
	v_mul_f32_e32 v168, v168, v163
	v_mul_f32_e32 v169, v169, v163
	v_mul_f32_e32 v170, v170, v163
	v_mul_f32_e32 v171, v171, v163
	v_max_f32_e32 v164, 0xc3e00000, v164
	v_max_f32_e32 v165, 0xc3e00000, v165
	v_max_f32_e32 v166, 0xc3e00000, v166
	v_max_f32_e32 v167, 0xc3e00000, v167
	v_max_f32_e32 v168, 0xc3e00000, v168
	v_max_f32_e32 v169, 0xc3e00000, v169
	v_max_f32_e32 v170, 0xc3e00000, v170
	v_max_f32_e32 v171, 0xc3e00000, v171
	v_min_f32_e32 v164, 0x43e00000, v164
	v_min_f32_e32 v165, 0x43e00000, v165
	v_min_f32_e32 v166, 0x43e00000, v166
	v_min_f32_e32 v167, 0x43e00000, v167
	v_min_f32_e32 v168, 0x43e00000, v168
	v_min_f32_e32 v169, 0x43e00000, v169
	v_min_f32_e32 v170, 0x43e00000, v170
	v_min_f32_e32 v171, 0x43e00000, v171
	v_cndmask_b32_e32 v164, 0, v164, vcc
	v_cndmask_b32_e32 v165, 0, v165, vcc
	v_cndmask_b32_e32 v166, 0, v166, vcc
	v_cndmask_b32_e32 v167, 0, v167, vcc
	v_cndmask_b32_e32 v168, 0, v168, vcc
	v_cndmask_b32_e32 v169, 0, v169, vcc
	v_cndmask_b32_e32 v170, 0, v170, vcc
	v_cndmask_b32_e32 v171, 0, v171, vcc
	v_mov_b32_e32 v188, 0
	v_mov_b32_e32 v189, 0
	v_cvt_pk_fp8_f32 v188, v164, v165
	v_cvt_pk_fp8_f32 v189, v168, v169
	v_add_u32_e32 v192, 0x2000, v150
	v_cvt_pk_fp8_f32 v188, v166, v167 op_sel:[0,0,1]
	v_cvt_pk_fp8_f32 v189, v170, v171 op_sel:[0,0,1]
	s_nop 1
	global_store_dwordx2 v192, v[188:189], s[12:13] sc1
	v_add_u32_e32 v162, 0x30, v130
	v_cmp_lt_i32_e32 vcc, v162, v145
	s_waitcnt vmcnt(7)
	v_mul_f32_e32 v163, 0x3c800000, v157
	v_mul_f32_e32 v164, 0xbd38aa3b, v76
	v_mul_f32_e32 v165, 0xbd38aa3b, v77
	v_mul_f32_e32 v166, 0xbd38aa3b, v78
	v_mul_f32_e32 v167, 0xbd38aa3b, v79
	v_mul_f32_e32 v168, 0xbd38aa3b, v68
	v_mul_f32_e32 v169, 0xbd38aa3b, v69
	v_mul_f32_e32 v170, 0xbd38aa3b, v70
	v_mul_f32_e32 v171, 0xbd38aa3b, v71
	v_exp_f32_e32 v164, v164
	v_exp_f32_e32 v165, v165
	v_exp_f32_e32 v166, v166
	v_exp_f32_e32 v167, v167
	v_exp_f32_e32 v168, v168
	v_exp_f32_e32 v169, v169
	v_exp_f32_e32 v170, v170
	v_exp_f32_e32 v171, v171
	v_add_f32_e32 v164, 1.0, v164
	v_add_f32_e32 v165, 1.0, v165
	v_add_f32_e32 v166, 1.0, v166
	v_add_f32_e32 v167, 1.0, v167
	v_add_f32_e32 v168, 1.0, v168
	v_add_f32_e32 v169, 1.0, v169
	v_add_f32_e32 v170, 1.0, v170
	v_add_f32_e32 v171, 1.0, v171
	v_rcp_f32_e32 v164, v164
	v_rcp_f32_e32 v165, v165
	v_rcp_f32_e32 v166, v166
	v_rcp_f32_e32 v167, v167
	v_rcp_f32_e32 v168, v168
	v_rcp_f32_e32 v169, v169
	v_rcp_f32_e32 v170, v170
	v_rcp_f32_e32 v171, v171
	v_mul_f32_e32 v164, v76, v164
	v_mul_f32_e32 v165, v77, v165
	v_mul_f32_e32 v166, v78, v166
	v_mul_f32_e32 v167, v79, v167
	v_mul_f32_e32 v168, v68, v168
	v_mul_f32_e32 v169, v69, v169
	v_mul_f32_e32 v170, v70, v170
	v_mul_f32_e32 v171, v71, v171
	v_mul_f32_e32 v164, v164, v72
	v_mul_f32_e32 v165, v165, v73
	v_mul_f32_e32 v166, v166, v74
	v_mul_f32_e32 v167, v167, v75
	v_mul_f32_e32 v168, v168, v64
	v_mul_f32_e32 v169, v169, v65
	v_mul_f32_e32 v170, v170, v66
	v_mul_f32_e32 v171, v171, v67
	v_mul_f32_e32 v164, v164, v163
	v_mul_f32_e32 v165, v165, v163
	v_mul_f32_e32 v166, v166, v163
	v_mul_f32_e32 v167, v167, v163
	v_mul_f32_e32 v168, v168, v163
	v_mul_f32_e32 v169, v169, v163
	v_mul_f32_e32 v170, v170, v163
	v_mul_f32_e32 v171, v171, v163
	v_max_f32_e32 v164, 0xc3e00000, v164
	v_max_f32_e32 v165, 0xc3e00000, v165
	v_max_f32_e32 v166, 0xc3e00000, v166
	v_max_f32_e32 v167, 0xc3e00000, v167
	v_max_f32_e32 v168, 0xc3e00000, v168
	v_max_f32_e32 v169, 0xc3e00000, v169
	v_max_f32_e32 v170, 0xc3e00000, v170
	v_max_f32_e32 v171, 0xc3e00000, v171
	v_min_f32_e32 v164, 0x43e00000, v164
	v_min_f32_e32 v165, 0x43e00000, v165
	v_min_f32_e32 v166, 0x43e00000, v166
	v_min_f32_e32 v167, 0x43e00000, v167
	v_min_f32_e32 v168, 0x43e00000, v168
	v_min_f32_e32 v169, 0x43e00000, v169
	v_min_f32_e32 v170, 0x43e00000, v170
	v_min_f32_e32 v171, 0x43e00000, v171
	v_cndmask_b32_e32 v164, 0, v164, vcc
	v_cndmask_b32_e32 v165, 0, v165, vcc
	v_cndmask_b32_e32 v166, 0, v166, vcc
	v_cndmask_b32_e32 v167, 0, v167, vcc
	v_cndmask_b32_e32 v168, 0, v168, vcc
	v_cndmask_b32_e32 v169, 0, v169, vcc
	v_cndmask_b32_e32 v170, 0, v170, vcc
	v_cndmask_b32_e32 v171, 0, v171, vcc
	v_mov_b32_e32 v190, 0
	v_mov_b32_e32 v191, 0
	v_cvt_pk_fp8_f32 v190, v164, v165
	v_cvt_pk_fp8_f32 v191, v168, v169
	v_add_u32_e32 v192, 0x3000, v150
	v_cvt_pk_fp8_f32 v190, v166, v167 op_sel:[0,0,1]
	v_cvt_pk_fp8_f32 v191, v170, v171 op_sel:[0,0,1]
	s_nop 1
	global_store_dwordx2 v192, v[190:191], s[12:13] sc1
	v_add_u32_e32 v162, 0x80, v130
	v_cmp_lt_i32_e32 vcc, v162, v145
	s_waitcnt vmcnt(7)
	v_mul_f32_e32 v163, 0x3c800000, v158
	v_mul_f32_e32 v164, 0xbd38aa3b, v60
	v_mul_f32_e32 v165, 0xbd38aa3b, v61
	v_mul_f32_e32 v166, 0xbd38aa3b, v62
	v_mul_f32_e32 v167, 0xbd38aa3b, v63
	v_mul_f32_e32 v168, 0xbd38aa3b, v52
	v_mul_f32_e32 v169, 0xbd38aa3b, v53
	v_mul_f32_e32 v170, 0xbd38aa3b, v54
	v_mul_f32_e32 v171, 0xbd38aa3b, v55
	v_exp_f32_e32 v164, v164
	v_exp_f32_e32 v165, v165
	v_exp_f32_e32 v166, v166
	v_exp_f32_e32 v167, v167
	v_exp_f32_e32 v168, v168
	v_exp_f32_e32 v169, v169
	v_exp_f32_e32 v170, v170
	v_exp_f32_e32 v171, v171
	v_add_f32_e32 v164, 1.0, v164
	v_add_f32_e32 v165, 1.0, v165
	v_add_f32_e32 v166, 1.0, v166
	v_add_f32_e32 v167, 1.0, v167
	v_add_f32_e32 v168, 1.0, v168
	v_add_f32_e32 v169, 1.0, v169
	v_add_f32_e32 v170, 1.0, v170
	v_add_f32_e32 v171, 1.0, v171
	v_rcp_f32_e32 v164, v164
	v_rcp_f32_e32 v165, v165
	v_rcp_f32_e32 v166, v166
	v_rcp_f32_e32 v167, v167
	v_rcp_f32_e32 v168, v168
	v_rcp_f32_e32 v169, v169
	v_rcp_f32_e32 v170, v170
	v_rcp_f32_e32 v171, v171
	v_mul_f32_e32 v164, v60, v164
	v_mul_f32_e32 v165, v61, v165
	v_mul_f32_e32 v166, v62, v166
	v_mul_f32_e32 v167, v63, v167
	v_mul_f32_e32 v168, v52, v168
	v_mul_f32_e32 v169, v53, v169
	v_mul_f32_e32 v170, v54, v170
	v_mul_f32_e32 v171, v55, v171
	v_mul_f32_e32 v164, v164, v56
	v_mul_f32_e32 v165, v165, v57
	v_mul_f32_e32 v166, v166, v58
	v_mul_f32_e32 v167, v167, v59
	v_mul_f32_e32 v168, v168, v48
	v_mul_f32_e32 v169, v169, v49
	v_mul_f32_e32 v170, v170, v50
	v_mul_f32_e32 v171, v171, v51
	v_mul_f32_e32 v164, v164, v163
	v_mul_f32_e32 v165, v165, v163
	v_mul_f32_e32 v166, v166, v163
	v_mul_f32_e32 v167, v167, v163
	v_mul_f32_e32 v168, v168, v163
	v_mul_f32_e32 v169, v169, v163
	v_mul_f32_e32 v170, v170, v163
	v_mul_f32_e32 v171, v171, v163
	v_max_f32_e32 v164, 0xc3e00000, v164
	v_max_f32_e32 v165, 0xc3e00000, v165
	v_max_f32_e32 v166, 0xc3e00000, v166
	v_max_f32_e32 v167, 0xc3e00000, v167
	v_max_f32_e32 v168, 0xc3e00000, v168
	v_max_f32_e32 v169, 0xc3e00000, v169
	v_max_f32_e32 v170, 0xc3e00000, v170
	v_max_f32_e32 v171, 0xc3e00000, v171
	v_min_f32_e32 v164, 0x43e00000, v164
	v_min_f32_e32 v165, 0x43e00000, v165
	v_min_f32_e32 v166, 0x43e00000, v166
	v_min_f32_e32 v167, 0x43e00000, v167
	v_min_f32_e32 v168, 0x43e00000, v168
	v_min_f32_e32 v169, 0x43e00000, v169
	v_min_f32_e32 v170, 0x43e00000, v170
	v_min_f32_e32 v171, 0x43e00000, v171
	v_cndmask_b32_e32 v164, 0, v164, vcc
	v_cndmask_b32_e32 v165, 0, v165, vcc
	v_cndmask_b32_e32 v166, 0, v166, vcc
	v_cndmask_b32_e32 v167, 0, v167, vcc
	v_cndmask_b32_e32 v168, 0, v168, vcc
	v_cndmask_b32_e32 v169, 0, v169, vcc
	v_cndmask_b32_e32 v170, 0, v170, vcc
	v_cndmask_b32_e32 v171, 0, v171, vcc
	v_mov_b32_e32 v188, 0
	v_mov_b32_e32 v189, 0
	v_cvt_pk_fp8_f32 v188, v164, v165
	v_cvt_pk_fp8_f32 v189, v168, v169
	v_add_u32_e32 v192, 0x8000, v150
	v_cvt_pk_fp8_f32 v188, v166, v167 op_sel:[0,0,1]
	v_cvt_pk_fp8_f32 v189, v170, v171 op_sel:[0,0,1]
	s_nop 1
	global_store_dwordx2 v192, v[188:189], s[12:13] sc1
	v_add_u32_e32 v162, 0x90, v130
	v_cmp_lt_i32_e32 vcc, v162, v145
	s_waitcnt vmcnt(7)
	v_mul_f32_e32 v163, 0x3c800000, v159
	v_mul_f32_e32 v164, 0xbd38aa3b, v44
	v_mul_f32_e32 v165, 0xbd38aa3b, v45
	v_mul_f32_e32 v166, 0xbd38aa3b, v46
	v_mul_f32_e32 v167, 0xbd38aa3b, v47
	v_mul_f32_e32 v168, 0xbd38aa3b, v36
	v_mul_f32_e32 v169, 0xbd38aa3b, v37
	v_mul_f32_e32 v170, 0xbd38aa3b, v38
	v_mul_f32_e32 v171, 0xbd38aa3b, v39
	v_exp_f32_e32 v164, v164
	v_exp_f32_e32 v165, v165
	v_exp_f32_e32 v166, v166
	v_exp_f32_e32 v167, v167
	v_exp_f32_e32 v168, v168
	v_exp_f32_e32 v169, v169
	v_exp_f32_e32 v170, v170
	v_exp_f32_e32 v171, v171
	v_add_f32_e32 v164, 1.0, v164
	v_add_f32_e32 v165, 1.0, v165
	v_add_f32_e32 v166, 1.0, v166
	v_add_f32_e32 v167, 1.0, v167
	v_add_f32_e32 v168, 1.0, v168
	v_add_f32_e32 v169, 1.0, v169
	v_add_f32_e32 v170, 1.0, v170
	v_add_f32_e32 v171, 1.0, v171
	v_rcp_f32_e32 v164, v164
	v_rcp_f32_e32 v165, v165
	v_rcp_f32_e32 v166, v166
	v_rcp_f32_e32 v167, v167
	v_rcp_f32_e32 v168, v168
	v_rcp_f32_e32 v169, v169
	v_rcp_f32_e32 v170, v170
	v_rcp_f32_e32 v171, v171
	v_mul_f32_e32 v164, v44, v164
	v_mul_f32_e32 v165, v45, v165
	v_mul_f32_e32 v166, v46, v166
	v_mul_f32_e32 v167, v47, v167
	v_mul_f32_e32 v168, v36, v168
	v_mul_f32_e32 v169, v37, v169
	v_mul_f32_e32 v170, v38, v170
	v_mul_f32_e32 v171, v39, v171
	v_mul_f32_e32 v164, v164, v40
	v_mul_f32_e32 v165, v165, v41
	v_mul_f32_e32 v166, v166, v42
	v_mul_f32_e32 v167, v167, v43
	v_mul_f32_e32 v168, v168, v32
	v_mul_f32_e32 v169, v169, v33
	v_mul_f32_e32 v170, v170, v34
	v_mul_f32_e32 v171, v171, v35
	v_mul_f32_e32 v164, v164, v163
	v_mul_f32_e32 v165, v165, v163
	v_mul_f32_e32 v166, v166, v163
	v_mul_f32_e32 v167, v167, v163
	v_mul_f32_e32 v168, v168, v163
	v_mul_f32_e32 v169, v169, v163
	v_mul_f32_e32 v170, v170, v163
	v_mul_f32_e32 v171, v171, v163
	v_max_f32_e32 v164, 0xc3e00000, v164
	v_max_f32_e32 v165, 0xc3e00000, v165
	v_max_f32_e32 v166, 0xc3e00000, v166
	v_max_f32_e32 v167, 0xc3e00000, v167
	v_max_f32_e32 v168, 0xc3e00000, v168
	v_max_f32_e32 v169, 0xc3e00000, v169
	v_max_f32_e32 v170, 0xc3e00000, v170
	v_max_f32_e32 v171, 0xc3e00000, v171
	v_min_f32_e32 v164, 0x43e00000, v164
	v_min_f32_e32 v165, 0x43e00000, v165
	v_min_f32_e32 v166, 0x43e00000, v166
	v_min_f32_e32 v167, 0x43e00000, v167
	v_min_f32_e32 v168, 0x43e00000, v168
	v_min_f32_e32 v169, 0x43e00000, v169
	v_min_f32_e32 v170, 0x43e00000, v170
	v_min_f32_e32 v171, 0x43e00000, v171
	v_cndmask_b32_e32 v164, 0, v164, vcc
	v_cndmask_b32_e32 v165, 0, v165, vcc
	v_cndmask_b32_e32 v166, 0, v166, vcc
	v_cndmask_b32_e32 v167, 0, v167, vcc
	v_cndmask_b32_e32 v168, 0, v168, vcc
	v_cndmask_b32_e32 v169, 0, v169, vcc
	v_cndmask_b32_e32 v170, 0, v170, vcc
	v_cndmask_b32_e32 v171, 0, v171, vcc
	v_mov_b32_e32 v190, 0
	v_mov_b32_e32 v191, 0
	v_cvt_pk_fp8_f32 v190, v164, v165
	v_cvt_pk_fp8_f32 v191, v168, v169
	v_add_u32_e32 v192, 0x9000, v150
	v_cvt_pk_fp8_f32 v190, v166, v167 op_sel:[0,0,1]
	v_cvt_pk_fp8_f32 v191, v170, v171 op_sel:[0,0,1]
	s_nop 1
	global_store_dwordx2 v192, v[190:191], s[12:13] sc1
	v_add_u32_e32 v162, 0xa0, v130
	v_cmp_lt_i32_e32 vcc, v162, v145
	s_waitcnt vmcnt(7)
	v_mul_f32_e32 v163, 0x3c800000, v160
	v_mul_f32_e32 v164, 0xbd38aa3b, v28
	v_mul_f32_e32 v165, 0xbd38aa3b, v29
	v_mul_f32_e32 v166, 0xbd38aa3b, v30
	v_mul_f32_e32 v167, 0xbd38aa3b, v31
	v_mul_f32_e32 v168, 0xbd38aa3b, v20
	v_mul_f32_e32 v169, 0xbd38aa3b, v21
	v_mul_f32_e32 v170, 0xbd38aa3b, v22
	v_mul_f32_e32 v171, 0xbd38aa3b, v23
	v_exp_f32_e32 v164, v164
	v_exp_f32_e32 v165, v165
	v_exp_f32_e32 v166, v166
	v_exp_f32_e32 v167, v167
	v_exp_f32_e32 v168, v168
	v_exp_f32_e32 v169, v169
	v_exp_f32_e32 v170, v170
	v_exp_f32_e32 v171, v171
	v_add_f32_e32 v164, 1.0, v164
	v_add_f32_e32 v165, 1.0, v165
	v_add_f32_e32 v166, 1.0, v166
	v_add_f32_e32 v167, 1.0, v167
	v_add_f32_e32 v168, 1.0, v168
	v_add_f32_e32 v169, 1.0, v169
	v_add_f32_e32 v170, 1.0, v170
	v_add_f32_e32 v171, 1.0, v171
	v_rcp_f32_e32 v164, v164
	v_rcp_f32_e32 v165, v165
	v_rcp_f32_e32 v166, v166
	v_rcp_f32_e32 v167, v167
	v_rcp_f32_e32 v168, v168
	v_rcp_f32_e32 v169, v169
	v_rcp_f32_e32 v170, v170
	v_rcp_f32_e32 v171, v171
	v_mul_f32_e32 v164, v28, v164
	v_mul_f32_e32 v165, v29, v165
	v_mul_f32_e32 v166, v30, v166
	v_mul_f32_e32 v167, v31, v167
	v_mul_f32_e32 v168, v20, v168
	v_mul_f32_e32 v169, v21, v169
	v_mul_f32_e32 v170, v22, v170
	v_mul_f32_e32 v171, v23, v171
	v_mul_f32_e32 v164, v164, v24
	v_mul_f32_e32 v165, v165, v25
	v_mul_f32_e32 v166, v166, v26
	v_mul_f32_e32 v167, v167, v27
	v_mul_f32_e32 v168, v168, v16
	v_mul_f32_e32 v169, v169, v17
	v_mul_f32_e32 v170, v170, v18
	v_mul_f32_e32 v171, v171, v19
	v_mul_f32_e32 v164, v164, v163
	v_mul_f32_e32 v165, v165, v163
	v_mul_f32_e32 v166, v166, v163
	v_mul_f32_e32 v167, v167, v163
	v_mul_f32_e32 v168, v168, v163
	v_mul_f32_e32 v169, v169, v163
	v_mul_f32_e32 v170, v170, v163
	v_mul_f32_e32 v171, v171, v163
	v_max_f32_e32 v164, 0xc3e00000, v164
	v_max_f32_e32 v165, 0xc3e00000, v165
	v_max_f32_e32 v166, 0xc3e00000, v166
	v_max_f32_e32 v167, 0xc3e00000, v167
	v_max_f32_e32 v168, 0xc3e00000, v168
	v_max_f32_e32 v169, 0xc3e00000, v169
	v_max_f32_e32 v170, 0xc3e00000, v170
	v_max_f32_e32 v171, 0xc3e00000, v171
	v_min_f32_e32 v164, 0x43e00000, v164
	v_min_f32_e32 v165, 0x43e00000, v165
	v_min_f32_e32 v166, 0x43e00000, v166
	v_min_f32_e32 v167, 0x43e00000, v167
	v_min_f32_e32 v168, 0x43e00000, v168
	v_min_f32_e32 v169, 0x43e00000, v169
	v_min_f32_e32 v170, 0x43e00000, v170
	v_min_f32_e32 v171, 0x43e00000, v171
	v_cndmask_b32_e32 v164, 0, v164, vcc
	v_cndmask_b32_e32 v165, 0, v165, vcc
	v_cndmask_b32_e32 v166, 0, v166, vcc
	v_cndmask_b32_e32 v167, 0, v167, vcc
	v_cndmask_b32_e32 v168, 0, v168, vcc
	v_cndmask_b32_e32 v169, 0, v169, vcc
	v_cndmask_b32_e32 v170, 0, v170, vcc
	v_cndmask_b32_e32 v171, 0, v171, vcc
	v_mov_b32_e32 v188, 0
	v_mov_b32_e32 v189, 0
	v_cvt_pk_fp8_f32 v188, v164, v165
	v_cvt_pk_fp8_f32 v189, v168, v169
	v_add_u32_e32 v192, 0xa000, v150
	v_cvt_pk_fp8_f32 v188, v166, v167 op_sel:[0,0,1]
	v_cvt_pk_fp8_f32 v189, v170, v171 op_sel:[0,0,1]
	s_nop 1
	global_store_dwordx2 v192, v[188:189], s[12:13] sc1
	v_add_u32_e32 v162, 0xb0, v130
	v_cmp_lt_i32_e32 vcc, v162, v145
	s_waitcnt vmcnt(7)
	v_mul_f32_e32 v163, 0x3c800000, v161
	v_mul_f32_e32 v164, 0xbd38aa3b, v12
	v_mul_f32_e32 v165, 0xbd38aa3b, v13
	v_mul_f32_e32 v166, 0xbd38aa3b, v14
	v_mul_f32_e32 v167, 0xbd38aa3b, v15
	v_mul_f32_e32 v168, 0xbd38aa3b, v4
	v_mul_f32_e32 v169, 0xbd38aa3b, v5
	v_mul_f32_e32 v170, 0xbd38aa3b, v6
	v_mul_f32_e32 v171, 0xbd38aa3b, v7
	v_exp_f32_e32 v164, v164
	v_exp_f32_e32 v165, v165
	v_exp_f32_e32 v166, v166
	v_exp_f32_e32 v167, v167
	v_exp_f32_e32 v168, v168
	v_exp_f32_e32 v169, v169
	v_exp_f32_e32 v170, v170
	v_exp_f32_e32 v171, v171
	v_add_f32_e32 v164, 1.0, v164
	v_add_f32_e32 v165, 1.0, v165
	v_add_f32_e32 v166, 1.0, v166
	v_add_f32_e32 v167, 1.0, v167
	v_add_f32_e32 v168, 1.0, v168
	v_add_f32_e32 v169, 1.0, v169
	v_add_f32_e32 v170, 1.0, v170
	v_add_f32_e32 v171, 1.0, v171
	v_rcp_f32_e32 v164, v164
	v_rcp_f32_e32 v165, v165
	v_rcp_f32_e32 v166, v166
	v_rcp_f32_e32 v167, v167
	v_rcp_f32_e32 v168, v168
	v_rcp_f32_e32 v169, v169
	v_rcp_f32_e32 v170, v170
	v_rcp_f32_e32 v171, v171
	v_mul_f32_e32 v164, v12, v164
	v_mul_f32_e32 v165, v13, v165
	v_mul_f32_e32 v166, v14, v166
	v_mul_f32_e32 v167, v15, v167
	v_mul_f32_e32 v168, v4, v168
	v_mul_f32_e32 v169, v5, v169
	v_mul_f32_e32 v170, v6, v170
	v_mul_f32_e32 v171, v7, v171
	v_mul_f32_e32 v164, v164, v8
	v_mul_f32_e32 v165, v165, v9
	v_mul_f32_e32 v166, v166, v10
	v_mul_f32_e32 v167, v167, v11
	v_mul_f32_e32 v168, v168, v0
	v_mul_f32_e32 v169, v169, v1
	v_mul_f32_e32 v170, v170, v2
	v_mul_f32_e32 v171, v171, v3
	v_mul_f32_e32 v164, v164, v163
	v_mul_f32_e32 v165, v165, v163
	v_mul_f32_e32 v166, v166, v163
	v_mul_f32_e32 v167, v167, v163
	v_mul_f32_e32 v168, v168, v163
	v_mul_f32_e32 v169, v169, v163
	v_mul_f32_e32 v170, v170, v163
	v_mul_f32_e32 v171, v171, v163
	v_max_f32_e32 v164, 0xc3e00000, v164
	v_max_f32_e32 v165, 0xc3e00000, v165
	v_max_f32_e32 v166, 0xc3e00000, v166
	v_max_f32_e32 v167, 0xc3e00000, v167
	v_max_f32_e32 v168, 0xc3e00000, v168
	v_max_f32_e32 v169, 0xc3e00000, v169
	v_max_f32_e32 v170, 0xc3e00000, v170
	v_max_f32_e32 v171, 0xc3e00000, v171
	v_min_f32_e32 v164, 0x43e00000, v164
	v_min_f32_e32 v165, 0x43e00000, v165
	v_min_f32_e32 v166, 0x43e00000, v166
	v_min_f32_e32 v167, 0x43e00000, v167
	v_min_f32_e32 v168, 0x43e00000, v168
	v_min_f32_e32 v169, 0x43e00000, v169
	v_min_f32_e32 v170, 0x43e00000, v170
	v_min_f32_e32 v171, 0x43e00000, v171
	v_cndmask_b32_e32 v164, 0, v164, vcc
	v_cndmask_b32_e32 v165, 0, v165, vcc
	v_cndmask_b32_e32 v166, 0, v166, vcc
	v_cndmask_b32_e32 v167, 0, v167, vcc
	v_cndmask_b32_e32 v168, 0, v168, vcc
	v_cndmask_b32_e32 v169, 0, v169, vcc
	v_cndmask_b32_e32 v170, 0, v170, vcc
	v_cndmask_b32_e32 v171, 0, v171, vcc
	v_mov_b32_e32 v190, 0
	v_mov_b32_e32 v191, 0
	v_cvt_pk_fp8_f32 v190, v164, v165
	v_cvt_pk_fp8_f32 v191, v168, v169
	v_add_u32_e32 v192, 0xb000, v150
	v_cvt_pk_fp8_f32 v190, v166, v167 op_sel:[0,0,1]
	v_cvt_pk_fp8_f32 v191, v170, v171 op_sel:[0,0,1]
	s_nop 1
	global_store_dwordx2 v192, v[190:191], s[12:13] sc1
	v_bfe_u32 v114, v146, 4, 2
	s_waitcnt vmcnt(0)
	v_or_b32_e32 v0, v114, v143
	v_cmp_eq_u32_e32 vcc, 0, v0
	s_and_saveexec_b64 s[22:23], vcc
	s_cbranch_execz .LBB0_2596
	s_mov_b64 s[24:25], exec
	v_mbcnt_lo_u32_b32 v0, s24, 0
	v_mbcnt_hi_u32_b32 v0, s25, v0
	v_cmp_eq_u32_e32 vcc, 0, v0
	s_and_b64 s[26:27], exec, vcc
	s_mov_b64 exec, s[26:27]
	s_cbranch_execz .LBB0_2596
	s_lshl_b32 s26, s31, 5
	s_ashr_i32 s27, s26, 31
	s_lshl_b64 s[26:27], s[26:27], 2
	s_add_u32 s26, s48, s26
	s_addc_u32 s27, s49, s27
	s_bcnt1_i32_b64 s14, s[24:25]
	s_lshl_b32 s14, s14, 1
	v_mov_b32_e32 v0, s14
	global_atomic_add v140, v0, s[26:27]

.LBB0_2608:
	ds_read_b128 v[72:75], v67
	ds_read_b128 v[76:79], v67 offset:1024
	ds_read_b128 v[80:83], v67 offset:2048
	ds_read_b128 v[84:87], v67 offset:3072
	ds_read_b128 v[88:91], v68
	ds_read_b128 v[92:95], v68 offset:1024
	ds_read_b128 v[96:99], v68 offset:2048
	ds_read_b128 v[100:103], v68 offset:3072
	s_cmp_eq_u32 s36, 4
	s_cselect_b32 s16, s8, s34
	s_cselect_b32 s17, s9, s35
	s_cselect_b32 s14, s0, s30
	s_cselect_b32 s15, s1, s31
	s_add_u32 s4, s16, 0x80
	s_addc_u32 s5, s17, 0
	ds_read_b128 v[104:107], v69
	ds_read_b128 v[108:111], v69 offset:1024
	ds_read_b128 v[112:115], v69 offset:2048
	ds_read_b128 v[116:119], v69 offset:3072
	ds_read_b128 v[120:123], v69 offset:4096
	ds_read_b128 v[124:127], v69 offset:5120
	ds_read_b128 v[128:131], v69 offset:6144
	ds_read_b128 v[132:135], v69 offset:7168
	s_waitcnt vmcnt(6)
	s_waitcnt lgkmcnt(0)
	s_barrier
	s_setprio 3
	v_mfma_f32_16x16x128_f8f6f4 v[60:63], v[72:79], v[104:111], v[60:63]
	v_mfma_f32_16x16x128_f8f6f4 v[52:55], v[80:87], v[104:111], v[52:55]
	v_mfma_f32_16x16x128_f8f6f4 v[44:47], v[72:79], v[112:119], v[44:47]
	v_mfma_f32_16x16x128_f8f6f4 v[36:39], v[80:87], v[112:119], v[36:39]
	v_mfma_f32_16x16x128_f8f6f4 v[28:31], v[72:79], v[120:127], v[28:31]
	v_mfma_f32_16x16x128_f8f6f4 v[20:23], v[80:87], v[120:127], v[20:23]
	v_mfma_f32_16x16x128_f8f6f4 v[12:15], v[72:79], v[128:135], v[12:15]
	v_mfma_f32_16x16x128_f8f6f4 v[136:139], v[80:87], v[128:135], v[4:7]
	v_mfma_f32_16x16x128_f8f6f4 v[56:59], v[88:95], v[104:111], v[56:59]
	v_mfma_f32_16x16x128_f8f6f4 v[48:51], v[96:103], v[104:111], v[48:51]
	v_mfma_f32_16x16x128_f8f6f4 v[40:43], v[88:95], v[112:119], v[40:43]
	v_mfma_f32_16x16x128_f8f6f4 v[32:35], v[96:103], v[112:119], v[32:35]
	v_mfma_f32_16x16x128_f8f6f4 v[24:27], v[88:95], v[120:127], v[24:27]
	v_mfma_f32_16x16x128_f8f6f4 v[16:19], v[96:103], v[120:127], v[16:19]
	v_mfma_f32_16x16x128_f8f6f4 v[8:11], v[88:95], v[128:135], v[8:11]
	v_mfma_f32_16x16x128_f8f6f4 v[128:131], v[96:103], v[128:135], v[0:3]
	s_setprio 0
	s_barrier
	s_nop 4
	v_mov_b32_e32 v0, v64
	s_mov_b64 s[50:51], s[14:15]
	s_mov_b32 m0, s37
	s_nop 0
	global_load_lds_dwordx4 v0, s[50:51]
	s_add_u32 s50, s14, 0x10000
	v_mov_b32_e32 v0, v64
	s_addc_u32 s51, s15, 0
	s_mov_b32 m0, s38
	s_nop 0
	global_load_lds_dwordx4 v0, s[50:51]
	s_add_u32 s50, s14, 0x20000
	v_mov_b32_e32 v0, v64
	s_addc_u32 s51, s15, 0
	s_mov_b32 m0, s39
	s_nop 0
	global_load_lds_dwordx4 v0, s[50:51]
	v_mov_b32_e32 v0, v64
	s_add_u32 s50, s14, 0x30000
	s_addc_u32 s51, s15, 0
	s_mov_b32 m0, s40
	s_nop 0
	global_load_lds_dwordx4 v0, s[50:51]
	v_mov_b32_e32 v0, v65
	s_mov_b64 s[50:51], s[16:17]
	s_mov_b32 m0, s23
	s_nop 0
	global_load_lds_dwordx4 v0, s[50:51]
	v_mov_b32_e32 v0, v66
	s_mov_b32 m0, s25
	s_nop 0
	global_load_lds_dwordx4 v0, s[16:17]
	s_waitcnt vmcnt(6)
	s_waitcnt lgkmcnt(0)
	s_barrier
	s_barrier
	ds_read_b128 v[0:3], v70
	ds_read_b128 v[4:7], v70 offset:1024
	ds_read_b128 v[72:75], v70 offset:2048
	ds_read_b128 v[76:79], v70 offset:3072
	ds_read_b128 v[80:83], v71
	ds_read_b128 v[84:87], v71 offset:1024
	ds_read_b128 v[88:91], v71 offset:2048
	ds_read_b128 v[92:95], v71 offset:3072
	ds_read_b128 v[96:99], v69 offset:32768
	ds_read_b128 v[100:103], v69 offset:33792
	ds_read_b128 v[104:107], v69 offset:34816
	ds_read_b128 v[108:111], v69 offset:35840
	ds_read_b128 v[112:115], v69 offset:36864
	ds_read_b128 v[116:119], v69 offset:37888
	ds_read_b128 v[120:123], v69 offset:38912
	ds_read_b128 v[124:127], v69 offset:39936
	s_waitcnt vmcnt(6)
	s_waitcnt lgkmcnt(0)
	s_barrier
	s_setprio 3
	v_mfma_f32_16x16x128_f8f6f4 v[60:63], v[0:7], v[96:103], v[60:63]
	v_mfma_f32_16x16x128_f8f6f4 v[52:55], v[72:79], v[96:103], v[52:55]
	v_mfma_f32_16x16x128_f8f6f4 v[44:47], v[0:7], v[104:111], v[44:47]
	v_mfma_f32_16x16x128_f8f6f4 v[36:39], v[72:79], v[104:111], v[36:39]
	v_mfma_f32_16x16x128_f8f6f4 v[28:31], v[0:7], v[112:119], v[28:31]
	v_mfma_f32_16x16x128_f8f6f4 v[20:23], v[72:79], v[112:119], v[20:23]
	v_mfma_f32_16x16x128_f8f6f4 v[12:15], v[0:7], v[120:127], v[12:15]
	v_mfma_f32_16x16x128_f8f6f4 v[4:7], v[72:79], v[120:127], v[136:139]
	v_mfma_f32_16x16x128_f8f6f4 v[56:59], v[80:87], v[96:103], v[56:59]
	s_add_u32 s16, s14, 0x80
	s_addc_u32 s17, s15, 0
	v_mfma_f32_16x16x128_f8f6f4 v[48:51], v[88:95], v[96:103], v[48:51]
	v_mfma_f32_16x16x128_f8f6f4 v[40:43], v[80:87], v[104:111], v[40:43]
	v_mfma_f32_16x16x128_f8f6f4 v[32:35], v[88:95], v[104:111], v[32:35]
	v_mfma_f32_16x16x128_f8f6f4 v[24:27], v[80:87], v[112:119], v[24:27]
	v_mfma_f32_16x16x128_f8f6f4 v[16:19], v[88:95], v[112:119], v[16:19]
	v_mfma_f32_16x16x128_f8f6f4 v[8:11], v[80:87], v[120:127], v[8:11]
	v_mfma_f32_16x16x128_f8f6f4 v[0:3], v[88:95], v[120:127], v[128:131]
	s_setprio 0
	s_barrier
	v_mov_b32_e32 v72, v64
	s_mov_b32 m0, s41
	s_nop 0
	global_load_lds_dwordx4 v72, s[16:17]
	s_add_u32 s16, s14, 0x10080
	v_mov_b32_e32 v72, v64
	s_addc_u32 s17, s15, 0
	s_mov_b32 m0, s42
	s_nop 0
	global_load_lds_dwordx4 v72, s[16:17]
	v_mov_b32_e32 v72, v64
	s_add_u32 s16, s14, 0x20080
	s_addc_u32 s17, s15, 0
	s_mov_b32 m0, s43
	s_add_u32 s14, s14, 0x30080
	global_load_lds_dwordx4 v72, s[16:17]
	v_mov_b32_e32 v72, v64
	s_addc_u32 s15, s15, 0
	s_mov_b32 m0, s44
	s_nop 0
	global_load_lds_dwordx4 v72, s[14:15]
	v_mov_b32_e32 v72, v65
	s_mov_b64 s[14:15], s[4:5]
	s_mov_b32 m0, s26
	s_nop 0
	global_load_lds_dwordx4 v72, s[14:15]
	v_mov_b32_e32 v72, v66
	s_mov_b32 m0, s27
	s_nop 0
	global_load_lds_dwordx4 v72, s[4:5]
	s_waitcnt vmcnt(6)
	s_waitcnt lgkmcnt(0)
	s_barrier
	s_barrier
	s_add_i32 s36, s36, 2
	s_add_u32 s30, s30, 0x100
	s_addc_u32 s31, s31, 0
	s_add_u32 s34, s34, 0x100
	s_addc_u32 s35, s35, 0
	s_cmp_gt_u32 s36, 5
	s_cbranch_scc0 .LBB0_2608
	s_cmpk_lt_u32 s22, 0x100
	s_cbranch_scc0 .LBB0_2611
	s_barrier

.LBB0_2724:
	ds_read_b128 v[56:59], v197
	ds_read_b128 v[60:63], v197 offset:1024
	ds_read_b128 v[80:83], v197 offset:2048
	ds_read_b128 v[84:87], v197 offset:3072
	ds_read_b128 v[0:3], v198
	ds_read_b128 v[4:7], v198 offset:1024
	ds_read_b128 v[8:11], v198 offset:2048
	ds_read_b128 v[12:15], v198 offset:3072
	s_add_u32 s42, s34, 0x80
	s_addc_u32 s43, s35, 0
	s_add_u32 s44, s14, 0x80
	s_addc_u32 s45, s15, 0
	s_add_u32 s64, s40, 0x8080
	v_mov_b32_e32 v16, v195
	s_addc_u32 s65, s41, 0
	s_add_i32 m0, s50, 0xc000
	ds_read_b128 v[64:67], v199
	ds_read_b128 v[68:71], v199 offset:1024
	ds_read_b128 v[72:75], v199 offset:2048
	ds_read_b128 v[76:79], v199 offset:3072
	ds_read_b128 v[88:91], v199 offset:4096
	ds_read_b128 v[92:95], v199 offset:5120
	ds_read_b128 v[96:99], v199 offset:6144
	ds_read_b128 v[100:103], v199 offset:7168
	s_add_u32 s40, s40, 0xc080
	s_addc_u32 s41, s41, 0
	global_load_lds_dwordx4 v16, s[64:65] sc1
	v_mov_b32_e32 v16, v195
	s_add_i32 m0, s50, 0xe000
	s_nop 0
	global_load_lds_dwordx4 v16, s[40:41] sc1
	s_waitcnt vmcnt(8)
	s_waitcnt lgkmcnt(0)
	s_barrier
	s_setprio 3
	v_mfma_f32_16x16x128_f8f6f4 v[16:19], v[56:63], v[64:71], 0
	v_mfma_f32_16x16x128_f8f6f4 v[20:23], v[80:87], v[64:71], 0
	v_mfma_f32_16x16x128_f8f6f4 v[24:27], v[56:63], v[72:79], 0
	v_mfma_f32_16x16x128_f8f6f4 v[28:31], v[80:87], v[72:79], 0
	v_mfma_f32_16x16x128_f8f6f4 v[32:35], v[56:63], v[88:95], 0
	v_mfma_f32_16x16x128_f8f6f4 v[36:39], v[80:87], v[88:95], 0
	v_mfma_f32_16x16x128_f8f6f4 v[40:43], v[56:63], v[96:103], 0
	v_mfma_f32_16x16x128_f8f6f4 v[44:47], v[80:87], v[96:103], 0
	v_mfma_f32_16x16x128_f8f6f4 v[48:51], v[0:7], v[64:71], 0
	v_mfma_f32_16x16x128_f8f6f4 v[52:55], v[8:15], v[64:71], 0
	v_mfma_f32_16x16x128_f8f6f4 v[64:67], v[0:7], v[72:79], 0
	v_mfma_f32_16x16x128_f8f6f4 v[68:71], v[8:15], v[72:79], 0
	v_mfma_f32_16x16x128_f8f6f4 v[72:75], v[0:7], v[88:95], 0
	v_mfma_f32_16x16x128_f8f6f4 v[76:79], v[8:15], v[88:95], 0
	v_mfma_f32_16x16x128_f8f6f4 v[128:131], v[0:7], v[96:103], 0
	v_mfma_f32_16x16x128_f8f6f4 v[132:135], v[8:15], v[96:103], 0
	s_setprio 0
	s_barrier
	v_mov_b32_e32 v120, v194
	s_mov_b64 s[40:41], s[14:15]
	s_add_i32 s19, s61, s27
	ds_read_b128 v[88:91], v199 offset:16384
	ds_read_b128 v[92:95], v199 offset:17408
	ds_read_b128 v[96:99], v199 offset:18432
	ds_read_b128 v[100:103], v199 offset:19456
	ds_read_b128 v[104:107], v199 offset:20480
	ds_read_b128 v[108:111], v199 offset:21504
	ds_read_b128 v[112:115], v199 offset:22528
	ds_read_b128 v[116:119], v199 offset:23552
	s_mov_b32 m0, s19
	s_nop 0
	global_load_lds_dwordx4 v120, s[40:41]
	s_add_u32 s40, s14, 0x4000
	v_mov_b32_e32 v120, v194
	s_addc_u32 s41, s15, 0
	s_add_i32 m0, s19, 0x2000
	s_nop 0
	global_load_lds_dwordx4 v120, s[40:41]
	s_add_u32 s40, s14, 0x8000
	v_mov_b32_e32 v120, v194
	s_addc_u32 s41, s15, 0
	s_add_i32 s19, s62, s27
	s_mov_b32 m0, s19
	s_nop 0
	global_load_lds_dwordx4 v120, s[40:41]
	s_add_u32 s40, s14, 0xc000
	v_mov_b32_e32 v120, v194
	s_addc_u32 s41, s15, 0
	s_add_i32 m0, s19, 0x2000
	s_nop 0
	global_load_lds_dwordx4 v120, s[40:41]
	v_mov_b32_e32 v120, v195
	s_mov_b64 s[40:41], s[34:35]
	s_mov_b32 m0, s50
	s_nop 0
	global_load_lds_dwordx4 v120, s[40:41] sc1
	s_add_u32 s40, s34, 0x4000
	v_mov_b32_e32 v120, v195
	s_addc_u32 s41, s35, 0
	s_mov_b32 m0, s51
	s_nop 0
	global_load_lds_dwordx4 v120, s[40:41] sc1
	s_waitcnt vmcnt(8)
	s_waitcnt lgkmcnt(0)
	s_barrier
	s_setprio 3
	v_mfma_f32_16x16x128_f8f6f4 v[136:139], v[56:63], v[88:95], 0
	v_mfma_f32_16x16x128_f8f6f4 v[140:143], v[80:87], v[88:95], 0
	v_mfma_f32_16x16x128_f8f6f4 v[144:147], v[56:63], v[96:103], 0
	v_mfma_f32_16x16x128_f8f6f4 v[148:151], v[80:87], v[96:103], 0
	v_mfma_f32_16x16x128_f8f6f4 v[152:155], v[56:63], v[104:111], 0
	v_mfma_f32_16x16x128_f8f6f4 v[156:159], v[80:87], v[104:111], 0
	v_mfma_f32_16x16x128_f8f6f4 v[160:163], v[56:63], v[112:119], 0
	v_mfma_f32_16x16x128_f8f6f4 v[164:167], v[80:87], v[112:119], 0
	v_mfma_f32_16x16x128_f8f6f4 v[168:171], v[0:7], v[88:95], 0
	v_mfma_f32_16x16x128_f8f6f4 v[176:179], v[0:7], v[96:103], 0
	v_mfma_f32_16x16x128_f8f6f4 v[184:187], v[0:7], v[104:111], 0
	v_mfma_f32_16x16x128_f8f6f4 v[0:3], v[0:7], v[112:119], 0
	v_mfma_f32_16x16x128_f8f6f4 v[4:7], v[8:15], v[112:119], 0
	v_mfma_f32_16x16x128_f8f6f4 v[172:175], v[8:15], v[88:95], 0
	v_mfma_f32_16x16x128_f8f6f4 v[180:183], v[8:15], v[96:103], 0
	v_mfma_f32_16x16x128_f8f6f4 v[188:191], v[8:15], v[104:111], 0
	s_setprio 0
	s_barrier
	s_add_i32 s19, 0, 0x18000
	v_add_u32_e32 v56, s19, v196
	s_add_i32 s29, 0, 0x1c000
	ds_read_b128 v[8:11], v56
	ds_read_b128 v[12:15], v56 offset:1024
	ds_read_b128 v[200:203], v56 offset:2048
	ds_read_b128 v[204:207], v56 offset:3072
	v_add_u32_e32 v56, s29, v196
	ds_read_b128 v[208:211], v56
	ds_read_b128 v[212:215], v56 offset:1024
	ds_read_b128 v[216:219], v56 offset:2048
	ds_read_b128 v[220:223], v56 offset:3072
	s_add_u32 s40, s34, 0x8000
	v_mov_b32_e32 v56, v195
	s_addc_u32 s41, s35, 0
	s_mov_b32 m0, s52
	ds_read_b128 v[88:91], v199 offset:32768
	ds_read_b128 v[92:95], v199 offset:33792
	ds_read_b128 v[224:227], v199 offset:34816
	ds_read_b128 v[228:231], v199 offset:35840
	ds_read_b128 v[232:235], v199 offset:36864
	ds_read_b128 v[236:239], v199 offset:37888
	ds_read_b128 v[240:243], v199 offset:38912
	ds_read_b128 v[244:247], v199 offset:39936
	s_nop 0
	global_load_lds_dwordx4 v56, s[40:41] sc1
	s_add_u32 s40, s34, 0xc000
	v_mov_b32_e32 v56, v195
	s_addc_u32 s41, s35, 0
	s_mov_b32 m0, s53
	s_nop 0
	global_load_lds_dwordx4 v56, s[40:41] sc1
	s_waitcnt vmcnt(8)
	s_waitcnt lgkmcnt(0)
	s_barrier
	s_setprio 3
	v_mfma_f32_16x16x128_f8f6f4 v[112:115], v[8:15], v[88:95], v[16:19]
	v_mfma_f32_16x16x128_f8f6f4 v[116:119], v[200:207], v[88:95], v[20:23]
	v_mfma_f32_16x16x128_f8f6f4 v[96:99], v[8:15], v[224:231], v[24:27]
	v_mfma_f32_16x16x128_f8f6f4 v[100:103], v[200:207], v[224:231], v[28:31]
	v_mfma_f32_16x16x128_f8f6f4 v[80:83], v[8:15], v[232:239], v[32:35]
	v_mfma_f32_16x16x128_f8f6f4 v[84:87], v[200:207], v[232:239], v[36:39]
	v_mfma_f32_16x16x128_f8f6f4 v[56:59], v[8:15], v[240:247], v[40:43]
	v_mfma_f32_16x16x128_f8f6f4 v[60:63], v[200:207], v[240:247], v[44:47]
	v_mfma_f32_16x16x128_f8f6f4 v[120:123], v[208:215], v[88:95], v[48:51]
	v_mfma_f32_16x16x128_f8f6f4 v[124:127], v[216:223], v[88:95], v[52:55]
	v_mfma_f32_16x16x128_f8f6f4 v[104:107], v[208:215], v[224:231], v[64:67]
	v_mfma_f32_16x16x128_f8f6f4 v[108:111], v[216:223], v[224:231], v[68:71]
	v_mfma_f32_16x16x128_f8f6f4 v[88:91], v[208:215], v[232:239], v[72:75]
	v_mfma_f32_16x16x128_f8f6f4 v[92:95], v[216:223], v[232:239], v[76:79]
	v_mfma_f32_16x16x128_f8f6f4 v[64:67], v[208:215], v[240:247], v[128:131]
	v_mfma_f32_16x16x128_f8f6f4 v[68:71], v[216:223], v[240:247], v[132:135]
	s_setprio 0
	s_barrier
	v_mov_b32_e32 v24, v194
	s_add_i32 s19, s19, s27
	ds_read_b128 v[16:19], v199 offset:49152
	ds_read_b128 v[20:23], v199 offset:50176
	ds_read_b128 v[128:131], v199 offset:51200
	ds_read_b128 v[132:135], v199 offset:52224
	ds_read_b128 v[224:227], v199 offset:53248
	ds_read_b128 v[228:231], v199 offset:54272
	ds_read_b128 v[232:235], v199 offset:55296
	ds_read_b128 v[236:239], v199 offset:56320
	s_mov_b32 m0, s19
	s_add_u32 s40, s14, 0x4080
	s_addc_u32 s41, s15, 0
	global_load_lds_dwordx4 v24, s[44:45]
	v_mov_b32_e32 v24, v194
	s_add_i32 m0, s19, 0x2000
	s_nop 0
	global_load_lds_dwordx4 v24, s[40:41]
	s_add_u32 s40, s14, 0x8080
	v_mov_b32_e32 v24, v194
	s_addc_u32 s41, s15, 0
	s_add_i32 s19, s29, s27
	s_mov_b32 m0, s19
	s_nop 0
	global_load_lds_dwordx4 v24, s[40:41]
	v_mov_b32_e32 v24, v194
	s_add_u32 s40, s14, 0xc080
	s_addc_u32 s41, s15, 0
	s_add_i32 m0, s19, 0x2000
	s_nop 0
	global_load_lds_dwordx4 v24, s[40:41]
	v_mov_b32_e32 v24, v195
	s_mov_b32 m0, s56
	s_add_u32 s40, s34, 0x4080
	s_addc_u32 s41, s35, 0
	global_load_lds_dwordx4 v24, s[42:43] sc1
	v_mov_b32_e32 v24, v195
	s_mov_b32 m0, s57
	s_nop 0
	global_load_lds_dwordx4 v24, s[40:41] sc1
	s_waitcnt vmcnt(8)
	s_waitcnt lgkmcnt(0)
	s_barrier
	s_setprio 3
	v_mfma_f32_16x16x128_f8f6f4 v[48:51], v[8:15], v[16:23], v[136:139]
	v_mfma_f32_16x16x128_f8f6f4 v[52:55], v[200:207], v[16:23], v[140:143]
	v_mfma_f32_16x16x128_f8f6f4 v[32:35], v[8:15], v[128:135], v[144:147]
	v_mfma_f32_16x16x128_f8f6f4 v[36:39], v[200:207], v[128:135], v[148:151]
	v_mfma_f32_16x16x128_f8f6f4 v[24:27], v[8:15], v[224:231], v[152:155]
	v_mfma_f32_16x16x128_f8f6f4 v[28:31], v[200:207], v[224:231], v[156:159]
	v_mfma_f32_16x16x128_f8f6f4 v[8:11], v[8:15], v[232:239], v[160:163]
	v_mfma_f32_16x16x128_f8f6f4 v[12:15], v[200:207], v[232:239], v[164:167]
	v_mfma_f32_16x16x128_f8f6f4 v[72:75], v[208:215], v[16:23], v[168:171]
	v_mfma_f32_16x16x128_f8f6f4 v[76:79], v[216:223], v[16:23], v[172:175]
	v_mfma_f32_16x16x128_f8f6f4 v[40:43], v[208:215], v[128:135], v[176:179]
	v_mfma_f32_16x16x128_f8f6f4 v[44:47], v[216:223], v[128:135], v[180:183]
	v_mfma_f32_16x16x128_f8f6f4 v[16:19], v[208:215], v[224:231], v[184:187]
	v_mfma_f32_16x16x128_f8f6f4 v[20:23], v[216:223], v[224:231], v[188:191]
	v_mfma_f32_16x16x128_f8f6f4 v[0:3], v[208:215], v[232:239], v[0:3]
	v_mfma_f32_16x16x128_f8f6f4 v[4:7], v[216:223], v[232:239], v[4:7]
	s_setprio 0
	s_barrier
	s_andn2_b64 vcc, exec, s[22:23]
	s_cbranch_vccnz .LBB0_2726
	s_barrier

.LBB0_2734:
	s_or_b64 exec, exec, s[38:39]
	v_mov_b32_e32 v240, -1
	v_mov_b32_e32 v241, -1
	v_mov_b32_e32 v242, -1
	v_mov_b32_e32 v243, -1
	v_add_u32_e32 v244, 0x80, v139
	v_cmp_lt_i32_e32 vcc, v244, v138
	s_and_saveexec_b64 s[38:39], vcc
	global_load_dword v240, v[130:131], off offset:512
	s_or_b64 exec, exec, s[38:39]
	v_add_u32_e32 v244, 0x90, v139
	v_cmp_lt_i32_e32 vcc, v244, v138
	s_and_saveexec_b64 s[38:39], vcc
	global_load_dword v241, v[130:131], off offset:576
	s_or_b64 exec, exec, s[38:39]
	v_add_u32_e32 v244, 0xa0, v139
	v_cmp_lt_i32_e32 vcc, v244, v138
	s_and_saveexec_b64 s[38:39], vcc
	global_load_dword v242, v[130:131], off offset:640
	s_or_b64 exec, exec, s[38:39]
	v_add_u32_e32 v244, 0xb0, v139
	v_cmp_lt_i32_e32 vcc, v244, v138
	s_and_saveexec_b64 s[38:39], vcc
	global_load_dword v243, v[130:131], off offset:704
	s_or_b64 exec, exec, s[38:39]
	s_lshl_b32 s19, s36, 8
	v_lshrrev_b32_e32 v128, 1, v128
	v_and_or_b32 v128, v128, 24, s19
	v_or_b32_e32 v128, s55, v128
	v_ashrrev_i32_e32 v129, 31, v128
	s_waitcnt vmcnt(0)
	v_cmp_lt_i32_e32 vcc, -1, v192
	s_and_saveexec_b64 s[36:37], vcc
	s_cbranch_execz .LBB0_2736
	v_pk_mul_f32 v[112:113], v[112:113], s[26:27] op_sel_hi:[1,0]
	v_pk_mul_f32 v[116:117], v[116:117], s[26:27] op_sel_hi:[1,0]
	v_mov_b32_e32 v142, v193
	v_mov_b32_e32 v143, v193
	v_cvt_pk_fp8_f32 v142, v112, v113
	v_cvt_pk_fp8_f32 v143, v116, v117
	v_pk_mul_f32 v[112:113], v[114:115], s[26:27] op_sel_hi:[1,0]
	v_pk_mul_f32 v[114:115], v[118:119], s[26:27] op_sel_hi:[1,0]
	v_cvt_pk_fp8_f32 v142, v112, v113 op_sel:[0,0,1]
	v_cvt_pk_fp8_f32 v143, v114, v115 op_sel:[0,0,1]
	v_pk_mul_f32 v[112:113], v[120:121], s[26:27] op_sel_hi:[1,0]
	v_pk_mul_f32 v[114:115], v[124:125], s[26:27] op_sel_hi:[1,0]
	v_mov_b32_e32 v116, v193
	v_mov_b32_e32 v117, v193
	v_cvt_pk_fp8_f32 v116, v112, v113
	v_cvt_pk_fp8_f32 v117, v114, v115
	v_pk_mul_f32 v[112:113], v[122:123], s[26:27] op_sel_hi:[1,0]
	v_pk_mul_f32 v[114:115], v[126:127], s[26:27] op_sel_hi:[1,0]
	v_lshlrev_b64 v[140:141], 10, v[192:193]
	v_cvt_pk_fp8_f32 v116, v112, v113 op_sel:[0,0,1]
	v_cvt_pk_fp8_f32 v117, v114, v115 op_sel:[0,0,1]
	v_lshl_add_u64 v[112:113], s[20:21], 0, v[140:141]
	v_lshl_add_u64 v[112:113], v[112:113], 0, v[128:129]
	global_store_dwordx2 v[112:113], v[142:143], off
	global_store_dwordx2 v[112:113], v[116:117], off offset:128

.LBB0_2742:
	s_or_b64 exec, exec, s[36:37]
	v_mov_b32_e32 v192, v240
	v_mov_b32_e32 v60, v241
	v_mov_b32_e32 v58, v242
	v_mov_b32_e32 v56, v243
	v_cmp_lt_i32_e32 vcc, -1, v192
	s_and_saveexec_b64 s[36:37], vcc
	s_cbranch_execz .LBB0_2752
	v_pk_mul_f32 v[48:49], v[48:49], s[26:27] op_sel_hi:[1,0]
	v_pk_mul_f32 v[52:53], v[52:53], s[26:27] op_sel_hi:[1,0]
	v_mov_b32_e32 v64, v193
	v_mov_b32_e32 v65, v193
	v_cvt_pk_fp8_f32 v64, v48, v49
	v_cvt_pk_fp8_f32 v65, v52, v53
	v_pk_mul_f32 v[48:49], v[50:51], s[26:27] op_sel_hi:[1,0]
	v_pk_mul_f32 v[50:51], v[54:55], s[26:27] op_sel_hi:[1,0]
	v_cvt_pk_fp8_f32 v64, v48, v49 op_sel:[0,0,1]
	v_cvt_pk_fp8_f32 v65, v50, v51 op_sel:[0,0,1]
	v_pk_mul_f32 v[48:49], v[72:73], s[26:27] op_sel_hi:[1,0]
	v_pk_mul_f32 v[50:51], v[76:77], s[26:27] op_sel_hi:[1,0]
	v_mov_b32_e32 v52, v193
	v_mov_b32_e32 v53, v193
	v_cvt_pk_fp8_f32 v52, v48, v49
	v_cvt_pk_fp8_f32 v53, v50, v51
	v_pk_mul_f32 v[48:49], v[74:75], s[26:27] op_sel_hi:[1,0]
	v_pk_mul_f32 v[50:51], v[78:79], s[26:27] op_sel_hi:[1,0]
	v_lshlrev_b64 v[62:63], 10, v[192:193]
	v_cvt_pk_fp8_f32 v52, v48, v49 op_sel:[0,0,1]
	v_cvt_pk_fp8_f32 v53, v50, v51 op_sel:[0,0,1]
	v_lshl_add_u64 v[48:49], s[20:21], 0, v[62:63]
	v_lshl_add_u64 v[48:49], v[48:49], 0, v[128:129]
	global_store_dwordx2 v[48:49], v[64:65], off
	global_store_dwordx2 v[48:49], v[52:53], off offset:128
